# non-temporal stores also for the scan output, compressed-attention output, gated-norm output and the final output
# baseline (speedup 1.0000x reference)
.LBB0_548:
	s_ashr_i32 s15, s14, 31
	s_and_b32 s0, s63, 0x10000
	s_lshl_b64 s[16:17], s[14:15], 2
	s_add_u32 s16, s24, s16
	s_addc_u32 s17, s25, s17
	s_add_i32 s0, s0, 0
	s_waitcnt lgkmcnt(0)
	s_barrier
	s_waitcnt vmcnt(2)
	v_lshlrev_b32_e32 v82, 16, v74
	v_lshl_add_u32 v172, v177, 4, s0
	ds_read_b128 v[102:105], v172
	ds_read_b128 v[130:133], v172 offset:1024
	v_and_b32_e32 v83, 0xffff0000, v74
	v_lshlrev_b32_e32 v84, 16, v75
	v_and_b32_e32 v85, 0xffff0000, v75
	v_lshlrev_b32_e32 v86, 16, v76
	v_and_b32_e32 v87, 0xffff0000, v76
	v_lshlrev_b32_e32 v88, 16, v77
	v_and_b32_e32 v89, 0xffff0000, v77
	v_lshlrev_b32_e32 v90, 16, v66
	v_and_b32_e32 v91, 0xffff0000, v66
	v_lshlrev_b32_e32 v92, 16, v67
	v_and_b32_e32 v93, 0xffff0000, v67
	v_lshlrev_b32_e32 v94, 16, v68
	v_and_b32_e32 v95, 0xffff0000, v68
	v_lshlrev_b32_e32 v96, 16, v69
	v_and_b32_e32 v97, 0xffff0000, v69
	v_cvt_pk_bf16_f32 v98, v34, v35
	v_cvt_pk_bf16_f32 v99, v36, v37
	v_cvt_pk_bf16_f32 v100, v38, v39
	v_cvt_pk_bf16_f32 v101, v40, v41
	s_waitcnt vmcnt(0)
	v_lshlrev_b32_e32 v66, 16, v70
	v_and_b32_e32 v67, 0xffff0000, v70
	s_waitcnt lgkmcnt(1)
	v_mfma_f32_32x32x16_bf16 v[82:97], v[102:105], v[98:101], v[82:97]
	ds_read_b128 v[102:105], v172 offset:8192
	ds_read_b128 v[134:137], v172 offset:9216
	v_lshlrev_b32_e32 v68, 16, v71
	v_and_b32_e32 v69, 0xffff0000, v71
	v_lshlrev_b32_e32 v70, 16, v72
	v_and_b32_e32 v71, 0xffff0000, v72
	v_lshlrev_b32_e32 v72, 16, v73
	v_and_b32_e32 v73, 0xffff0000, v73
	v_lshlrev_b32_e32 v74, 16, v78
	v_and_b32_e32 v75, 0xffff0000, v78
	v_lshlrev_b32_e32 v76, 16, v79
	v_and_b32_e32 v77, 0xffff0000, v79
	v_lshlrev_b32_e32 v78, 16, v80
	v_and_b32_e32 v79, 0xffff0000, v80
	v_lshlrev_b32_e32 v80, 16, v81
	v_and_b32_e32 v81, 0xffff0000, v81
	v_cvt_pk_bf16_f32 v146, v42, v43
	v_cvt_pk_bf16_f32 v147, v44, v45
	s_waitcnt lgkmcnt(1)
	v_mfma_f32_32x32x16_bf16 v[66:81], v[102:105], v[98:101], v[66:81]
	ds_read_b128 v[102:105], v172 offset:16384
	ds_read_b128 v[138:141], v172 offset:17408
	v_cvt_pk_bf16_f32 v148, v46, v47
	v_cvt_pk_bf16_f32 v149, v48, v49
	v_cmp_lt_i32_e32 vcc, v175, v176
	v_and_b32_e32 v179, 1, v177
	s_add_i32 s14, s14, 1
	v_cndmask_b32_e32 v0, v174, v175, vcc
	s_waitcnt lgkmcnt(1)
	v_mfma_f32_32x32x16_bf16 v[114:129], v[102:105], v[98:101], 0
	ds_read_b128 v[102:105], v172 offset:24576
	ds_read_b128 v[142:145], v172 offset:25600
	v_lshlrev_b32_e32 v178, 2, v0
	v_ashrrev_i32_e32 v0, 3, v177
	s_ashr_i32 s15, s14, 31
	v_lshlrev_b32_e32 v241, 1, v179
	v_lshlrev_b32_e32 v232, 5, v177
	v_ashrrev_i32_e32 v233, 31, v232
	s_waitcnt lgkmcnt(1)
	v_mfma_f32_32x32x16_bf16 v[98:113], v[102:105], v[98:101], 0
	v_mfma_f32_32x32x16_bf16 v[82:97], v[130:133], v[146:149], v[82:97]
	v_cvt_pk_bf16_f32 v130, v50, v51
	v_cvt_pk_bf16_f32 v131, v52, v53
	v_cvt_pk_bf16_f32 v132, v54, v55
	v_cvt_pk_bf16_f32 v133, v56, v57
	v_mfma_f32_32x32x16_bf16 v[66:81], v[134:137], v[146:149], v[66:81]
	v_mfma_f32_32x32x16_bf16 v[114:129], v[138:141], v[146:149], v[114:129]
	ds_read_b128 v[134:137], v172 offset:2048
	ds_read_b128 v[138:141], v172 offset:3072
	s_waitcnt lgkmcnt(2)
	v_mfma_f32_32x32x16_bf16 v[98:113], v[142:145], v[146:149], v[98:113]
	s_waitcnt lgkmcnt(1)
	v_mfma_f32_32x32x16_bf16 v[82:97], v[134:137], v[130:133], v[82:97]
	ds_read_b128 v[134:137], v172 offset:10240
	ds_read_b128 v[142:145], v172 offset:11264
	s_waitcnt lgkmcnt(1)
	v_mfma_f32_32x32x16_bf16 v[66:81], v[134:137], v[130:133], v[66:81]
	ds_read_b128 v[134:137], v172 offset:18432
	ds_read_b128 v[146:149], v172 offset:19456
	s_waitcnt lgkmcnt(1)
	v_mfma_f32_32x32x16_bf16 v[114:129], v[134:137], v[130:133], v[114:129]
	ds_read_b128 v[134:137], v172 offset:26624
	ds_read_b128 v[150:153], v172 offset:27648
	s_waitcnt lgkmcnt(1)
	v_mfma_f32_32x32x16_bf16 v[98:113], v[134:137], v[130:133], v[98:113]
	v_cvt_pk_bf16_f32 v130, v58, v59
	v_cvt_pk_bf16_f32 v131, v60, v61
	v_cvt_pk_bf16_f32 v132, v62, v63
	v_cvt_pk_bf16_f32 v133, v64, v65
	v_cvt_pk_bf16_f32 v134, v18, v19
	v_cvt_pk_bf16_f32 v135, v20, v21
	v_cvt_pk_bf16_f32 v136, v22, v23
	v_mfma_f32_32x32x16_bf16 v[82:97], v[138:141], v[130:133], v[82:97]
	v_cvt_pk_bf16_f32 v137, v24, v25
	v_mfma_f32_32x32x16_bf16 v[66:81], v[142:145], v[130:133], v[66:81]
	v_mfma_f32_32x32x16_bf16 v[114:129], v[146:149], v[130:133], v[114:129]
	s_waitcnt lgkmcnt(0)
	v_mfma_f32_32x32x16_bf16 v[98:113], v[150:153], v[130:133], v[98:113]
	ds_read_b128 v[130:133], v172 offset:4096
	ds_read_b128 v[138:141], v172 offset:5120
	s_waitcnt lgkmcnt(1)
	v_mfma_f32_32x32x16_bf16 v[82:97], v[130:133], v[134:137], v[82:97]
	ds_read_b128 v[130:133], v172 offset:12288
	ds_read_b128 v[142:145], v172 offset:13312
	s_waitcnt lgkmcnt(1)
	v_mfma_f32_32x32x16_bf16 v[66:81], v[130:133], v[134:137], v[66:81]
	ds_read_b128 v[130:133], v172 offset:20480
	ds_read_b128 v[146:149], v172 offset:21504
	s_waitcnt lgkmcnt(1)
	v_mfma_f32_32x32x16_bf16 v[114:129], v[130:133], v[134:137], v[114:129]
	ds_read_b128 v[130:133], v172 offset:28672
	ds_read_b128 v[150:153], v172 offset:29696
	s_waitcnt lgkmcnt(1)
	v_mfma_f32_32x32x16_bf16 v[98:113], v[130:133], v[134:137], v[98:113]
	v_cvt_pk_bf16_f32 v130, v26, v27
	v_cvt_pk_bf16_f32 v131, v28, v29
	v_cvt_pk_bf16_f32 v132, v30, v31
	v_cvt_pk_bf16_f32 v133, v32, v33
	v_cvt_pk_bf16_f32 v134, v2, v3
	v_cvt_pk_bf16_f32 v135, v4, v5
	v_cvt_pk_bf16_f32 v136, v6, v7
	v_mfma_f32_32x32x16_bf16 v[82:97], v[138:141], v[130:133], v[82:97]
	v_cvt_pk_bf16_f32 v137, v8, v9
	v_mfma_f32_32x32x16_bf16 v[66:81], v[142:145], v[130:133], v[66:81]
	v_mfma_f32_32x32x16_bf16 v[114:129], v[146:149], v[130:133], v[114:129]
	s_waitcnt lgkmcnt(0)
	v_mfma_f32_32x32x16_bf16 v[98:113], v[150:153], v[130:133], v[98:113]
	ds_read_b128 v[130:133], v172 offset:6144
	ds_read_b128 v[138:141], v172 offset:7168
	s_waitcnt lgkmcnt(1)
	v_mfma_f32_32x32x16_bf16 v[82:97], v[130:133], v[134:137], v[82:97]
	ds_read_b128 v[130:133], v172 offset:14336
	ds_read_b128 v[142:145], v172 offset:15360
	s_waitcnt lgkmcnt(1)
	v_mfma_f32_32x32x16_bf16 v[66:81], v[130:133], v[134:137], v[66:81]
	ds_read_b128 v[130:133], v172 offset:22528
	ds_read_b128 v[146:149], v172 offset:23552
	s_waitcnt lgkmcnt(1)
	v_mfma_f32_32x32x16_bf16 v[114:129], v[130:133], v[134:137], v[114:129]
	ds_read_b128 v[150:153], v172 offset:30720
	ds_read_b128 v[130:133], v172 offset:31744
	s_waitcnt lgkmcnt(1)
	v_mfma_f32_32x32x16_bf16 v[98:113], v[150:153], v[134:137], v[98:113]
	v_cvt_pk_bf16_f32 v134, v10, v11
	v_cvt_pk_bf16_f32 v135, v12, v13
	v_cvt_pk_bf16_f32 v136, v14, v15
	v_cvt_pk_bf16_f32 v137, v16, v17
	s_nop 1
	v_mfma_f32_32x32x16_bf16 v[82:97], v[138:141], v[134:137], v[82:97]
	v_and_or_b32 v138, v0, -4, v179
	global_load_dword v0, v173, s[16:17]
	v_lshlrev_b32_e32 v139, 1, v177
	v_and_b32_e32 v240, 62, v139
	v_ashrrev_i32_e32 v139, 31, v138
	v_or_b32_e32 v234, 2, v138
	v_add_u32_e32 v236, 34, v138
	s_waitcnt lgkmcnt(0)
	v_mfma_f32_32x32x16_bf16 v[98:113], v[130:133], v[134:137], v[98:113]
	ds_read_b128 v[130:133], v172 offset:57344
	ds_read_b128 v[162:165], v172 offset:58368
	s_nop 0
	v_cvt_pk_bf16_f32 v82, v82, v83
	v_cvt_pk_bf16_f32 v83, v84, v85
	v_cvt_pk_bf16_f32 v84, v86, v87
	v_cvt_pk_bf16_f32 v85, v88, v89
	ds_read_b128 v[86:89], v172 offset:61440
	ds_read_b128 v[166:169], v172 offset:62464
	v_lshlrev_b64 v[238:239], 12, v[138:139]
	v_mfma_f32_32x32x16_bf16 v[66:81], v[142:145], v[134:137], v[66:81]
	v_cvt_pk_bf16_f32 v90, v90, v91
	v_cvt_pk_bf16_f32 v91, v92, v93
	v_cvt_pk_bf16_f32 v92, v94, v95
	v_cvt_pk_bf16_f32 v93, v96, v97
	v_ashrrev_i32_e32 v235, 31, v234
	s_lshl_b64 s[16:17], s[14:15], 14
	s_add_u32 s16, s20, s16
	v_mfma_f32_32x32x16_bf16 v[114:129], v[146:149], v[134:137], v[114:129]
	s_nop 3
	v_cvt_pk_bf16_f32 v66, v66, v67
	v_cvt_pk_bf16_f32 v67, v68, v69
	v_cvt_pk_bf16_f32 v68, v70, v71
	v_cvt_pk_bf16_f32 v69, v72, v73
	s_addc_u32 s17, s21, s17
	v_ashrrev_i32_e32 v237, 31, v236
	s_waitcnt vmcnt(0)
	v_pk_mul_f32 v[48:49], v[48:49], v[0:1] op_sel_hi:[1,0]
	s_waitcnt lgkmcnt(3)
	v_mfma_f32_32x32x16_bf16 v[146:161], v[130:133], v[82:85], 0
	v_mul_f32_e64 v46, v46, v0
	v_mul_f32_e64 v47, v47, v0
	v_mul_f32_e64 v44, v44, v0
	v_mul_f32_e64 v45, v45, v0
	v_mul_f32_e64 v42, v42, v0
	v_mul_f32_e64 v43, v43, v0
	v_pk_mul_f32 v[40:41], v[40:41], v[0:1] op_sel_hi:[1,0]
	v_pk_mul_f32 v[38:39], v[38:39], v[0:1] op_sel_hi:[1,0]
	v_pk_mul_f32 v[36:37], v[36:37], v[0:1] op_sel_hi:[1,0]
	v_pk_mul_f32 v[34:35], v[34:35], v[0:1] op_sel_hi:[1,0]
	s_waitcnt lgkmcnt(1)
	v_mfma_f32_32x32x16_bf16 v[130:145], v[86:89], v[82:85], 0
	ds_read_b128 v[86:89], v172 offset:63488
	ds_read_b128 v[180:183], v172 offset:64512
	v_mul_f32_e64 v64, v64, v0
	v_mul_f32_e64 v65, v65, v0
	v_mul_f32_e64 v62, v62, v0
	v_mul_f32_e64 v63, v63, v0
	v_pk_mul_f32 v[60:61], v[60:61], v[0:1] op_sel_hi:[1,0]
	v_pk_mul_f32 v[58:59], v[58:59], v[0:1] op_sel_hi:[1,0]
	v_pk_mul_f32 v[56:57], v[56:57], v[0:1] op_sel_hi:[1,0]
	v_pk_mul_f32 v[54:55], v[54:55], v[0:1] op_sel_hi:[1,0]
	s_waitcnt lgkmcnt(2)
	v_mfma_f32_32x32x16_bf16 v[130:145], v[166:169], v[90:93], v[130:145]
	v_mul_f32_e64 v52, v52, v0
	v_mul_f32_e64 v53, v53, v0
	v_mul_f32_e64 v50, v50, v0
	v_mul_f32_e64 v51, v51, v0
	v_mul_f32_e64 v32, v32, v0
	v_mul_f32_e64 v33, v33, v0
	v_pk_mul_f32 v[30:31], v[30:31], v[0:1] op_sel_hi:[1,0]
	v_pk_mul_f32 v[28:29], v[28:29], v[0:1] op_sel_hi:[1,0]
	v_pk_mul_f32 v[26:27], v[26:27], v[0:1] op_sel_hi:[1,0]
	v_pk_mul_f32 v[24:25], v[24:25], v[0:1] op_sel_hi:[1,0]
	v_mfma_f32_32x32x16_bf16 v[146:161], v[162:165], v[90:93], v[146:161]
	ds_read_b128 v[94:97], v172 offset:49152
	ds_read_b128 v[184:187], v172 offset:50176
	ds_read_b128 v[188:191], v172 offset:53248
	ds_read_b128 v[192:195], v172 offset:54272
	ds_read_b128 v[162:165], v172 offset:55296
	ds_read_b128 v[82:85], v172 offset:56320
	ds_read_b128 v[196:199], v172 offset:36864
	ds_read_b128 v[200:203], v172 offset:45056
	ds_read_b128 v[204:207], v172 offset:32768
	ds_read_b128 v[208:211], v172 offset:33792
	v_or_b32_e32 v92, v238, v240
	v_lshlrev_b64 v[90:91], 12, v[234:235]
	v_or_b32_e32 v90, v90, v240
	v_pk_mul_f32 v[22:23], v[22:23], v[0:1] op_sel_hi:[1,0]
	v_pk_mul_f32 v[20:21], v[20:21], v[0:1] op_sel_hi:[1,0]
	s_waitcnt lgkmcnt(11)
	v_mfma_f32_32x32x16_bf16 v[130:145], v[86:89], v[66:69], v[130:145]
	ds_read_b128 v[212:215], v172 offset:37888
	ds_read_b128 v[66:69], v172 offset:40960
	ds_read_b128 v[216:219], v172 offset:41984
	v_cvt_pk_bf16_f32 v70, v146, v147
	v_cvt_pk_bf16_f32 v71, v148, v149
	v_cvt_pk_bf16_f32 v72, v150, v151
	v_cvt_pk_bf16_f32 v73, v152, v153
	v_pk_mul_f32 v[18:19], v[18:19], v[0:1] op_sel_hi:[1,0]
	v_pk_mul_f32 v[16:17], v[16:17], v[0:1] op_sel_hi:[1,0]
	s_waitcnt lgkmcnt(10)
	v_mfma_f32_32x32x16_bf16 v[98:113], v[188:191], v[70:73], v[98:113]
	v_sub_co_u32_e32 v188, vcc, v92, v241
	v_mul_f32_e64 v14, v14, v0
	v_mul_f32_e64 v15, v15, v0
	v_subbrev_co_u32_e32 v189, vcc, 0, v239, vcc
	v_mul_f32_e64 v12, v12, v0
	v_mul_f32_e64 v13, v13, v0
	v_pk_mul_f32 v[10:11], v[10:11], v[0:1] op_sel_hi:[1,0]
	v_pk_mul_f32 v[8:9], v[8:9], v[0:1] op_sel_hi:[1,0]
	v_pk_mul_f32 v[6:7], v[6:7], v[0:1] op_sel_hi:[1,0]
	v_pk_mul_f32 v[4:5], v[4:5], v[0:1] op_sel_hi:[1,0]
	v_pk_mul_f32 v[2:3], v[2:3], v[0:1] op_sel_hi:[1,0]
	v_mfma_f32_32x32x16_bf16 v[114:129], v[94:97], v[70:73], v[114:129]
	v_sub_co_u32_e32 v190, vcc, v90, v241
	ds_read_b128 v[220:223], v172 offset:46080
	ds_read_b128 v[166:169], v172 offset:43008
	ds_read_b128 v[150:153], v172 offset:47104
	ds_read_b128 v[224:227], v172 offset:34816
	ds_read_b128 v[146:149], v172 offset:35840
	ds_read_b128 v[228:231], v172 offset:38912
	ds_read_b128 v[94:97], v172 offset:39936
	ds_read_b128 v[86:89], v172 offset:44032
	v_subbrev_co_u32_e32 v191, vcc, 0, v91, vcc
	ds_read_b128 v[90:93], v172 offset:48128
	s_waitcnt lgkmcnt(13)
	v_mfma_f32_32x32x16_bf16 v[34:49], v[204:207], v[70:73], v[34:49]
	v_lshlrev_b64 v[234:235], 12, v[236:237]
	v_or_b32_e32 v172, v234, v240
	v_sub_co_u32_e32 v234, vcc, v172, v241
	s_nop 1
	v_subbrev_co_u32_e32 v235, vcc, 0, v235, vcc
	v_mfma_f32_32x32x16_bf16 v[50:65], v[196:199], v[70:73], v[50:65]
	v_lshl_add_u64 v[196:197], s[16:17], 0, v[232:233]
	s_add_u32 s16, s13, s4
	s_addc_u32 s17, s62, s5
	s_add_u32 s4, s4, 0x40000
	s_addc_u32 s5, s5, 0
	s_add_i32 s63, s63, 0x10000
	s_cmp_eq_u32 s4, 0x7c0000
	s_waitcnt lgkmcnt(10)
	v_mfma_f32_32x32x16_bf16 v[18:33], v[66:69], v[70:73], v[18:33]
	global_load_dwordx4 v[66:69], v[196:197], off offset:16
	v_mfma_f32_32x32x16_bf16 v[2:17], v[200:203], v[70:73], v[2:17]
	v_cvt_pk_bf16_f32 v70, v74, v75
	v_cvt_pk_bf16_f32 v71, v76, v77
	v_cvt_pk_bf16_f32 v72, v78, v79
	v_cvt_pk_bf16_f32 v73, v80, v81
	s_nop 1
	v_mfma_f32_32x32x16_bf16 v[130:145], v[180:183], v[70:73], v[130:145]
	global_load_dwordx4 v[74:77], v[196:197], off
	global_load_dwordx4 v[78:81], v[196:197], off offset:2064
	global_load_dwordx4 v[70:73], v[196:197], off offset:2048
	v_cvt_pk_bf16_f32 v181, v156, v157
	v_lshl_add_u64 v[156:157], s[16:17], 0, v[188:189]
	v_cvt_pk_bf16_f32 v183, v160, v161
	v_add_co_u32_e32 v160, vcc, s34, v156
	v_cvt_pk_bf16_f32 v180, v154, v155
	v_cvt_pk_bf16_f32 v182, v158, v159
	v_addc_co_u32_e32 v161, vcc, 0, v157, vcc
	s_nop 0
	v_mfma_f32_32x32x16_bf16 v[114:129], v[184:187], v[180:183], v[114:129]
	v_add_co_u32_e32 v184, vcc, s35, v156
	v_lshl_add_u64 v[158:159], s[16:17], 0, v[190:191]
	s_nop 0
	v_addc_co_u32_e32 v185, vcc, 0, v157, vcc
	v_add_co_u32_e32 v186, vcc, s33, v156
	v_mfma_f32_32x32x16_bf16 v[98:113], v[192:195], v[180:183], v[98:113]
	s_nop 0
	v_addc_co_u32_e32 v187, vcc, 0, v157, vcc
	v_add_co_u32_e32 v188, vcc, s36, v156
	v_cvt_pk_bf16_f32 v130, v130, v131
	s_nop 0
	v_addc_co_u32_e32 v189, vcc, 0, v157, vcc
	v_add_co_u32_e32 v190, vcc, s37, v156
	v_mfma_f32_32x32x16_bf16 v[34:49], v[208:211], v[180:183], v[34:49]
	s_nop 0
	v_addc_co_u32_e32 v191, vcc, 0, v157, vcc
	v_add_co_u32_e32 v192, vcc, s38, v156
	v_cvt_pk_bf16_f32 v131, v132, v133
	s_nop 0
	v_addc_co_u32_e32 v193, vcc, 0, v157, vcc
	v_add_co_u32_e32 v194, vcc, s39, v156
	v_mfma_f32_32x32x16_bf16 v[50:65], v[212:215], v[180:183], v[50:65]
	s_nop 0
	v_addc_co_u32_e32 v195, vcc, 0, v157, vcc
	v_add_co_u32_e32 v196, vcc, s40, v156
	v_cvt_pk_bf16_f32 v132, v134, v135
	s_nop 0
	v_addc_co_u32_e32 v197, vcc, 0, v157, vcc
	v_add_co_u32_e32 v198, vcc, s41, v156
	s_waitcnt lgkmcnt(9)
	v_mfma_f32_32x32x16_bf16 v[18:33], v[216:219], v[180:183], v[18:33]
	v_addc_co_u32_e32 v199, vcc, 0, v157, vcc
	v_cvt_pk_bf16_f32 v133, v136, v137
	v_cvt_pk_bf16_f32 v134, v138, v139
	v_cvt_pk_bf16_f32 v135, v140, v141
	v_cvt_pk_bf16_f32 v136, v142, v143
	v_cvt_pk_bf16_f32 v137, v144, v145
	s_waitcnt lgkmcnt(8)
	v_mfma_f32_32x32x16_bf16 v[2:17], v[220:223], v[180:183], v[2:17]
	v_add_co_u32_e32 v180, vcc, s42, v156
	v_lshl_add_u64 v[154:155], s[16:17], 0, v[234:235]
	s_nop 0
	v_addc_co_u32_e32 v181, vcc, 0, v157, vcc
	v_mfma_f32_32x32x16_bf16 v[98:113], v[162:165], v[130:133], v[98:113]
	v_add_co_u32_e32 v162, vcc, s43, v156
	s_nop 1
	v_addc_co_u32_e32 v163, vcc, 0, v157, vcc
	v_add_co_u32_e32 v164, vcc, s44, v156
	s_waitcnt lgkmcnt(5)
	v_mfma_f32_32x32x16_bf16 v[34:49], v[224:227], v[130:133], v[34:49]
	v_addc_co_u32_e32 v165, vcc, 0, v157, vcc
	v_add_co_u32_e32 v182, vcc, s45, v156
	s_nop 1
	v_addc_co_u32_e32 v183, vcc, 0, v157, vcc
	v_cmp_eq_u32_e32 vcc, 0, v179
	s_waitcnt lgkmcnt(3)
	v_mfma_f32_32x32x16_bf16 v[50:65], v[228:231], v[130:133], v[50:65]
	v_cndmask_b32_e32 v0, v114, v115, vcc
	v_cndmask_b32_e32 v138, v116, v117, vcc
	v_cndmask_b32_e32 v139, v118, v119, vcc
	v_cndmask_b32_e32 v140, v120, v121, vcc
	v_cndmask_b32_e32 v141, v122, v123, vcc
	v_cndmask_b32_e32 v142, v124, v125, vcc
	v_mfma_f32_32x32x16_bf16 v[18:33], v[166:169], v[130:133], v[18:33]
	ds_bpermute_b32 v0, v178, v0
	v_cndmask_b32_e32 v143, v126, v127, vcc
	v_cndmask_b32_e32 v144, v128, v129, vcc
	s_waitcnt lgkmcnt(0)
	v_cndmask_b32_e32 v115, v115, v0, vcc
	v_cndmask_b32_e32 v0, v0, v114, vcc
	v_mfma_f32_32x32x16_bf16 v[2:17], v[150:153], v[130:133], v[2:17]
	ds_bpermute_b32 v130, v178, v138
	ds_bpermute_b32 v131, v178, v139
	ds_bpermute_b32 v132, v178, v140
	ds_bpermute_b32 v133, v178, v141
	ds_bpermute_b32 v138, v178, v142
	ds_bpermute_b32 v139, v178, v143
	ds_bpermute_b32 v140, v178, v144
	v_mfma_f32_32x32x16_bf16 v[98:113], v[82:85], v[134:137], v[98:113]
	s_waitcnt lgkmcnt(6)
	v_cndmask_b32_e32 v114, v117, v130, vcc
	v_cndmask_b32_e32 v116, v130, v116, vcc
	s_waitcnt lgkmcnt(5)
	v_cndmask_b32_e32 v82, v119, v131, vcc
	v_cndmask_b32_e32 v83, v131, v118, vcc
	s_waitcnt lgkmcnt(4)
	v_cndmask_b32_e32 v84, v121, v132, vcc
	v_cndmask_b32_e32 v85, v132, v120, vcc
	s_waitcnt lgkmcnt(3)
	v_cndmask_b32_e32 v117, v123, v133, vcc
	v_cndmask_b32_e32 v118, v133, v122, vcc
	s_waitcnt lgkmcnt(2)
	v_cndmask_b32_e32 v119, v125, v138, vcc
	v_cndmask_b32_e32 v120, v138, v124, vcc
	v_cvt_pk_bf16_f32 v0, v0, v115
	v_mfma_f32_32x32x16_bf16 v[34:49], v[146:149], v[134:137], v[34:49]
	s_waitcnt lgkmcnt(1)
	v_cndmask_b32_e32 v121, v127, v139, vcc
	v_cndmask_b32_e32 v122, v139, v126, vcc
	s_waitcnt lgkmcnt(0)
	v_cndmask_b32_e32 v123, v129, v140, vcc
	v_cndmask_b32_e32 v124, v140, v128, vcc
	v_cvt_pk_bf16_f32 v114, v116, v114
	v_cvt_pk_bf16_f32 v82, v83, v82
	v_cvt_pk_bf16_f32 v83, v85, v84
	v_mfma_f32_32x32x16_bf16 v[50:65], v[94:97], v[134:137], v[50:65]
	v_cvt_pk_bf16_f32 v84, v118, v117
	v_cvt_pk_bf16_f32 v85, v120, v119
	global_store_dword v[156:157], v0, off nt
	v_cndmask_b32_e32 v0, v98, v99, vcc
	v_cvt_pk_bf16_f32 v94, v122, v121
	v_cvt_pk_bf16_f32 v95, v124, v123
	global_store_dword v[158:159], v114, off nt
	global_store_dword v[160:161], v82, off nt
	global_store_dword v[184:185], v83, off nt
	global_store_dword v[186:187], v84, off nt
	global_store_dword v[188:189], v85, off nt
	global_store_dword v[190:191], v94, off nt
	global_store_dword v[192:193], v95, off nt
	v_mfma_f32_32x32x16_bf16 v[18:33], v[86:89], v[134:137], v[18:33]
	v_cndmask_b32_e32 v82, v100, v101, vcc
	v_cndmask_b32_e32 v83, v102, v103, vcc
	v_cndmask_b32_e32 v84, v104, v105, vcc
	v_cndmask_b32_e32 v85, v106, v107, vcc
	v_cndmask_b32_e32 v86, v108, v109, vcc
	v_cndmask_b32_e32 v87, v110, v111, vcc
	v_cndmask_b32_e32 v88, v112, v113, vcc
	v_mfma_f32_32x32x16_bf16 v[2:17], v[90:93], v[134:137], v[2:17]
	ds_bpermute_b32 v0, v178, v0
	ds_bpermute_b32 v82, v178, v82
	ds_bpermute_b32 v83, v178, v83
	ds_bpermute_b32 v84, v178, v84
	ds_bpermute_b32 v85, v178, v85
	ds_bpermute_b32 v86, v178, v86
	ds_bpermute_b32 v87, v178, v87
	ds_bpermute_b32 v88, v178, v88
	s_waitcnt lgkmcnt(7)
	v_cndmask_b32_e32 v89, v99, v0, vcc
	v_cndmask_b32_e32 v0, v0, v98, vcc
	s_waitcnt lgkmcnt(6)
	v_cndmask_b32_e32 v90, v101, v82, vcc
	v_cndmask_b32_e32 v82, v82, v100, vcc
	s_waitcnt lgkmcnt(5)
	v_cndmask_b32_e32 v91, v103, v83, vcc
	v_cndmask_b32_e32 v83, v83, v102, vcc
	s_waitcnt lgkmcnt(4)
	v_cndmask_b32_e32 v92, v105, v84, vcc
	v_cndmask_b32_e32 v84, v84, v104, vcc
	s_waitcnt lgkmcnt(3)
	v_cndmask_b32_e32 v93, v107, v85, vcc
	v_cndmask_b32_e32 v85, v85, v106, vcc
	s_waitcnt lgkmcnt(2)
	v_cndmask_b32_e32 v94, v109, v86, vcc
	v_cndmask_b32_e32 v86, v86, v108, vcc
	s_waitcnt lgkmcnt(1)
	v_cndmask_b32_e32 v95, v111, v87, vcc
	v_cndmask_b32_e32 v87, v87, v110, vcc
	s_waitcnt lgkmcnt(0)
	v_cndmask_b32_e32 v96, v113, v88, vcc
	v_cndmask_b32_e32 v88, v88, v112, vcc
	v_cvt_pk_bf16_f32 v0, v0, v89
	v_cvt_pk_bf16_f32 v82, v82, v90
	v_cvt_pk_bf16_f32 v83, v83, v91
	v_cvt_pk_bf16_f32 v84, v84, v92
	v_cvt_pk_bf16_f32 v85, v85, v93
	v_cvt_pk_bf16_f32 v86, v86, v94
	v_cvt_pk_bf16_f32 v87, v87, v95
	v_cvt_pk_bf16_f32 v88, v88, v96
	global_store_dword v[194:195], v0, off nt
	global_store_dword v[154:155], v82, off nt
	global_store_dword v[196:197], v83, off nt
	global_store_dword v[198:199], v84, off nt
	global_store_dword v[180:181], v85, off nt
	global_store_dword v[162:163], v86, off nt
	global_store_dword v[164:165], v87, off nt
	global_store_dword v[182:183], v88, off nt
	s_cbranch_scc0 .LBB0_548
	s_waitcnt lgkmcnt(0)
	s_barrier
	s_waitcnt vmcnt(18)
	v_lshlrev_b32_e32 v82, 16, v74
	v_lshl_add_u32 v0, v177, 4, 0
	v_add_u32_e32 v0, 0x10000, v0
	ds_read_b128 v[98:101], v0
	v_and_b32_e32 v83, 0xffff0000, v74
	v_lshlrev_b32_e32 v84, 16, v75
	v_and_b32_e32 v85, 0xffff0000, v75
	v_lshlrev_b32_e32 v86, 16, v76
	v_and_b32_e32 v87, 0xffff0000, v76
	v_lshlrev_b32_e32 v88, 16, v77
	v_and_b32_e32 v89, 0xffff0000, v77
	v_lshlrev_b32_e32 v90, 16, v66
	v_and_b32_e32 v91, 0xffff0000, v66
	v_lshlrev_b32_e32 v92, 16, v67
	v_and_b32_e32 v93, 0xffff0000, v67
	v_lshlrev_b32_e32 v94, 16, v68
	v_and_b32_e32 v95, 0xffff0000, v68
	v_lshlrev_b32_e32 v96, 16, v69
	v_and_b32_e32 v97, 0xffff0000, v69
	v_cvt_pk_bf16_f32 v122, v34, v35
	v_cvt_pk_bf16_f32 v123, v36, v37
	v_cvt_pk_bf16_f32 v124, v38, v39
	v_cvt_pk_bf16_f32 v125, v40, v41
	ds_read_b128 v[34:37], v0 offset:8192
	ds_read_b128 v[38:41], v0 offset:1024
	s_waitcnt lgkmcnt(2)
	v_mfma_f32_32x32x16_bf16 v[82:97], v[98:101], v[122:125], v[82:97]
	s_waitcnt vmcnt(16)
	v_lshlrev_b32_e32 v66, 16, v70
	v_and_b32_e32 v67, 0xffff0000, v70
	v_lshlrev_b32_e32 v68, 16, v71
	v_and_b32_e32 v69, 0xffff0000, v71
	v_lshlrev_b32_e32 v70, 16, v72
	v_and_b32_e32 v71, 0xffff0000, v72
	v_lshlrev_b32_e32 v72, 16, v73
	v_and_b32_e32 v73, 0xffff0000, v73
	v_lshlrev_b32_e32 v74, 16, v78
	v_and_b32_e32 v75, 0xffff0000, v78
	v_lshlrev_b32_e32 v76, 16, v79
	v_and_b32_e32 v77, 0xffff0000, v79
	v_lshlrev_b32_e32 v78, 16, v80
	v_and_b32_e32 v79, 0xffff0000, v80
	v_lshlrev_b32_e32 v80, 16, v81
	v_and_b32_e32 v81, 0xffff0000, v81
	ds_read_b128 v[98:101], v0 offset:9216
	v_cvt_pk_bf16_f32 v126, v42, v43
	s_waitcnt lgkmcnt(2)
	v_mfma_f32_32x32x16_bf16 v[66:81], v[34:37], v[122:125], v[66:81]
	v_cvt_pk_bf16_f32 v127, v44, v45
	v_cvt_pk_bf16_f32 v128, v46, v47
	v_cvt_pk_bf16_f32 v129, v48, v49
	ds_read_b128 v[34:37], v0 offset:2048
	v_cvt_pk_bf16_f32 v110, v50, v51
	v_cvt_pk_bf16_f32 v111, v52, v53
	v_cvt_pk_bf16_f32 v112, v54, v55
	s_waitcnt lgkmcnt(2)
	v_mfma_f32_32x32x16_bf16 v[82:97], v[38:41], v[126:129], v[82:97]
	v_cvt_pk_bf16_f32 v113, v56, v57
	ds_read_b128 v[38:41], v0 offset:3072
	v_cvt_pk_bf16_f32 v118, v58, v59
	v_cvt_pk_bf16_f32 v119, v60, v61
	v_cvt_pk_bf16_f32 v120, v62, v63
	v_cvt_pk_bf16_f32 v121, v64, v65
	v_cvt_pk_bf16_f32 v114, v18, v19
	s_waitcnt lgkmcnt(2)
	v_mfma_f32_32x32x16_bf16 v[66:81], v[98:101], v[126:129], v[66:81]
	v_cvt_pk_bf16_f32 v115, v20, v21
	v_cvt_pk_bf16_f32 v116, v22, v23
	v_cvt_pk_bf16_f32 v117, v24, v25
	v_cvt_pk_bf16_f32 v106, v26, v27
	v_cvt_pk_bf16_f32 v107, v28, v29
	v_cvt_pk_bf16_f32 v108, v30, v31
	v_cvt_pk_bf16_f32 v109, v32, v33
	s_waitcnt lgkmcnt(1)
	v_mfma_f32_32x32x16_bf16 v[82:97], v[34:37], v[110:113], v[82:97]
	ds_read_b128 v[34:37], v0 offset:10240
	ds_read_b128 v[42:45], v0 offset:11264
	ds_read_b128 v[18:21], v0 offset:5120
	v_cvt_pk_bf16_f32 v102, v2, v3
	v_cvt_pk_bf16_f32 v103, v4, v5
	v_cvt_pk_bf16_f32 v104, v6, v7
	v_cvt_pk_bf16_f32 v105, v8, v9
	v_cvt_pk_bf16_f32 v98, v10, v11
	s_waitcnt lgkmcnt(2)
	v_mfma_f32_32x32x16_bf16 v[66:81], v[34:37], v[110:113], v[66:81]
	ds_read_b128 v[34:37], v0 offset:4096
	v_cvt_pk_bf16_f32 v99, v12, v13
	v_cvt_pk_bf16_f32 v100, v14, v15
	v_cvt_pk_bf16_f32 v101, v16, v17
	s_lshl_b32 s1, s12, 8
	s_lshl_b32 s0, s12, 7
	s_and_b32 s1, s1, 0xf00
	v_mfma_f32_32x32x16_bf16 v[82:97], v[38:41], v[118:121], v[82:97]
	s_add_u32 s1, s22, s1
	s_addc_u32 s2, s23, 0
	s_or_b32 s4, s0, 0x7c0
	s_ashr_i32 s5, s4, 31
	s_lshl_b64 s[4:5], s[4:5], 12
	s_add_u32 s4, s1, s4
	s_addc_u32 s5, s2, s5
	s_waitcnt lgkmcnt(0)
	v_mfma_f32_32x32x16_bf16 v[82:97], v[34:37], v[114:117], v[82:97]
	ds_read_b128 v[22:25], v0 offset:12288
	ds_read_b128 v[34:37], v0 offset:13312
	ds_read_b128 v[2:5], v0 offset:7168
	v_mfma_f32_32x32x16_bf16 v[82:97], v[18:21], v[106:109], v[82:97]
	ds_read_b128 v[18:21], v0 offset:6144
	v_mfma_f32_32x32x16_bf16 v[66:81], v[42:45], v[118:121], v[66:81]
	s_waitcnt lgkmcnt(3)
	v_mfma_f32_32x32x16_bf16 v[66:81], v[22:25], v[114:117], v[66:81]
	s_waitcnt lgkmcnt(0)
	v_mfma_f32_32x32x16_bf16 v[82:97], v[18:21], v[102:105], v[82:97]
	ds_read_b128 v[6:9], v0 offset:14336
	ds_read_b128 v[18:21], v0 offset:15360
	ds_read_b128 v[10:13], v0 offset:58368
	v_mfma_f32_32x32x16_bf16 v[66:81], v[34:37], v[106:109], v[66:81]
	v_mfma_f32_32x32x16_bf16 v[82:97], v[2:5], v[98:101], v[82:97]
	ds_read_b128 v[2:5], v0 offset:57344
	s_waitcnt lgkmcnt(3)
	v_mfma_f32_32x32x16_bf16 v[66:81], v[6:9], v[102:105], v[66:81]
	s_nop 8
	v_cvt_pk_bf16_f32 v6, v82, v83
	v_cvt_pk_bf16_f32 v7, v84, v85
	v_cvt_pk_bf16_f32 v8, v86, v87
	v_cvt_pk_bf16_f32 v9, v88, v89
	s_waitcnt lgkmcnt(0)
	s_nop 0
	v_mfma_f32_32x32x16_bf16 v[50:65], v[2:5], v[6:9], 0
	ds_read_b128 v[2:5], v0 offset:61440
	ds_read_b128 v[14:17], v0 offset:62464
	s_waitcnt lgkmcnt(1)
	v_mfma_f32_32x32x16_bf16 v[34:49], v[2:5], v[6:9], 0
	v_cvt_pk_bf16_f32 v2, v90, v91
	v_cvt_pk_bf16_f32 v3, v92, v93
	v_cvt_pk_bf16_f32 v4, v94, v95
	v_cvt_pk_bf16_f32 v5, v96, v97
	v_and_b32_e32 v94, 31, v177
	v_lshlrev_b32_e32 v172, 1, v94
	v_mfma_f32_32x32x16_bf16 v[66:81], v[18:21], v[98:101], v[66:81]
	v_mfma_f32_32x32x16_bf16 v[50:65], v[10:13], v[2:5], v[50:65]
	s_nop 10
	v_cvt_pk_bf16_f32 v6, v66, v67
	v_cvt_pk_bf16_f32 v7, v68, v69
	v_cvt_pk_bf16_f32 v8, v70, v71
	v_cvt_pk_bf16_f32 v9, v72, v73
	ds_read_b128 v[10:13], v0 offset:64512
	v_cvt_pk_bf16_f32 v50, v50, v51
	s_waitcnt lgkmcnt(1)
	v_mfma_f32_32x32x16_bf16 v[34:49], v[14:17], v[2:5], v[34:49]
	ds_read_b128 v[2:5], v0 offset:63488
	v_cvt_pk_bf16_f32 v51, v52, v53
	v_cvt_pk_bf16_f32 v52, v54, v55
	v_cvt_pk_bf16_f32 v54, v58, v59
	v_cvt_pk_bf16_f32 v55, v60, v61
	v_cvt_pk_bf16_f32 v53, v56, v57
	v_cvt_pk_bf16_f32 v56, v62, v63
	s_waitcnt lgkmcnt(0)
	v_mfma_f32_32x32x16_bf16 v[34:49], v[2:5], v[6:9], v[34:49]
	v_cvt_pk_bf16_f32 v2, v74, v75
	v_cvt_pk_bf16_f32 v3, v76, v77
	v_cvt_pk_bf16_f32 v4, v78, v79
	v_cvt_pk_bf16_f32 v5, v80, v81
	v_cvt_pk_bf16_f32 v57, v64, v65
	s_nop 0
	v_mfma_f32_32x32x16_bf16 v[34:49], v[10:13], v[2:5], v[34:49]
	ds_read_b128 v[2:5], v0 offset:16384
	ds_read_b128 v[66:69], v0 offset:17408
	s_waitcnt lgkmcnt(1)
	v_mfma_f32_32x32x16_bf16 v[18:33], v[2:5], v[122:125], 0
	ds_read_b128 v[2:5], v0 offset:24576
	ds_read_b128 v[70:73], v0 offset:25600
	s_nop 5
	v_cvt_pk_bf16_f32 v34, v34, v35
	v_cvt_pk_bf16_f32 v35, v36, v37
	v_cvt_pk_bf16_f32 v36, v38, v39
	v_cvt_pk_bf16_f32 v37, v40, v41
	v_cvt_pk_bf16_f32 v42, v42, v43
	v_cvt_pk_bf16_f32 v43, v44, v45
	s_waitcnt lgkmcnt(1)
	v_mfma_f32_32x32x16_bf16 v[2:17], v[2:5], v[122:125], 0
	v_cvt_pk_bf16_f32 v44, v46, v47
	v_cvt_pk_bf16_f32 v45, v48, v49
	v_mfma_f32_32x32x16_bf16 v[18:33], v[66:69], v[126:129], v[18:33]
	s_waitcnt lgkmcnt(0)
	v_mfma_f32_32x32x16_bf16 v[2:17], v[70:73], v[126:129], v[2:17]
	ds_read_b128 v[66:69], v0 offset:18432
	ds_read_b128 v[70:73], v0 offset:19456
	ds_read_b128 v[58:61], v0 offset:22528
	ds_read_b128 v[38:41], v0 offset:23552
	s_waitcnt lgkmcnt(3)
	v_mfma_f32_32x32x16_bf16 v[18:33], v[66:69], v[110:113], v[18:33]
	ds_read_b128 v[66:69], v0 offset:20480
	s_waitcnt lgkmcnt(3)
	v_mfma_f32_32x32x16_bf16 v[18:33], v[70:73], v[118:121], v[18:33]
	ds_read_b128 v[70:73], v0 offset:21504
	s_waitcnt lgkmcnt(1)
	v_mfma_f32_32x32x16_bf16 v[18:33], v[66:69], v[114:117], v[18:33]
	s_waitcnt lgkmcnt(0)
	v_mfma_f32_32x32x16_bf16 v[18:33], v[70:73], v[106:109], v[18:33]
	v_mfma_f32_32x32x16_bf16 v[18:33], v[58:61], v[102:105], v[18:33]
	ds_read_b128 v[46:49], v0 offset:26624
	ds_read_b128 v[58:61], v0 offset:27648
	ds_read_b128 v[62:65], v0 offset:49152
	s_waitcnt lgkmcnt(2)
	v_mfma_f32_32x32x16_bf16 v[2:17], v[46:49], v[110:113], v[2:17]
	v_ashrrev_i32_e32 v48, 3, v177
	v_mfma_f32_32x32x16_bf16 v[18:33], v[38:41], v[98:101], v[18:33]
	ds_read_b128 v[38:41], v0 offset:28672
	ds_read_b128 v[66:69], v0 offset:29696
	ds_read_b128 v[70:73], v0 offset:30720
	ds_read_b128 v[74:77], v0 offset:31744
	ds_read_b128 v[78:81], v0 offset:50176
	ds_read_b128 v[82:85], v0 offset:53248
	ds_read_b128 v[86:89], v0 offset:54272
	s_waitcnt lgkmcnt(8)
	v_mfma_f32_32x32x16_bf16 v[2:17], v[58:61], v[118:121], v[2:17]
	s_waitcnt lgkmcnt(7)
	v_mfma_f32_32x32x16_bf16 v[18:33], v[62:65], v[50:53], v[18:33]
	ds_read_b128 v[62:65], v0 offset:55296
	ds_read_b128 v[90:93], v0 offset:56320
	v_and_b32_e32 v0, 1, v177
	v_and_or_b32 v48, v48, -4, v0
	v_ashrrev_i32_e32 v49, 31, v48
	s_waitcnt lgkmcnt(8)
	v_mfma_f32_32x32x16_bf16 v[2:17], v[38:41], v[114:117], v[2:17]
	s_waitcnt lgkmcnt(4)
	v_mfma_f32_32x32x16_bf16 v[18:33], v[78:81], v[54:57], v[18:33]
	v_lshl_add_u64 v[78:79], s[4:5], 0, v[172:173]
	v_cmp_eq_u32_e64 s[4:5], 0, v0
	v_lshlrev_b32_e32 v80, 1, v0
	v_sub_co_u32_e32 v46, vcc, v78, v80
	s_nop 1
	v_subbrev_co_u32_e32 v47, vcc, 0, v79, vcc
	v_mfma_f32_32x32x16_bf16 v[2:17], v[66:69], v[106:109], v[2:17]
	s_nop 3
	v_cndmask_b32_e64 v81, v18, v19, s[4:5]
	ds_bpermute_b32 v81, v178, v81
	v_cndmask_b32_e64 v38, v22, v23, s[4:5]
	ds_bpermute_b32 v38, v178, v38
	s_waitcnt lgkmcnt(1)
	v_cndmask_b32_e64 v0, v19, v81, s[4:5]
	v_cndmask_b32_e64 v18, v81, v18, s[4:5]
	v_mfma_f32_32x32x16_bf16 v[2:17], v[70:73], v[102:105], v[2:17]
	v_cvt_pk_bf16_f32 v0, v18, v0
	v_cndmask_b32_e64 v18, v20, v21, s[4:5]
	ds_bpermute_b32 v58, v178, v18
	v_lshlrev_b64 v[18:19], 12, v[48:49]
	v_lshl_add_u64 v[18:19], v[46:47], 0, v[18:19]
	global_store_dword v[18:19], v0, off nt
	s_waitcnt lgkmcnt(0)
	v_cndmask_b32_e64 v0, v21, v58, s[4:5]
	v_cndmask_b32_e64 v20, v58, v20, s[4:5]
	v_cvt_pk_bf16_f32 v0, v20, v0
	v_or_b32_e32 v20, 2, v48
	v_mfma_f32_32x32x16_bf16 v[2:17], v[74:77], v[98:101], v[2:17]
	v_ashrrev_i32_e32 v21, 31, v20
	v_lshlrev_b64 v[20:21], 12, v[20:21]
	v_lshl_add_u64 v[20:21], v[46:47], 0, v[20:21]
	global_store_dword v[20:21], v0, off nt
	v_cndmask_b32_e64 v0, v23, v38, s[4:5]
	v_cndmask_b32_e64 v20, v38, v22, s[4:5]
	v_cvt_pk_bf16_f32 v0, v20, v0
	v_cndmask_b32_e64 v20, v24, v25, s[4:5]
	ds_bpermute_b32 v22, v178, v20
	v_mfma_f32_32x32x16_bf16 v[2:17], v[82:85], v[50:53], v[2:17]
	v_add_co_u32_e32 v20, vcc, s34, v18
	s_nop 1
	v_addc_co_u32_e32 v21, vcc, 0, v19, vcc
	global_store_dword v[20:21], v0, off nt
	s_waitcnt lgkmcnt(0)
	v_cndmask_b32_e64 v0, v25, v22, s[4:5]
	v_cndmask_b32_e64 v20, v22, v24, s[4:5]
	v_cvt_pk_bf16_f32 v0, v20, v0
	v_cndmask_b32_e64 v20, v26, v27, s[4:5]
	ds_bpermute_b32 v22, v178, v20
	v_add_co_u32_e32 v20, vcc, s35, v18
	v_mfma_f32_32x32x16_bf16 v[2:17], v[86:89], v[54:57], v[2:17]
	s_nop 0
	v_addc_co_u32_e32 v21, vcc, 0, v19, vcc
	global_store_dword v[20:21], v0, off nt
	s_waitcnt lgkmcnt(0)
	v_cndmask_b32_e64 v0, v27, v22, s[4:5]
	v_cndmask_b32_e64 v20, v22, v26, s[4:5]
	v_cvt_pk_bf16_f32 v0, v20, v0
	v_cndmask_b32_e64 v20, v28, v29, s[4:5]
	ds_bpermute_b32 v22, v178, v20
	v_add_co_u32_e32 v20, vcc, s33, v18
	v_mfma_f32_32x32x16_bf16 v[2:17], v[62:65], v[34:37], v[2:17]
	s_nop 0
	v_addc_co_u32_e32 v21, vcc, 0, v19, vcc
	global_store_dword v[20:21], v0, off nt
	s_waitcnt lgkmcnt(0)
	v_cndmask_b32_e64 v0, v29, v22, s[4:5]
	v_cndmask_b32_e64 v20, v22, v28, s[4:5]
	v_cvt_pk_bf16_f32 v0, v20, v0
	v_cndmask_b32_e64 v20, v30, v31, s[4:5]
	ds_bpermute_b32 v22, v178, v20
	v_add_co_u32_e32 v20, vcc, s36, v18
	v_mfma_f32_32x32x16_bf16 v[2:17], v[90:93], v[42:45], v[2:17]
	s_nop 0
	v_addc_co_u32_e32 v21, vcc, 0, v19, vcc
	global_store_dword v[20:21], v0, off nt
	s_waitcnt lgkmcnt(0)
	v_cndmask_b32_e64 v0, v31, v22, s[4:5]
	v_cndmask_b32_e64 v20, v22, v30, s[4:5]
	v_cvt_pk_bf16_f32 v0, v20, v0
	v_cndmask_b32_e64 v20, v32, v33, s[4:5]
	ds_bpermute_b32 v22, v178, v20
	v_add_co_u32_e32 v20, vcc, s37, v18
	s_nop 1
	v_addc_co_u32_e32 v21, vcc, 0, v19, vcc
	global_store_dword v[20:21], v0, off nt
	s_waitcnt lgkmcnt(0)
	v_cndmask_b32_e64 v0, v33, v22, s[4:5]
	v_cndmask_b32_e64 v20, v22, v32, s[4:5]
	v_cvt_pk_bf16_f32 v0, v20, v0
	v_cndmask_b32_e64 v20, v2, v3, s[4:5]
	ds_bpermute_b32 v22, v178, v20
	v_add_co_u32_e32 v20, vcc, s38, v18
	s_waitcnt lgkmcnt(0)
	v_cndmask_b32_e64 v2, v22, v2, s[4:5]
	v_addc_co_u32_e32 v21, vcc, 0, v19, vcc
	global_store_dword v[20:21], v0, off nt
	v_cndmask_b32_e64 v0, v3, v22, s[4:5]
	v_cvt_pk_bf16_f32 v0, v2, v0
	v_cndmask_b32_e64 v2, v4, v5, s[4:5]
	ds_bpermute_b32 v20, v178, v2
	v_add_co_u32_e32 v2, vcc, s39, v18
	s_nop 1
	v_addc_co_u32_e32 v3, vcc, 0, v19, vcc
	global_store_dword v[2:3], v0, off nt
	v_cndmask_b32_e64 v3, v6, v7, s[4:5]
	s_waitcnt lgkmcnt(0)
	v_cndmask_b32_e64 v0, v5, v20, s[4:5]
	v_cndmask_b32_e64 v2, v20, v4, s[4:5]
	ds_bpermute_b32 v4, v178, v3
	v_cvt_pk_bf16_f32 v0, v2, v0
	v_add_u32_e32 v2, 34, v48
	v_ashrrev_i32_e32 v3, 31, v2
	v_lshlrev_b64 v[2:3], 12, v[2:3]
	v_lshl_add_u64 v[2:3], v[46:47], 0, v[2:3]
	global_store_dword v[2:3], v0, off nt
	s_waitcnt lgkmcnt(0)
	v_cndmask_b32_e64 v0, v7, v4, s[4:5]
	v_cndmask_b32_e64 v2, v4, v6, s[4:5]
	v_cvt_pk_bf16_f32 v0, v2, v0
	v_cndmask_b32_e64 v2, v8, v9, s[4:5]
	ds_bpermute_b32 v4, v178, v2
	v_add_co_u32_e32 v2, vcc, s40, v18
	s_nop 1
	v_addc_co_u32_e32 v3, vcc, 0, v19, vcc
	global_store_dword v[2:3], v0, off nt
	s_waitcnt lgkmcnt(0)
	v_cndmask_b32_e64 v0, v9, v4, s[4:5]
	v_cndmask_b32_e64 v2, v4, v8, s[4:5]
	v_cvt_pk_bf16_f32 v0, v2, v0
	v_cndmask_b32_e64 v2, v10, v11, s[4:5]
	ds_bpermute_b32 v4, v178, v2
	v_add_co_u32_e32 v2, vcc, s41, v18
	s_nop 1
	v_addc_co_u32_e32 v3, vcc, 0, v19, vcc
	global_store_dword v[2:3], v0, off nt
	s_waitcnt lgkmcnt(0)
	v_cndmask_b32_e64 v0, v11, v4, s[4:5]
	v_cndmask_b32_e64 v2, v4, v10, s[4:5]
	v_cvt_pk_bf16_f32 v0, v2, v0
	v_cndmask_b32_e64 v2, v12, v13, s[4:5]
	ds_bpermute_b32 v4, v178, v2
	v_add_co_u32_e32 v2, vcc, s42, v18
	s_nop 1
	v_addc_co_u32_e32 v3, vcc, 0, v19, vcc
	global_store_dword v[2:3], v0, off nt
	s_waitcnt lgkmcnt(0)
	v_cndmask_b32_e64 v0, v13, v4, s[4:5]
	v_cndmask_b32_e64 v2, v4, v12, s[4:5]
	v_cvt_pk_bf16_f32 v0, v2, v0
	v_cndmask_b32_e64 v2, v14, v15, s[4:5]
	ds_bpermute_b32 v4, v178, v2
	v_add_co_u32_e32 v2, vcc, s43, v18
	s_nop 1
	v_addc_co_u32_e32 v3, vcc, 0, v19, vcc
	global_store_dword v[2:3], v0, off nt
	v_cndmask_b32_e64 v3, v16, v17, s[4:5]
	s_waitcnt lgkmcnt(0)
	v_cndmask_b32_e64 v0, v15, v4, s[4:5]
	v_cndmask_b32_e64 v2, v4, v14, s[4:5]
	ds_bpermute_b32 v4, v178, v3
	v_cvt_pk_bf16_f32 v0, v2, v0
	v_add_co_u32_e32 v2, vcc, s44, v18
	s_nop 1
	v_addc_co_u32_e32 v3, vcc, 0, v19, vcc
	global_store_dword v[2:3], v0, off nt
	s_waitcnt lgkmcnt(0)
	v_cndmask_b32_e64 v0, v17, v4, s[4:5]
	v_cndmask_b32_e64 v2, v4, v16, s[4:5]
	v_cvt_pk_bf16_f32 v0, v2, v0
	v_add_co_u32_e32 v2, vcc, 0x3a000, v18
	s_mov_b64 s[4:5], 0
	s_nop 0
	v_addc_co_u32_e32 v3, vcc, 0, v19, vcc
	global_store_dword v[2:3], v0, off nt
	s_barrier

.LBB0_561:
	v_cmp_eq_u32_e32 vcc, 0, v175
	v_pk_add_f32 v[76:77], v[76:77], v[90:91]
	v_pk_add_f32 v[68:69], v[68:69], v[82:83]
	v_pk_add_f32 v[66:67], v[66:67], v[74:75]
	v_pk_add_f32 v[70:71], v[70:71], v[84:85]
	v_pk_add_f32 v[74:75], v[88:89], v[96:97]
	v_pk_add_f32 v[78:79], v[78:79], v[92:93]
	v_pk_add_f32 v[72:73], v[72:73], v[86:87]
	v_pk_add_f32 v[80:81], v[80:81], v[94:95]
	v_cndmask_b32_e64 v135, v211, 0, vcc
	v_cndmask_b32_e32 v134, v212, v211, vcc
	v_cndmask_b32_e32 v150, v213, v212, vcc
	s_waitcnt lgkmcnt(12)
	v_cndmask_b32_e32 v151, v203, v213, vcc
	v_pk_add_f32 v[66:67], v[66:67], v[72:73]
	v_pk_add_f32 v[68:69], v[68:69], v[78:79]
	v_pk_add_f32 v[72:73], v[76:77], v[74:75]
	v_pk_add_f32 v[70:71], v[70:71], v[80:81]
	s_waitcnt lgkmcnt(8)
	v_cndmask_b32_e32 v75, v198, v210, vcc
	v_cndmask_b32_e32 v74, v210, v209, vcc
	v_cndmask_b32_e32 v77, v209, v206, vcc
	v_cndmask_b32_e32 v76, v206, v203, vcc
	v_pk_add_f32 v[70:71], v[134:135], v[70:71]
	v_pk_add_f32 v[72:73], v[150:151], v[72:73]
	v_pk_add_f32 v[68:69], v[76:77], v[68:69]
	v_pk_add_f32 v[66:67], v[74:75], v[66:67]
	v_pk_add_f32 v[114:115], v[114:115], v[68:69]
	v_pk_add_f32 v[112:113], v[112:113], v[66:67]
	v_pk_add_f32 v[110:111], v[110:111], v[72:73]
	v_pk_add_f32 v[108:109], v[108:109], v[70:71]
	v_pk_add_f32 v[66:67], v[154:155], v[152:153]
	v_pk_add_f32 v[68:69], v[148:149], v[156:157]
	v_pk_add_f32 v[70:71], v[146:147], v[128:129]
	v_pk_add_f32 v[72:73], v[144:145], v[130:131]
	v_pk_add_f32 v[66:67], v[66:67], v[70:71]
	v_pk_add_f32 v[68:69], v[68:69], v[72:73]
	s_waitcnt lgkmcnt(5)
	v_cndmask_b32_e32 v71, v207, v208, vcc
	v_cndmask_b32_e32 v70, v208, v199, vcc
	v_cndmask_b32_e32 v73, v199, v198, vcc
	s_waitcnt lgkmcnt(4)
	v_cndmask_b32_e32 v72, v202, v207, vcc
	v_pk_add_f32 v[68:69], v[68:69], v[72:73]
	v_pk_add_f32 v[66:67], v[66:67], v[70:71]
	v_pk_add_f32 v[106:107], v[106:107], v[68:69]
	v_pk_add_f32 v[104:105], v[104:105], v[66:67]
	v_pk_add_f32 v[66:67], v[140:141], v[142:143]
	v_pk_add_f32 v[68:69], v[138:139], v[132:133]
	v_and_b32_e32 v0, 1, v116
	v_pk_add_f32 v[66:67], v[66:67], v[68:69]
	s_waitcnt lgkmcnt(2)
	v_cndmask_b32_e32 v69, v200, v204, vcc
	v_cndmask_b32_e32 v68, v204, v202, vcc
	v_pk_add_f32 v[66:67], v[66:67], v[68:69]
	v_pk_add_f32 v[68:69], v[122:123], v[136:137]
	v_pk_add_f32 v[102:103], v[102:103], v[66:67]
	v_pk_add_f32 v[66:67], v[124:125], v[126:127]
	v_ashrrev_i32_e32 v117, 31, v116
	v_pk_add_f32 v[66:67], v[66:67], v[68:69]
	v_xor_b32_e32 v68, 1, v171
	v_cmp_lt_i32_e64 s[4:5], v68, v188
	s_waitcnt lgkmcnt(0)
	v_cndmask_b32_e32 v69, v205, v201, vcc
	s_add_u32 s8, s18, s16
	v_cndmask_b32_e64 v68, v171, v68, s[4:5]
	v_cmp_eq_u32_e64 s[4:5], 0, v0
	v_lshlrev_b32_e32 v72, 2, v68
	s_addc_u32 s9, s19, s17
	v_cndmask_b32_e64 v68, v50, v51, s[4:5]
	ds_bpermute_b32 v70, v72, v68
	v_cndmask_b32_e32 v68, v201, v200, vcc
	v_pk_add_f32 v[66:67], v[66:67], v[68:69]
	v_lshlrev_b64 v[68:69], 1, v[116:117]
	v_pk_add_f32 v[118:119], v[118:119], v[66:67]
	v_or_b32_e32 v66, v187, v0
	s_waitcnt lgkmcnt(0)
	v_cndmask_b32_e64 v51, v51, v70, s[4:5]
	v_cndmask_b32_e64 v50, v70, v50, s[4:5]
	v_ashrrev_i32_e32 v67, 31, v66
	v_cvt_pk_bf16_f32 v70, v50, v51
	v_lshlrev_b64 v[50:51], 12, v[66:67]
	v_lshl_add_u64 v[50:51], v[50:51], 0, v[68:69]
	v_lshlrev_b32_e32 v67, 1, v0
	v_sub_co_u32_e64 v50, s[6:7], v50, v67
	v_cndmask_b32_e64 v71, v52, v53, s[4:5]
	s_nop 0
	v_subbrev_co_u32_e64 v51, s[6:7], 0, v51, s[6:7]
	v_lshl_add_u64 v[50:51], s[8:9], 0, v[50:51]
	ds_bpermute_b32 v71, v72, v71
	v_add_co_u32_e64 v50, s[6:7], s33, v50
	s_add_u32 s16, s16, 0x100
	s_nop 0
	v_addc_co_u32_e64 v51, s[6:7], 0, v51, s[6:7]
	global_store_dword v[50:51], v70, off nt
	v_or_b32_e32 v70, v186, v0
	v_cndmask_b32_e64 v0, v54, v55, s[4:5]
	ds_bpermute_b32 v0, v72, v0
	s_waitcnt lgkmcnt(1)
	v_cndmask_b32_e64 v53, v53, v71, s[4:5]
	v_cndmask_b32_e64 v52, v71, v52, s[4:5]
	v_ashrrev_i32_e32 v71, 31, v70
	v_cvt_pk_bf16_f32 v73, v52, v53
	v_lshlrev_b64 v[52:53], 12, v[70:71]
	v_lshl_add_u64 v[52:53], v[52:53], 0, v[68:69]
	v_sub_co_u32_e64 v52, s[6:7], v52, v67
	s_waitcnt lgkmcnt(0)
	v_cndmask_b32_e64 v55, v55, v0, s[4:5]
	v_subbrev_co_u32_e64 v53, s[6:7], 0, v53, s[6:7]
	v_cndmask_b32_e64 v0, v0, v54, s[4:5]
	v_add_u32_e32 v54, 8, v66
	v_lshl_add_u64 v[52:53], s[8:9], 0, v[52:53]
	v_cvt_pk_bf16_f32 v0, v0, v55
	v_ashrrev_i32_e32 v55, 31, v54
	v_add_co_u32_e64 v52, s[6:7], s33, v52
	v_lshlrev_b64 v[54:55], 12, v[54:55]
	s_nop 0
	v_addc_co_u32_e64 v53, s[6:7], 0, v53, s[6:7]
	v_lshl_add_u64 v[54:55], v[54:55], 0, v[68:69]
	v_cndmask_b32_e64 v71, v56, v57, s[4:5]
	v_sub_co_u32_e64 v54, s[6:7], v54, v67
	ds_bpermute_b32 v71, v72, v71
	s_nop 0
	v_subbrev_co_u32_e64 v55, s[6:7], 0, v55, s[6:7]
	v_lshl_add_u64 v[54:55], s[8:9], 0, v[54:55]
	v_add_co_u32_e64 v54, s[6:7], s33, v54
	global_store_dword v[52:53], v73, off nt
	s_nop 0
	v_addc_co_u32_e64 v55, s[6:7], 0, v55, s[6:7]
	global_store_dword v[54:55], v0, off nt
	s_waitcnt lgkmcnt(0)
	v_cndmask_b32_e64 v0, v57, v71, s[4:5]
	v_cndmask_b32_e64 v56, v71, v56, s[4:5]
	v_cvt_pk_bf16_f32 v0, v56, v0
	v_add_u32_e32 v56, 8, v70
	v_ashrrev_i32_e32 v57, 31, v56
	v_lshlrev_b64 v[56:57], 12, v[56:57]
	v_lshl_add_u64 v[56:57], v[56:57], 0, v[68:69]
	v_cndmask_b32_e64 v71, v58, v59, s[4:5]
	v_sub_co_u32_e64 v56, s[6:7], v56, v67
	ds_bpermute_b32 v71, v72, v71
	s_nop 0
	v_subbrev_co_u32_e64 v57, s[6:7], 0, v57, s[6:7]
	v_lshl_add_u64 v[56:57], s[8:9], 0, v[56:57]
	v_add_co_u32_e64 v56, s[6:7], s33, v56
	s_waitcnt lgkmcnt(0)
	v_cndmask_b32_e64 v58, v71, v58, s[4:5]
	v_addc_co_u32_e64 v57, s[6:7], 0, v57, s[6:7]
	global_store_dword v[56:57], v0, off nt
	v_cndmask_b32_e64 v0, v59, v71, s[4:5]
	v_cvt_pk_bf16_f32 v0, v58, v0
	v_add_u32_e32 v58, 16, v66
	v_ashrrev_i32_e32 v59, 31, v58
	v_lshlrev_b64 v[58:59], 12, v[58:59]
	v_lshl_add_u64 v[58:59], v[58:59], 0, v[68:69]
	v_cndmask_b32_e64 v71, v60, v61, s[4:5]
	v_sub_co_u32_e64 v58, s[6:7], v58, v67
	ds_bpermute_b32 v71, v72, v71
	s_nop 0
	v_subbrev_co_u32_e64 v59, s[6:7], 0, v59, s[6:7]
	v_lshl_add_u64 v[58:59], s[8:9], 0, v[58:59]
	v_add_co_u32_e64 v58, s[6:7], s33, v58
	s_waitcnt lgkmcnt(0)
	v_cndmask_b32_e64 v60, v71, v60, s[4:5]
	v_addc_co_u32_e64 v59, s[6:7], 0, v59, s[6:7]
	global_store_dword v[58:59], v0, off nt
	v_cndmask_b32_e64 v0, v61, v71, s[4:5]
	v_cvt_pk_bf16_f32 v0, v60, v0
	v_add_u32_e32 v60, 16, v70
	v_ashrrev_i32_e32 v61, 31, v60
	v_lshlrev_b64 v[60:61], 12, v[60:61]
	v_lshl_add_u64 v[60:61], v[60:61], 0, v[68:69]
	v_cndmask_b32_e64 v71, v62, v63, s[4:5]
	v_sub_co_u32_e64 v60, s[6:7], v60, v67
	ds_bpermute_b32 v71, v72, v71
	s_nop 0
	v_subbrev_co_u32_e64 v61, s[6:7], 0, v61, s[6:7]
	v_lshl_add_u64 v[60:61], s[8:9], 0, v[60:61]
	v_add_co_u32_e64 v60, s[6:7], s33, v60
	s_waitcnt lgkmcnt(0)
	v_cndmask_b32_e64 v62, v71, v62, s[4:5]
	v_addc_co_u32_e64 v61, s[6:7], 0, v61, s[6:7]
	global_store_dword v[60:61], v0, off nt
	v_cndmask_b32_e64 v0, v63, v71, s[4:5]
	v_cvt_pk_bf16_f32 v0, v62, v0
	v_add_u32_e32 v62, 24, v66
	v_ashrrev_i32_e32 v63, 31, v62
	v_lshlrev_b64 v[62:63], 12, v[62:63]
	v_lshl_add_u64 v[62:63], v[62:63], 0, v[68:69]
	v_cndmask_b32_e64 v66, v64, v65, s[4:5]
	v_sub_co_u32_e64 v62, s[6:7], v62, v67
	ds_bpermute_b32 v66, v72, v66
	s_nop 0
	v_subbrev_co_u32_e64 v63, s[6:7], 0, v63, s[6:7]
	v_lshl_add_u64 v[62:63], s[8:9], 0, v[62:63]
	v_add_co_u32_e64 v62, s[6:7], s33, v62
	s_waitcnt lgkmcnt(0)
	v_cndmask_b32_e64 v64, v66, v64, s[4:5]
	v_addc_co_u32_e64 v63, s[6:7], 0, v63, s[6:7]
	global_store_dword v[62:63], v0, off nt
	v_cndmask_b32_e64 v0, v65, v66, s[4:5]
	v_cvt_pk_bf16_f32 v0, v64, v0
	v_add_u32_e32 v64, 24, v70
	v_ashrrev_i32_e32 v65, 31, v64
	v_lshlrev_b64 v[64:65], 12, v[64:65]
	v_lshl_add_u64 v[64:65], v[64:65], 0, v[68:69]
	v_sub_co_u32_e64 v64, s[6:7], v64, v67
	v_cndmask_b32_e64 v66, v34, v35, s[4:5]
	s_nop 0
	v_subbrev_co_u32_e64 v65, s[6:7], 0, v65, s[6:7]
	v_lshl_add_u64 v[64:65], s[8:9], 0, v[64:65]
	v_add_co_u32_e64 v64, s[6:7], s33, v64
	ds_bpermute_b32 v66, v72, v66
	s_nop 0
	v_addc_co_u32_e64 v65, s[6:7], 0, v65, s[6:7]
	global_store_dword v[64:65], v0, off nt
	v_cndmask_b32_e64 v0, v36, v37, s[4:5]
	ds_bpermute_b32 v0, v72, v0
	s_waitcnt lgkmcnt(1)
	v_cndmask_b32_e64 v35, v35, v66, s[4:5]
	v_cndmask_b32_e64 v34, v66, v34, s[4:5]
	v_cvt_pk_bf16_f32 v34, v34, v35
	global_store_dword v[50:51], v34, off offset:64 nt
	s_waitcnt lgkmcnt(0)
	v_cndmask_b32_e64 v34, v37, v0, s[4:5]
	v_cndmask_b32_e64 v0, v0, v36, s[4:5]
	v_cndmask_b32_e64 v35, v38, v39, s[4:5]
	ds_bpermute_b32 v35, v72, v35
	v_cvt_pk_bf16_f32 v0, v0, v34
	global_store_dword v[52:53], v0, off offset:64 nt
	v_cndmask_b32_e64 v0, v40, v41, s[4:5]
	ds_bpermute_b32 v0, v72, v0
	s_waitcnt lgkmcnt(1)
	v_cndmask_b32_e64 v34, v39, v35, s[4:5]
	v_cndmask_b32_e64 v35, v35, v38, s[4:5]
	v_cvt_pk_bf16_f32 v34, v35, v34
	global_store_dword v[54:55], v34, off offset:64 nt
	s_waitcnt lgkmcnt(0)
	v_cndmask_b32_e64 v34, v41, v0, s[4:5]
	v_cndmask_b32_e64 v0, v0, v40, s[4:5]
	v_cndmask_b32_e64 v35, v42, v43, s[4:5]
	ds_bpermute_b32 v35, v72, v35
	v_cvt_pk_bf16_f32 v0, v0, v34
	global_store_dword v[56:57], v0, off offset:64 nt
	v_cndmask_b32_e64 v0, v44, v45, s[4:5]
	ds_bpermute_b32 v0, v72, v0
	s_waitcnt lgkmcnt(1)
	v_cndmask_b32_e64 v34, v43, v35, s[4:5]
	v_cndmask_b32_e64 v35, v35, v42, s[4:5]
	v_cvt_pk_bf16_f32 v34, v35, v34
	global_store_dword v[58:59], v34, off offset:64 nt
	s_waitcnt lgkmcnt(0)
	v_cndmask_b32_e64 v34, v45, v0, s[4:5]
	v_cndmask_b32_e64 v0, v0, v44, s[4:5]
	v_cndmask_b32_e64 v35, v46, v47, s[4:5]
	ds_bpermute_b32 v35, v72, v35
	v_cvt_pk_bf16_f32 v0, v0, v34
	global_store_dword v[60:61], v0, off offset:64 nt
	v_cndmask_b32_e64 v0, v48, v49, s[4:5]
	ds_bpermute_b32 v0, v72, v0
	s_waitcnt lgkmcnt(1)
	v_cndmask_b32_e64 v34, v47, v35, s[4:5]
	v_cndmask_b32_e64 v35, v35, v46, s[4:5]
	v_cvt_pk_bf16_f32 v34, v35, v34
	global_store_dword v[62:63], v34, off offset:64 nt
	s_waitcnt lgkmcnt(0)
	v_cndmask_b32_e64 v34, v49, v0, s[4:5]
	v_cndmask_b32_e64 v0, v0, v48, s[4:5]
	v_cndmask_b32_e64 v35, v18, v19, s[4:5]
	ds_bpermute_b32 v35, v72, v35
	v_cvt_pk_bf16_f32 v0, v0, v34
	global_store_dword v[64:65], v0, off offset:64 nt
	v_cndmask_b32_e64 v0, v20, v21, s[4:5]
	ds_bpermute_b32 v0, v72, v0
	s_waitcnt lgkmcnt(1)
	v_cndmask_b32_e64 v19, v19, v35, s[4:5]
	v_cndmask_b32_e64 v18, v35, v18, s[4:5]
	v_cvt_pk_bf16_f32 v18, v18, v19
	global_store_dword v[50:51], v18, off offset:128 nt
	s_waitcnt lgkmcnt(0)
	v_cndmask_b32_e64 v18, v21, v0, s[4:5]
	v_cndmask_b32_e64 v0, v0, v20, s[4:5]
	v_cndmask_b32_e64 v19, v22, v23, s[4:5]
	ds_bpermute_b32 v19, v72, v19
	v_cvt_pk_bf16_f32 v0, v0, v18
	global_store_dword v[52:53], v0, off offset:128 nt
	v_cndmask_b32_e64 v0, v24, v25, s[4:5]
	ds_bpermute_b32 v0, v72, v0
	s_waitcnt lgkmcnt(1)
	v_cndmask_b32_e64 v18, v23, v19, s[4:5]
	v_cndmask_b32_e64 v19, v19, v22, s[4:5]
	v_cvt_pk_bf16_f32 v18, v19, v18
	global_store_dword v[54:55], v18, off offset:128 nt
	s_waitcnt lgkmcnt(0)
	v_cndmask_b32_e64 v18, v25, v0, s[4:5]
	v_cndmask_b32_e64 v0, v0, v24, s[4:5]
	v_cndmask_b32_e64 v19, v26, v27, s[4:5]
	ds_bpermute_b32 v19, v72, v19
	v_cvt_pk_bf16_f32 v0, v0, v18
	global_store_dword v[56:57], v0, off offset:128 nt
	v_cndmask_b32_e64 v0, v28, v29, s[4:5]
	ds_bpermute_b32 v0, v72, v0
	s_waitcnt lgkmcnt(1)
	v_cndmask_b32_e64 v18, v27, v19, s[4:5]
	v_cndmask_b32_e64 v19, v19, v26, s[4:5]
	v_cvt_pk_bf16_f32 v18, v19, v18
	global_store_dword v[58:59], v18, off offset:128 nt
	s_waitcnt lgkmcnt(0)
	v_cndmask_b32_e64 v18, v29, v0, s[4:5]
	v_cndmask_b32_e64 v0, v0, v28, s[4:5]
	v_cndmask_b32_e64 v19, v30, v31, s[4:5]
	ds_bpermute_b32 v19, v72, v19
	v_cvt_pk_bf16_f32 v0, v0, v18
	global_store_dword v[60:61], v0, off offset:128 nt
	v_cndmask_b32_e64 v0, v32, v33, s[4:5]
	ds_bpermute_b32 v0, v72, v0
	s_waitcnt lgkmcnt(1)
	v_cndmask_b32_e64 v18, v31, v19, s[4:5]
	v_cndmask_b32_e64 v19, v19, v30, s[4:5]
	v_cvt_pk_bf16_f32 v18, v19, v18
	global_store_dword v[62:63], v18, off offset:128 nt
	s_waitcnt lgkmcnt(0)
	v_cndmask_b32_e64 v18, v33, v0, s[4:5]
	v_cndmask_b32_e64 v0, v0, v32, s[4:5]
	v_cndmask_b32_e64 v19, v2, v3, s[4:5]
	ds_bpermute_b32 v19, v72, v19
	v_cvt_pk_bf16_f32 v0, v0, v18
	global_store_dword v[64:65], v0, off offset:128 nt
	v_cndmask_b32_e64 v0, v4, v5, s[4:5]
	ds_bpermute_b32 v0, v72, v0
	s_waitcnt lgkmcnt(1)
	v_cndmask_b32_e64 v3, v3, v19, s[4:5]
	v_cndmask_b32_e64 v2, v19, v2, s[4:5]
	v_cvt_pk_bf16_f32 v2, v2, v3
	global_store_dword v[50:51], v2, off offset:192 nt
	s_waitcnt lgkmcnt(0)
	v_cndmask_b32_e64 v2, v5, v0, s[4:5]
	v_cndmask_b32_e64 v0, v0, v4, s[4:5]
	v_cndmask_b32_e64 v3, v6, v7, s[4:5]
	ds_bpermute_b32 v3, v72, v3
	v_cvt_pk_bf16_f32 v0, v0, v2
	global_store_dword v[52:53], v0, off offset:192 nt
	v_cndmask_b32_e64 v0, v8, v9, s[4:5]
	ds_bpermute_b32 v0, v72, v0
	s_waitcnt lgkmcnt(1)
	v_cndmask_b32_e64 v2, v7, v3, s[4:5]
	v_cndmask_b32_e64 v3, v3, v6, s[4:5]
	v_cvt_pk_bf16_f32 v2, v3, v2
	global_store_dword v[54:55], v2, off offset:192 nt
	s_waitcnt lgkmcnt(0)
	v_cndmask_b32_e64 v2, v9, v0, s[4:5]
	v_cndmask_b32_e64 v0, v0, v8, s[4:5]
	v_cndmask_b32_e64 v3, v10, v11, s[4:5]
	ds_bpermute_b32 v3, v72, v3
	v_cvt_pk_bf16_f32 v0, v0, v2
	global_store_dword v[56:57], v0, off offset:192 nt
	v_cndmask_b32_e64 v0, v12, v13, s[4:5]
	ds_bpermute_b32 v0, v72, v0
	s_waitcnt lgkmcnt(1)
	v_cndmask_b32_e64 v2, v11, v3, s[4:5]
	v_cndmask_b32_e64 v3, v3, v10, s[4:5]
	v_cvt_pk_bf16_f32 v2, v3, v2
	global_store_dword v[58:59], v2, off offset:192 nt
	s_waitcnt lgkmcnt(0)
	v_cndmask_b32_e64 v2, v13, v0, s[4:5]
	v_cndmask_b32_e64 v0, v0, v12, s[4:5]
	v_cndmask_b32_e64 v3, v14, v15, s[4:5]
	ds_bpermute_b32 v3, v72, v3
	v_cvt_pk_bf16_f32 v0, v0, v2
	global_store_dword v[60:61], v0, off offset:192 nt
	v_cndmask_b32_e64 v0, v16, v17, s[4:5]
	ds_bpermute_b32 v0, v72, v0
	s_waitcnt lgkmcnt(1)
	v_cndmask_b32_e64 v2, v15, v3, s[4:5]
	v_cndmask_b32_e64 v3, v3, v14, s[4:5]
	v_cvt_pk_bf16_f32 v2, v3, v2
	global_store_dword v[62:63], v2, off offset:192 nt
	s_waitcnt lgkmcnt(0)
	v_cndmask_b32_e64 v2, v17, v0, s[4:5]
	v_cndmask_b32_e64 v0, v0, v16, s[4:5]
	s_addc_u32 s17, s17, 0
	v_cvt_pk_bf16_f32 v0, v0, v2
	s_cmpk_eq_i32 s16, 0x400
	global_store_dword v[64:65], v0, off offset:192 nt
	s_cbranch_scc1 .LBB0_580

.LBB0_580:
	s_lshr_b32 s4, s20, 6
	v_add_u32_e32 v19, 28, v175
	v_writelane_b32 v255, s3, 33
	v_cmp_lt_i32_e64 s[0:1], s4, v19
	v_add_u32_e32 v2, 30, v175
	v_cmp_eq_u32_e64 s[14:15], 0, v2
	v_writelane_b32 v255, s0, 34
	v_cmp_eq_u32_e64 s[20:21], s4, v2
	s_or_b64 s[14:15], s[14:15], s[20:21]
	v_writelane_b32 v255, s1, 35
	v_cndmask_b32_e64 v0, v118, v172, s[0:1]
	v_cmp_lt_i32_e64 s[0:1], s4, v2
	v_cmp_eq_u32_e64 s[18:19], 0, v19
	v_cmp_eq_u32_e64 s[22:23], s4, v19
	v_writelane_b32 v255, s0, 36
	v_sub_u32_e32 v29, 31, v175
	v_cmp_eq_u32_e64 s[16:17], 0, v182
	v_cndmask_b32_e64 v3, v119, v172, s[0:1]
	v_cndmask_b32_e64 v3, v3, v173, s[14:15]
	ds_bpermute_b32 v18, v183, v3
	s_or_b64 s[14:15], s[18:19], s[22:23]
	v_cndmask_b32_e64 v13, v0, v173, s[14:15]
	v_cmp_lt_i32_e64 s[18:19], v29, v19
	v_writelane_b32 v255, s1, 37
	s_waitcnt lgkmcnt(0)
	v_cmp_eq_f32_e64 s[14:15], v13, v18
	s_and_b64 s[0:1], s[18:19], s[14:15]
	v_writelane_b32 v255, s0, 38
	v_cmp_eq_u32_e64 s[8:9], 0, v181
	v_cmp_eq_u32_e64 s[18:19], s4, v182
	v_writelane_b32 v255, s1, 39
	v_cmp_lt_i32_e64 s[0:1], s4, v180
	v_cmp_eq_u32_e64 s[28:29], s4, v181
	v_cmp_eq_u32_e64 s[36:37], 0, v176
	v_writelane_b32 v255, s0, 40
	v_cmp_eq_u32_e64 s[10:11], 0, v180
	v_cmp_eq_u32_e64 s[34:35], s4, v180
	v_writelane_b32 v255, s1, 41
	v_cndmask_b32_e64 v28, v115, v172, s[0:1]
	v_cmp_lt_i32_e64 s[0:1], s4, v181
	v_cmp_eq_u32_e64 s[92:93], s4, v176
	s_or_b64 s[96:97], s[8:9], s[28:29]
	v_writelane_b32 v255, s0, 42
	s_or_b64 s[16:17], s[16:17], s[18:19]
	v_cmp_lt_i32_e64 s[28:29], s4, v176
	v_writelane_b32 v255, s1, 43
	v_cndmask_b32_e64 v31, v112, v172, s[0:1]
	v_cmp_lt_i32_e64 s[0:1], s4, v182
	v_cmp_eq_u32_e64 s[40:41], 0, v178
	v_cmp_eq_u32_e64 s[84:85], s4, v175
	v_writelane_b32 v255, s0, 44
	v_cmp_eq_u32_e64 s[88:89], s4, v178
	s_or_b64 s[94:95], s[10:11], s[34:35]
	v_cndmask_b32_e64 v32, v113, v172, s[0:1]
	v_cmp_lt_i32_e64 s[34:35], s4, v175
	v_cndmask_b32_e64 v35, v32, v173, s[16:17]
	v_cndmask_b32_e64 v32, v108, v172, s[28:29]
	v_cmp_lt_i32_e64 s[16:17], s4, v178
	s_or_b64 s[36:37], s[36:37], s[92:93]
	v_cmp_eq_u32_e64 s[38:39], 0, v177
	v_cmp_eq_u32_e64 s[90:91], s4, v177
	v_cndmask_b32_e64 v33, v109, v172, s[34:35]
	v_cmp_lt_i32_e64 s[18:19], s4, v177
	v_cndmask_b32_e64 v37, v28, v173, s[94:95]
	v_cndmask_b32_e64 v28, v111, v172, s[16:17]
	s_or_b64 s[40:41], s[40:41], s[88:89]
	v_cndmask_b32_e64 v42, v32, v173, s[36:37]
	s_or_b64 s[36:37], vcc, s[84:85]
	v_cmp_eq_u32_e64 s[12:13], 0, v179
	v_cmp_eq_u32_e64 s[86:87], s4, v179
	v_cmp_lt_i32_e64 s[14:15], s4, v179
	v_cndmask_b32_e64 v34, v31, v173, s[96:97]
	v_cndmask_b32_e64 v31, v110, v172, s[18:19]
	v_cndmask_b32_e64 v40, v28, v173, s[40:41]
	s_or_b64 s[38:39], s[38:39], s[90:91]
	v_cndmask_b32_e64 v28, v33, v173, s[36:37]
	v_cndmask_b32_e64 v0, v114, v172, s[14:15]
	s_or_b64 s[86:87], s[12:13], s[86:87]
	v_cndmask_b32_e64 v39, v31, v173, s[38:39]
	v_cmp_gt_f32_e64 s[36:37], v42, v28
	v_cndmask_b32_e64 v36, v0, v173, s[86:87]
	v_cmp_lt_i32_e64 s[48:49], v29, v175
	v_cndmask_b32_e64 v0, 0, 1, s[36:37]
	v_cmp_gt_f32_e64 s[36:37], v39, v28
	v_writelane_b32 v255, s1, 45
	v_cmp_lt_i32_e64 s[42:43], v29, v176
	v_cndmask_b32_e64 v31, 0, 1, s[36:37]
	v_cmp_gt_f32_e64 s[36:37], v36, v28
	v_add_u32_e32 v21, 20, v175
	v_add_u32_e32 v20, 22, v175
	v_cndmask_b32_e64 v32, 0, 1, s[36:37]
	v_cmp_gt_f32_e64 s[36:37], v34, v28
	v_add_u32_e32 v25, 16, v175
	v_cmp_eq_u32_e64 s[40:41], 0, v20
	v_cndmask_b32_e64 v33, 0, 1, s[36:37]
	v_cmp_gt_f32_e64 s[36:37], v13, v28
	v_add_u32_e32 v23, 18, v175
	v_cmp_eq_u32_e64 s[86:87], s4, v21
	v_cndmask_b32_e64 v41, 0, 1, s[36:37]
	v_cmp_eq_f32_e64 s[36:37], v28, v18
	s_and_b64 s[0:1], s[48:49], s[36:37]
	v_cmp_gt_f32_e64 s[36:37], v40, v28
	v_writelane_b32 v255, s0, 46
	v_cmp_eq_u32_e64 s[48:49], 0, v23
	v_addc_co_u32_e64 v0, s[36:37], v31, v0, s[36:37]
	v_cmp_gt_f32_e64 s[36:37], v37, v28
	v_writelane_b32 v255, s1, 47
	v_cmp_lt_i32_e64 s[0:1], s4, v21
	v_addc_co_u32_e64 v0, s[36:37], v0, v32, s[36:37]
	v_cmp_gt_f32_e64 s[36:37], v35, v28
	v_writelane_b32 v255, s0, 48
	v_cmp_eq_u32_e64 s[88:89], s4, v23
	v_addc_co_u32_e64 v46, s[36:37], v0, v33, s[36:37]
	v_cmp_ge_f32_e64 s[36:37], v28, v42
	v_writelane_b32 v255, s1, 49
	s_or_b64 s[48:49], s[48:49], s[88:89]
	v_cndmask_b32_e64 v0, 0, 1, s[36:37]
	v_cmp_gt_f32_e64 s[36:37], v39, v42
	v_cmp_eq_u32_e64 s[84:85], 0, v25
	v_cmp_eq_u32_e64 s[90:91], s4, v25
	v_cndmask_b32_e64 v31, 0, 1, s[36:37]
	v_cmp_gt_f32_e64 s[36:37], v36, v42
	v_sub_u32_e32 v30, 19, v175
	v_cmp_lt_i32_e64 s[46:47], v30, v176
	v_cndmask_b32_e64 v32, 0, 1, s[36:37]
	v_cmp_gt_f32_e64 s[36:37], v34, v42
	v_add_u32_e32 v24, 24, v175
	v_add_u32_e32 v22, 26, v175
	v_cndmask_b32_e64 v33, 0, 1, s[36:37]
	v_cmp_gt_f32_e64 s[36:37], v13, v42
	v_cmp_lt_i32_e64 s[96:97], s4, v24
	ds_bpermute_b32 v38, v183, v42
	v_cndmask_b32_e64 v44, 0, 1, s[36:37]
	v_cmp_eq_f32_e64 s[36:37], v42, v18
	s_and_b64 s[94:95], s[42:43], s[36:37]
	v_cmp_gt_f32_e64 s[36:37], v40, v42
	v_cmp_eq_u32_e64 s[42:43], s4, v20
	s_or_b64 s[40:41], s[40:41], s[42:43]
	v_addc_co_u32_e64 v0, s[36:37], v31, v0, s[36:37]
	v_cmp_gt_f32_e64 s[36:37], v37, v42
	v_cndmask_b32_e64 v31, v105, v172, s[0:1]
	v_cmp_lt_i32_e64 s[0:1], s4, v20
	v_addc_co_u32_e64 v0, s[36:37], v0, v32, s[36:37]
	v_cmp_gt_f32_e64 s[36:37], v35, v42
	v_writelane_b32 v255, s0, 50
	v_cndmask_b32_e64 v43, v102, v172, s[96:97]
	v_addc_co_u32_e64 v0, s[36:37], v0, v33, s[36:37]
	v_writelane_b32 v255, s1, 51
	v_cndmask_b32_e64 v32, v106, v172, s[0:1]
	v_cmp_lt_i32_e64 s[0:1], s4, v25
	v_cmp_eq_u32_e64 s[36:37], 0, v21
	s_or_b64 s[86:87], s[36:37], s[86:87]
	v_writelane_b32 v255, s0, 52
	v_cndmask_b32_e64 v50, v32, v173, s[40:41]
	v_cndmask_b32_e64 v49, v31, v173, s[86:87]
	v_writelane_b32 v255, s1, 53
	v_cndmask_b32_e64 v32, v107, v172, s[0:1]
	v_cmp_lt_i32_e64 s[0:1], s4, v23
	v_cmp_eq_u32_e64 s[86:87], s4, v24
	v_sub_u32_e32 v15, 1, v175
	v_writelane_b32 v255, s0, 54
	ds_bpermute_b32 v48, v183, v39
	v_cmp_lt_i32_e64 s[82:83], v15, v176
	v_cndmask_b32_e64 v31, v104, v172, s[0:1]
	v_cndmask_b32_e64 v52, v31, v173, s[48:49]
	ds_bpermute_b32 v31, v183, v52
	s_or_b64 s[48:49], s[84:85], s[90:91]
	v_cndmask_b32_e64 v51, v32, v173, s[48:49]
	v_cmp_gt_f32_e64 s[48:49], v51, v42
	v_writelane_b32 v255, s1, 55
	v_cmp_eq_u32_e64 s[84:85], 0, v22
	v_cndmask_b32_e64 v32, 0, 1, s[48:49]
	s_waitcnt lgkmcnt(0)
	v_cmp_eq_f32_e64 s[48:49], v42, v31
	s_and_b64 s[92:93], s[46:47], s[48:49]
	v_cmp_gt_f32_e64 s[46:47], v49, v42
	v_cmp_lt_i32_e64 s[0:1], s4, v22
	v_sub_u32_e32 v27, 3, v175
	v_cndmask_b32_e64 v33, 0, 1, s[46:47]
	v_cmp_gt_f32_e64 s[46:47], v52, v42
	v_writelane_b32 v255, s0, 56
	v_cmp_lt_i32_e64 s[80:81], v27, v176
	v_addc_co_u32_e64 v0, s[46:47], v0, v32, s[46:47]
	v_cmp_gt_f32_e64 s[46:47], v50, v42
	v_cndmask_b32_e64 v32, v103, v172, s[0:1]
	ds_bpermute_b32 v47, v183, v36
	v_addc_co_u32_e64 v0, s[46:47], v0, v33, s[46:47]
	v_cmp_eq_u32_e64 s[46:47], 0, v24
	s_or_b64 s[88:89], s[46:47], s[86:87]
	v_cmp_eq_u32_e64 s[86:87], s4, v22
	s_or_b64 s[84:85], s[84:85], s[86:87]
	v_cndmask_b32_e64 v43, v43, v173, s[88:89]
	v_cndmask_b32_e64 v33, v32, v173, s[84:85]
	ds_bpermute_b32 v32, v183, v28
	v_cmp_gt_f32_e64 s[88:89], v43, v42
	v_sub_u32_e32 v17, 5, v175
	v_sub_u32_e32 v12, 7, v175
	v_cndmask_b32_e64 v45, 0, 1, s[88:89]
	v_cmp_gt_f32_e64 s[88:89], v33, v42
	v_cmp_lt_i32_e64 s[78:79], v17, v176
	v_cmp_lt_i32_e64 s[76:77], v12, v176
	v_addc_co_u32_e64 v0, s[88:89], v0, v45, s[88:89]
	v_cmp_gt_f32_e64 s[88:89], v3, v42
	ds_bpermute_b32 v45, v183, v40
	v_sub_u32_e32 v10, 9, v175
	v_addc_co_u32_e64 v53, s[88:89], v0, v44, s[88:89]
	s_waitcnt lgkmcnt(1)
	v_cmp_eq_f32_e64 s[88:89], v42, v32
	s_and_b64 s[4:5], s[82:83], s[88:89]
	v_cmp_lt_f32_e64 s[82:83], v42, v32
	s_or_b64 s[4:5], s[82:83], s[4:5]
	v_cmp_eq_f32_e64 s[88:89], v42, v38
	v_cndmask_b32_e64 v55, 0, 1, s[4:5]
	s_and_b64 s[4:5], s[80:81], s[88:89]
	v_cmp_lt_f32_e64 s[80:81], v42, v38
	s_or_b64 s[80:81], s[80:81], s[4:5]
	v_cmp_eq_f32_e64 s[88:89], v42, v48
	ds_bpermute_b32 v44, v183, v37
	s_and_b64 s[4:5], s[78:79], s[88:89]
	s_waitcnt lgkmcnt(1)
	v_cmp_eq_f32_e64 s[88:89], v42, v45
	v_addc_co_u32_e64 v0, s[80:81], v53, v55, s[80:81]
	v_cmp_lt_f32_e64 s[78:79], v42, v48
	s_and_b64 s[88:89], s[76:77], s[88:89]
	v_cmp_lt_f32_e64 s[80:81], v42, v45
	v_cmp_lt_i32_e64 s[74:75], v10, v176
	s_or_b64 s[4:5], s[78:79], s[4:5]
	s_or_b64 s[88:89], s[80:81], s[88:89]
	v_cmp_eq_f32_e64 s[80:81], v42, v47
	ds_bpermute_b32 v53, v183, v34
	v_sub_u32_e32 v8, 11, v175
	v_cndmask_b32_e64 v54, 0, 1, s[4:5]
	s_and_b64 s[4:5], s[74:75], s[80:81]
	v_cmp_lt_f32_e64 s[74:75], v42, v47
	v_cmp_lt_i32_e64 s[72:73], v8, v176
	s_or_b64 s[4:5], s[74:75], s[4:5]
	s_waitcnt lgkmcnt(1)
	v_cmp_eq_f32_e64 s[74:75], v42, v44
	ds_bpermute_b32 v59, v183, v35
	v_cndmask_b32_e64 v55, 0, 1, s[4:5]
	s_and_b64 s[4:5], s[72:73], s[74:75]
	v_addc_co_u32_e64 v0, s[74:75], v0, v54, s[88:89]
	v_sub_u32_e32 v6, 13, v175
	v_cmp_lt_f32_e64 s[74:75], v42, v44
	ds_bpermute_b32 v56, v183, v51
	v_cmp_lt_i32_e64 s[70:71], v6, v176
	s_or_b64 s[88:89], s[74:75], s[4:5]
	s_waitcnt lgkmcnt(2)
	v_cmp_eq_f32_e64 s[74:75], v42, v53
	v_sub_u32_e32 v26, 15, v175
	s_and_b64 s[4:5], s[70:71], s[74:75]
	v_cmp_lt_f32_e64 s[70:71], v42, v53
	v_cmp_lt_i32_e64 s[68:69], v26, v176
	s_or_b64 s[4:5], s[70:71], s[4:5]
	s_waitcnt lgkmcnt(1)
	v_cmp_eq_f32_e64 s[70:71], v42, v59
	v_sub_u32_e32 v16, 17, v175
	v_cndmask_b32_e64 v54, 0, 1, s[4:5]
	s_and_b64 s[4:5], s[68:69], s[70:71]
	v_addc_co_u32_e64 v0, s[70:71], v0, v55, s[88:89]
	v_cmp_lt_i32_e64 s[66:67], v16, v176
	v_cmp_lt_f32_e64 s[70:71], v42, v59
	s_waitcnt lgkmcnt(0)
	v_cmp_eq_f32_e64 s[88:89], v42, v56
	ds_bpermute_b32 v55, v183, v43
	s_or_b64 s[70:71], s[70:71], s[4:5]
	s_and_b64 s[4:5], s[66:67], s[88:89]
	v_cmp_lt_f32_e64 s[66:67], v42, v56
	s_or_b64 s[4:5], s[66:67], s[4:5]
	v_addc_co_u32_e64 v0, s[66:67], v0, v54, s[70:71]
	ds_bpermute_b32 v54, v183, v33
	ds_bpermute_b32 v58, v183, v49
	v_sub_u32_e32 v9, 25, v175
	v_cmp_lt_f32_e64 s[66:67], v42, v31
	v_cmp_lt_i32_e64 s[64:65], v9, v176
	s_or_b64 s[70:71], s[66:67], s[92:93]
	s_waitcnt lgkmcnt(2)
	v_cmp_eq_f32_e64 s[66:67], v42, v55
	ds_bpermute_b32 v57, v183, v50
	v_sub_u32_e32 v7, 27, v175
	v_cndmask_b32_e64 v60, 0, 1, s[4:5]
	s_and_b64 s[4:5], s[64:65], s[66:67]
	v_cmp_lt_f32_e64 s[64:65], v42, v55
	v_sub_u32_e32 v14, 21, v175
	v_cmp_lt_i32_e64 s[62:63], v7, v176
	s_or_b64 s[4:5], s[64:65], s[4:5]
	s_waitcnt lgkmcnt(2)
	v_cmp_eq_f32_e64 s[64:65], v42, v54
	v_cmp_lt_i32_e64 s[60:61], v14, v176
	v_cndmask_b32_e64 v61, 0, 1, s[4:5]
	s_and_b64 s[4:5], s[62:63], s[64:65]
	s_waitcnt lgkmcnt(1)
	v_cmp_eq_f32_e64 s[62:63], v42, v58
	v_sub_u32_e32 v11, 23, v175
	s_and_b64 s[6:7], s[60:61], s[62:63]
	v_cmp_lt_f32_e64 s[60:61], v42, v58
	v_cmp_lt_i32_e64 s[58:59], v11, v176
	s_or_b64 s[6:7], s[60:61], s[6:7]
	s_waitcnt lgkmcnt(0)
	v_cmp_eq_f32_e64 s[60:61], v42, v57
	ds_bpermute_b32 v4, v183, v13
	v_cndmask_b32_e64 v62, 0, 1, s[6:7]
	s_and_b64 s[6:7], s[58:59], s[60:61]
	v_addc_co_u32_e64 v0, s[58:59], v0, v60, s[70:71]
	v_cmp_lt_f32_e64 s[58:59], v42, v57
	s_or_b64 s[60:61], s[58:59], s[6:7]
	v_addc_co_u32_e64 v0, s[60:61], v0, v62, s[60:61]
	v_sub_u32_e32 v5, 29, v175
	v_cmp_lt_f32_e64 s[60:61], v42, v54
	v_cmp_lt_i32_e64 s[50:51], v5, v176
	s_or_b64 s[70:71], s[60:61], s[4:5]
	s_waitcnt lgkmcnt(0)
	v_cmp_eq_f32_e64 s[60:61], v42, v4
	s_and_b64 s[4:5], s[50:51], s[60:61]
	v_cmp_lt_f32_e64 s[50:51], v42, v4
	s_or_b64 s[4:5], s[50:51], s[4:5]
	v_addc_co_u32_e64 v61, s[50:51], v0, v61, s[70:71]
	v_cmp_ge_f32_e64 s[70:71], v28, v39
	v_cmp_lt_i32_e64 s[92:93], v29, v177
	v_cndmask_b32_e64 v60, 0, 1, s[4:5]
	v_cndmask_b32_e64 v0, 0, 1, s[70:71]
	v_cmp_ge_f32_e64 s[70:71], v42, v39
	v_cmp_lt_i32_e64 s[72:73], v30, v177
	v_cmp_lt_i32_e64 s[56:57], v15, v177
	v_cndmask_b32_e64 v62, 0, 1, s[70:71]
	v_cmp_gt_f32_e64 s[70:71], v36, v39
	v_cmp_lt_i32_e64 s[54:55], v27, v177
	v_cmp_lt_i32_e64 s[52:53], v17, v177
	v_cndmask_b32_e64 v63, 0, 1, s[70:71]
	v_cmp_gt_f32_e64 s[70:71], v34, v39
	v_cmp_lt_i32_e64 s[86:87], v12, v177
	v_cmp_lt_i32_e64 s[84:85], v10, v177
	v_cndmask_b32_e64 v64, 0, 1, s[70:71]
	v_cmp_gt_f32_e64 s[70:71], v13, v39
	v_cmp_lt_i32_e64 s[82:83], v8, v177
	v_cmp_lt_i32_e64 s[78:79], v6, v177
	v_cndmask_b32_e64 v65, 0, 1, s[70:71]
	v_cmp_eq_f32_e64 s[70:71], v39, v18
	s_and_b64 s[4:5], s[92:93], s[70:71]
	v_cmp_gt_f32_e64 s[70:71], v40, v39
	v_cmp_lt_i32_e64 s[76:77], v26, v177
	v_cmp_lt_i32_e64 s[80:81], v16, v177
	v_addc_co_u32_e64 v0, s[70:71], v62, v0, s[70:71]
	v_cmp_gt_f32_e64 s[70:71], v37, v39
	v_cmp_lt_i32_e64 s[90:91], v9, v177
	v_cmp_lt_i32_e64 s[88:89], v7, v177
	v_addc_co_u32_e64 v0, s[70:71], v0, v63, s[70:71]
	v_cmp_gt_f32_e64 s[70:71], v35, v39
	v_cmp_lt_i32_e64 s[74:75], v14, v177
	v_cmp_lt_i32_e64 s[68:69], v11, v177
	v_addc_co_u32_e64 v0, s[70:71], v0, v64, s[70:71]
	v_cmp_gt_f32_e64 s[70:71], v51, v39
	v_cmp_lt_i32_e64 s[66:67], v5, v177
	v_cmp_lt_i32_e64 s[62:63], v15, v178
	v_cndmask_b32_e64 v62, 0, 1, s[70:71]
	v_cmp_eq_f32_e64 s[70:71], v39, v31
	s_and_b64 s[6:7], s[72:73], s[70:71]
	v_cmp_gt_f32_e64 s[70:71], v49, v39
	v_cmp_lt_i32_e64 s[58:59], v27, v178
	v_cmp_lt_i32_e64 s[64:65], v17, v178
	v_cndmask_b32_e64 v63, 0, 1, s[70:71]
	v_cmp_gt_f32_e64 s[70:71], v52, v39
	v_cmp_lt_i32_e64 s[60:61], v12, v178
	v_cmp_lt_i32_e64 s[72:73], v8, v178
	v_addc_co_u32_e64 v0, s[70:71], v0, v62, s[70:71]
	v_cmp_gt_f32_e64 s[70:71], v50, v39
	v_cmp_lt_i32_e64 s[92:93], v9, v178
	v_cmp_lt_f32_e64 s[50:51], v42, v18
	v_addc_co_u32_e64 v0, s[70:71], v0, v63, s[70:71]
	v_cmp_gt_f32_e64 s[70:71], v43, v39
	s_or_b64 s[12:13], s[50:51], s[94:95]
	v_cmp_lt_i32_e64 s[94:95], v7, v178
	v_cndmask_b32_e64 v62, 0, 1, s[70:71]
	v_cmp_gt_f32_e64 s[70:71], v33, v39
	v_cmp_lt_i32_e64 s[44:45], v30, v175
	v_cmp_lt_i32_e64 s[30:31], v15, v175
	v_addc_co_u32_e64 v0, s[70:71], v0, v62, s[70:71]
	v_cmp_gt_f32_e64 s[70:71], v3, v39
	v_cmp_lt_i32_e64 s[24:25], v27, v175
	v_cmp_lt_i32_e64 s[26:27], v17, v175
	v_addc_co_u32_e64 v0, s[70:71], v0, v65, s[70:71]
	v_cmp_eq_f32_e64 s[70:71], v39, v32
	s_and_b64 s[8:9], s[56:57], s[70:71]
	v_cmp_lt_f32_e64 s[56:57], v39, v32
	s_or_b64 s[8:9], s[56:57], s[8:9]
	v_cmp_eq_f32_e64 s[56:57], v39, v38
	v_cndmask_b32_e64 v62, 0, 1, s[8:9]
	s_and_b64 s[8:9], s[54:55], s[56:57]
	v_cmp_lt_f32_e64 s[54:55], v39, v38
	s_or_b64 s[56:57], s[54:55], s[8:9]
	v_cmp_eq_f32_e64 s[54:55], v39, v48
	s_and_b64 s[8:9], s[52:53], s[54:55]
	v_cmp_lt_f32_e64 s[52:53], v39, v48
	s_or_b64 s[8:9], s[52:53], s[8:9]
	v_cmp_eq_f32_e64 s[52:53], v39, v45
	v_cndmask_b32_e64 v63, 0, 1, s[8:9]
	s_and_b64 s[8:9], s[86:87], s[52:53]
	v_addc_co_u32_e64 v0, s[52:53], v0, v62, s[56:57]
	v_cmp_lt_f32_e64 s[52:53], v39, v45
	v_cmp_eq_f32_e64 s[56:57], v39, v47
	s_or_b64 s[52:53], s[52:53], s[8:9]
	s_and_b64 s[8:9], s[84:85], s[56:57]
	v_cmp_lt_f32_e64 s[56:57], v39, v47
	s_or_b64 s[8:9], s[56:57], s[8:9]
	v_cmp_eq_f32_e64 s[56:57], v39, v44
	v_addc_co_u32_e64 v0, s[52:53], v0, v63, s[52:53]
	v_cndmask_b32_e64 v62, 0, 1, s[8:9]
	s_and_b64 s[8:9], s[82:83], s[56:57]
	v_cmp_lt_f32_e64 s[52:53], v39, v44
	v_cmp_eq_f32_e64 s[56:57], v39, v53
	s_or_b64 s[52:53], s[52:53], s[8:9]
	s_and_b64 s[8:9], s[78:79], s[56:57]
	v_cmp_lt_f32_e64 s[56:57], v39, v53
	s_or_b64 s[8:9], s[56:57], s[8:9]
	v_cmp_eq_f32_e64 s[56:57], v39, v59
	v_addc_co_u32_e64 v0, s[52:53], v0, v62, s[52:53]
	v_cndmask_b32_e64 v63, 0, 1, s[8:9]
	s_and_b64 s[8:9], s[76:77], s[56:57]
	v_cmp_lt_f32_e64 s[52:53], v39, v59
	s_or_b64 s[52:53], s[52:53], s[8:9]
	v_cmp_eq_f32_e64 s[56:57], v39, v56
	s_and_b64 s[8:9], s[80:81], s[56:57]
	v_cmp_lt_f32_e64 s[56:57], v39, v56
	v_addc_co_u32_e64 v0, s[52:53], v0, v63, s[52:53]
	s_or_b64 s[8:9], s[56:57], s[8:9]
	v_cmp_lt_f32_e64 s[52:53], v39, v31
	v_cmp_eq_f32_e64 s[56:57], v39, v55
	s_or_b64 s[52:53], s[52:53], s[6:7]
	s_and_b64 s[6:7], s[90:91], s[56:57]
	v_cmp_lt_f32_e64 s[56:57], v39, v55
	s_or_b64 s[6:7], s[56:57], s[6:7]
	v_cmp_eq_f32_e64 s[56:57], v39, v54
	v_cndmask_b32_e64 v63, 0, 1, s[6:7]
	s_and_b64 s[6:7], s[88:89], s[56:57]
	v_cmp_eq_f32_e64 s[56:57], v39, v58
	v_cndmask_b32_e64 v62, 0, 1, s[8:9]
	s_and_b64 s[8:9], s[74:75], s[56:57]
	v_cmp_lt_f32_e64 s[56:57], v39, v58
	s_or_b64 s[8:9], s[56:57], s[8:9]
	v_cmp_eq_f32_e64 s[56:57], v39, v57
	v_addc_co_u32_e64 v0, s[52:53], v0, v62, s[52:53]
	v_cndmask_b32_e64 v64, 0, 1, s[8:9]
	s_and_b64 s[8:9], s[68:69], s[56:57]
	v_cmp_lt_f32_e64 s[52:53], v39, v57
	s_or_b64 s[52:53], s[52:53], s[8:9]
	v_cmp_ge_f32_e64 s[88:89], v28, v40
	v_addc_co_u32_e64 v0, s[52:53], v0, v64, s[52:53]
	v_cmp_lt_f32_e64 s[52:53], v39, v54
	s_or_b64 s[52:53], s[52:53], s[6:7]
	v_cmp_lt_i32_e64 s[80:81], v29, v178
	v_addc_co_u32_e64 v63, s[52:53], v0, v63, s[52:53]
	v_cndmask_b32_e64 v0, 0, 1, s[88:89]
	v_cmp_ge_f32_e64 s[88:89], v42, v40
	v_cmp_lt_f32_e64 s[52:53], v39, v18
	s_or_b64 s[52:53], s[52:53], s[4:5]
	v_cndmask_b32_e64 v64, 0, 1, s[88:89]
	v_cmp_gt_f32_e64 s[88:89], v36, v40
	v_cmp_eq_f32_e64 s[68:69], v39, v4
	s_and_b64 s[6:7], s[66:67], s[68:69]
	v_cndmask_b32_e64 v65, 0, 1, s[88:89]
	v_cmp_gt_f32_e64 s[88:89], v34, v40
	v_cmp_lt_f32_e64 s[66:67], v39, v4
	v_cmp_lt_i32_e64 s[86:87], v30, v178
	v_cndmask_b32_e64 v66, 0, 1, s[88:89]
	v_cmp_gt_f32_e64 s[88:89], v13, v40
	s_or_b64 s[6:7], s[66:67], s[6:7]
	v_cndmask_b32_e64 v62, 0, 1, s[6:7]
	v_cndmask_b32_e64 v67, 0, 1, s[88:89]
	v_cmp_eq_f32_e64 s[88:89], v40, v18
	s_and_b64 s[4:5], s[80:81], s[88:89]
	v_cmp_ge_f32_e64 s[80:81], v39, v40
	v_cmp_lt_i32_e64 s[70:71], v10, v178
	v_cmp_lt_i32_e64 s[54:55], v6, v178
	v_addc_co_u32_e64 v0, s[80:81], v64, v0, s[80:81]
	v_cmp_gt_f32_e64 s[80:81], v37, v40
	v_cmp_lt_i32_e64 s[84:85], v26, v178
	v_cmp_lt_i32_e64 s[82:83], v16, v178
	v_addc_co_u32_e64 v0, s[80:81], v0, v65, s[80:81]
	v_cmp_gt_f32_e64 s[80:81], v35, v40
	v_cmp_lt_i32_e64 s[76:77], v14, v178
	v_cmp_lt_i32_e64 s[78:79], v11, v178
	v_addc_co_u32_e64 v0, s[80:81], v0, v66, s[80:81]
	v_cmp_gt_f32_e64 s[80:81], v51, v40
	v_cmp_lt_i32_e64 s[74:75], v5, v178
	v_cmp_lt_i32_e64 s[56:57], v15, v179
	v_cndmask_b32_e64 v64, 0, 1, s[80:81]
	v_cmp_eq_f32_e64 s[80:81], v40, v31
	s_and_b64 s[6:7], s[86:87], s[80:81]
	v_cmp_gt_f32_e64 s[80:81], v49, v40
	v_cmp_lt_i32_e64 s[68:69], v27, v179
	v_cmp_lt_i32_e64 s[66:67], v17, v179
	v_cndmask_b32_e64 v65, 0, 1, s[80:81]
	v_cmp_gt_f32_e64 s[80:81], v52, v40
	v_cmp_lt_i32_e64 s[88:89], v6, v179
	v_cmp_lt_i32_e64 s[86:87], v26, v179
	v_addc_co_u32_e64 v0, s[80:81], v0, v64, s[80:81]
	v_cmp_gt_f32_e64 s[80:81], v50, v40
	v_cmp_lt_i32_e64 s[90:91], v16, v179
	v_cmp_lt_i32_e64 s[20:21], v12, v175
	v_addc_co_u32_e64 v0, s[80:81], v0, v65, s[80:81]
	v_cmp_gt_f32_e64 s[80:81], v43, v40
	v_cmp_lt_i32_e64 s[22:23], v10, v175
	v_writelane_b32 v255, s1, 57
	v_cndmask_b32_e64 v64, 0, 1, s[80:81]
	v_cmp_gt_f32_e64 s[80:81], v33, v40
	s_nop 1
	v_addc_co_u32_e64 v0, s[80:81], v0, v64, s[80:81]
	v_cmp_gt_f32_e64 s[80:81], v3, v40
	s_nop 1
	v_addc_co_u32_e64 v0, s[80:81], v0, v67, s[80:81]
	v_cmp_eq_f32_e64 s[80:81], v40, v32
	s_and_b64 s[8:9], s[62:63], s[80:81]
	v_cmp_lt_f32_e64 s[62:63], v40, v32
	s_or_b64 s[8:9], s[62:63], s[8:9]
	v_cmp_eq_f32_e64 s[62:63], v40, v38
	v_cndmask_b32_e64 v64, 0, 1, s[8:9]
	s_and_b64 s[8:9], s[58:59], s[62:63]
	v_cmp_lt_f32_e64 s[58:59], v40, v38
	v_cmp_eq_f32_e64 s[62:63], v40, v48
	s_or_b64 s[58:59], s[58:59], s[8:9]
	s_and_b64 s[8:9], s[64:65], s[62:63]
	v_cmp_lt_f32_e64 s[62:63], v40, v48
	s_or_b64 s[8:9], s[62:63], s[8:9]
	v_cmp_eq_f32_e64 s[62:63], v40, v45
	v_addc_co_u32_e64 v0, s[58:59], v0, v64, s[58:59]
	v_cndmask_b32_e64 v65, 0, 1, s[8:9]
	s_and_b64 s[8:9], s[60:61], s[62:63]
	v_cmp_lt_f32_e64 s[58:59], v40, v45
	v_cmp_eq_f32_e64 s[60:61], v40, v47
	s_or_b64 s[58:59], s[58:59], s[8:9]
	s_and_b64 s[8:9], s[70:71], s[60:61]
	v_cmp_lt_f32_e64 s[60:61], v40, v47
	s_or_b64 s[8:9], s[60:61], s[8:9]
	v_cmp_eq_f32_e64 s[60:61], v40, v44
	v_addc_co_u32_e64 v0, s[58:59], v0, v65, s[58:59]
	v_cndmask_b32_e64 v64, 0, 1, s[8:9]
	s_and_b64 s[8:9], s[72:73], s[60:61]
	v_cmp_lt_f32_e64 s[58:59], v40, v44
	v_cmp_eq_f32_e64 s[60:61], v40, v53
	s_or_b64 s[58:59], s[58:59], s[8:9]
	s_and_b64 s[8:9], s[54:55], s[60:61]
	v_cmp_lt_f32_e64 s[54:55], v40, v53
	s_or_b64 s[8:9], s[54:55], s[8:9]
	v_cmp_eq_f32_e64 s[54:55], v40, v59
	v_cndmask_b32_e64 v65, 0, 1, s[8:9]
	s_and_b64 s[8:9], s[84:85], s[54:55]
	v_addc_co_u32_e64 v0, s[54:55], v0, v64, s[58:59]
	v_cmp_lt_f32_e64 s[54:55], v40, v59
	s_or_b64 s[54:55], s[54:55], s[8:9]
	v_cmp_eq_f32_e64 s[58:59], v40, v56
	s_and_b64 s[8:9], s[82:83], s[58:59]
	v_cmp_lt_f32_e64 s[58:59], v40, v56
	v_addc_co_u32_e64 v0, s[54:55], v0, v65, s[54:55]
	s_or_b64 s[8:9], s[58:59], s[8:9]
	v_cmp_lt_f32_e64 s[54:55], v40, v31
	v_cmp_eq_f32_e64 s[58:59], v40, v55
	s_or_b64 s[54:55], s[54:55], s[6:7]
	s_and_b64 s[6:7], s[92:93], s[58:59]
	v_cmp_lt_f32_e64 s[58:59], v40, v55
	s_or_b64 s[6:7], s[58:59], s[6:7]
	v_cmp_eq_f32_e64 s[58:59], v40, v54
	v_cndmask_b32_e64 v65, 0, 1, s[6:7]
	s_and_b64 s[6:7], s[94:95], s[58:59]
	v_cmp_eq_f32_e64 s[58:59], v40, v58
	v_cndmask_b32_e64 v64, 0, 1, s[8:9]
	s_and_b64 s[8:9], s[76:77], s[58:59]
	v_cmp_lt_f32_e64 s[58:59], v40, v58
	s_or_b64 s[8:9], s[58:59], s[8:9]
	v_cmp_eq_f32_e64 s[58:59], v40, v57
	v_addc_co_u32_e64 v0, s[54:55], v0, v64, s[54:55]
	v_cndmask_b32_e64 v66, 0, 1, s[8:9]
	s_and_b64 s[8:9], s[78:79], s[58:59]
	v_cmp_lt_f32_e64 s[54:55], v40, v57
	s_or_b64 s[54:55], s[54:55], s[8:9]
	v_cmp_eq_f32_e64 s[58:59], v40, v4
	v_addc_co_u32_e64 v0, s[54:55], v0, v66, s[54:55]
	v_cmp_lt_f32_e64 s[54:55], v40, v54
	s_or_b64 s[54:55], s[54:55], s[6:7]
	s_and_b64 s[6:7], s[74:75], s[58:59]
	v_cmp_ge_f32_e64 s[74:75], v28, v36
	v_addc_co_u32_e64 v65, s[54:55], v0, v65, s[54:55]
	s_nop 0
	v_cndmask_b32_e64 v0, 0, 1, s[74:75]
	v_cmp_ge_f32_e64 s[74:75], v42, v36
	v_cmp_lt_i32_e64 s[78:79], v29, v179
	v_cmp_lt_f32_e64 s[54:55], v40, v18
	v_cndmask_b32_e64 v66, 0, 1, s[74:75]
	v_cmp_ge_f32_e64 s[74:75], v40, v36
	s_or_b64 s[54:55], s[54:55], s[4:5]
	v_cmp_lt_f32_e64 s[58:59], v40, v4
	v_cndmask_b32_e64 v67, 0, 1, s[74:75]
	v_cmp_gt_f32_e64 s[74:75], v34, v36
	v_cmp_lt_i32_e64 s[84:85], v30, v179
	s_or_b64 s[6:7], s[58:59], s[6:7]
	v_cndmask_b32_e64 v68, 0, 1, s[74:75]
	v_cmp_gt_f32_e64 s[74:75], v13, v36
	v_cndmask_b32_e64 v64, 0, 1, s[6:7]
	v_cmp_lt_i32_e64 s[80:81], v12, v179
	v_cndmask_b32_e64 v69, 0, 1, s[74:75]
	v_cmp_eq_f32_e64 s[74:75], v36, v18
	s_and_b64 s[4:5], s[78:79], s[74:75]
	v_cmp_ge_f32_e64 s[74:75], v39, v36
	v_cmp_lt_i32_e64 s[64:65], v10, v179
	v_cmp_lt_i32_e64 s[62:63], v8, v179
	v_addc_co_u32_e64 v0, s[74:75], v66, v0, s[74:75]
	v_cmp_gt_f32_e64 s[74:75], v37, v36
	v_cmp_lt_i32_e64 s[92:93], v9, v179
	v_cmp_lt_i32_e64 s[94:95], v7, v179
	v_addc_co_u32_e64 v0, s[74:75], v0, v67, s[74:75]
	v_cmp_gt_f32_e64 s[74:75], v35, v36
	v_cmp_lt_i32_e64 s[72:73], v14, v179
	v_cmp_lt_i32_e64 s[70:71], v11, v179
	v_addc_co_u32_e64 v0, s[74:75], v0, v68, s[74:75]
	v_cmp_gt_f32_e64 s[74:75], v51, v36
	v_cmp_lt_i32_e64 s[76:77], v5, v179
	v_cmp_lt_i32_e64 s[60:61], v15, v180
	v_cndmask_b32_e64 v66, 0, 1, s[74:75]
	v_cmp_eq_f32_e64 s[74:75], v36, v31
	s_and_b64 s[6:7], s[84:85], s[74:75]
	v_cmp_gt_f32_e64 s[74:75], v49, v36
	v_cmp_lt_i32_e64 s[58:59], v27, v180
	v_cmp_lt_i32_e64 s[82:83], v12, v180
	v_cndmask_b32_e64 v67, 0, 1, s[74:75]
	v_cmp_gt_f32_e64 s[74:75], v52, v36
	v_cmp_lt_i32_e64 s[84:85], v8, v180
	v_cmp_lt_i32_e64 s[78:79], v6, v180
	v_addc_co_u32_e64 v0, s[74:75], v0, v66, s[74:75]
	v_cmp_gt_f32_e64 s[74:75], v50, v36
	s_nop 1
	v_addc_co_u32_e64 v0, s[74:75], v0, v67, s[74:75]
	v_cmp_gt_f32_e64 s[74:75], v43, v36
	s_nop 1
	v_cndmask_b32_e64 v66, 0, 1, s[74:75]
	v_cmp_gt_f32_e64 s[74:75], v33, v36
	s_nop 1
	v_addc_co_u32_e64 v0, s[74:75], v0, v66, s[74:75]
	v_cmp_gt_f32_e64 s[74:75], v3, v36
	s_nop 1
	v_addc_co_u32_e64 v0, s[74:75], v0, v69, s[74:75]
	v_cmp_eq_f32_e64 s[74:75], v36, v32
	s_and_b64 s[8:9], s[56:57], s[74:75]
	v_cmp_lt_f32_e64 s[56:57], v36, v32
	s_or_b64 s[8:9], s[56:57], s[8:9]
	v_cmp_eq_f32_e64 s[56:57], v36, v38
	v_cndmask_b32_e64 v66, 0, 1, s[8:9]
	s_and_b64 s[8:9], s[68:69], s[56:57]
	v_cmp_lt_f32_e64 s[56:57], v36, v38
	v_cmp_eq_f32_e64 s[68:69], v36, v48
	s_or_b64 s[56:57], s[56:57], s[8:9]
	s_and_b64 s[8:9], s[66:67], s[68:69]
	v_cmp_lt_f32_e64 s[66:67], v36, v48
	s_or_b64 s[8:9], s[66:67], s[8:9]
	v_cmp_eq_f32_e64 s[66:67], v36, v45
	v_addc_co_u32_e64 v0, s[56:57], v0, v66, s[56:57]
	v_cndmask_b32_e64 v67, 0, 1, s[8:9]
	s_and_b64 s[8:9], s[80:81], s[66:67]
	v_cmp_lt_f32_e64 s[56:57], v36, v45
	v_cmp_eq_f32_e64 s[68:69], v36, v47
	s_or_b64 s[56:57], s[56:57], s[8:9]
	s_and_b64 s[8:9], s[64:65], s[68:69]
	v_cmp_lt_f32_e64 s[64:65], v36, v47
	s_or_b64 s[8:9], s[64:65], s[8:9]
	v_cmp_eq_f32_e64 s[64:65], v36, v44
	v_addc_co_u32_e64 v0, s[56:57], v0, v67, s[56:57]
	v_cndmask_b32_e64 v66, 0, 1, s[8:9]
	s_and_b64 s[8:9], s[62:63], s[64:65]
	v_cmp_lt_f32_e64 s[56:57], v36, v44
	v_cmp_eq_f32_e64 s[62:63], v36, v53
	s_or_b64 s[56:57], s[56:57], s[8:9]
	s_and_b64 s[8:9], s[88:89], s[62:63]
	v_cmp_lt_f32_e64 s[62:63], v36, v53
	s_or_b64 s[8:9], s[62:63], s[8:9]
	v_cmp_eq_f32_e64 s[62:63], v36, v59
	v_addc_co_u32_e64 v0, s[56:57], v0, v66, s[56:57]
	v_cndmask_b32_e64 v67, 0, 1, s[8:9]
	s_and_b64 s[8:9], s[86:87], s[62:63]
	v_cmp_lt_f32_e64 s[56:57], v36, v59
	s_or_b64 s[56:57], s[56:57], s[8:9]
	v_cmp_eq_f32_e64 s[62:63], v36, v56
	s_and_b64 s[8:9], s[90:91], s[62:63]
	v_cmp_lt_f32_e64 s[62:63], v36, v56
	v_addc_co_u32_e64 v0, s[56:57], v0, v67, s[56:57]
	s_or_b64 s[8:9], s[62:63], s[8:9]
	v_cmp_lt_f32_e64 s[56:57], v36, v31
	v_cmp_eq_f32_e64 s[62:63], v36, v55
	s_or_b64 s[56:57], s[56:57], s[6:7]
	s_and_b64 s[6:7], s[92:93], s[62:63]
	v_cmp_lt_f32_e64 s[62:63], v36, v55
	s_or_b64 s[6:7], s[62:63], s[6:7]
	v_cmp_eq_f32_e64 s[62:63], v36, v54
	v_cndmask_b32_e64 v67, 0, 1, s[6:7]
	s_and_b64 s[6:7], s[94:95], s[62:63]
	v_cmp_eq_f32_e64 s[62:63], v36, v58
	v_cndmask_b32_e64 v66, 0, 1, s[8:9]
	s_and_b64 s[8:9], s[72:73], s[62:63]
	v_cmp_lt_f32_e64 s[62:63], v36, v58
	s_or_b64 s[8:9], s[62:63], s[8:9]
	v_cmp_eq_f32_e64 s[62:63], v36, v57
	v_addc_co_u32_e64 v0, s[56:57], v0, v66, s[56:57]
	v_cndmask_b32_e64 v68, 0, 1, s[8:9]
	s_and_b64 s[8:9], s[70:71], s[62:63]
	v_cmp_lt_f32_e64 s[56:57], v36, v57
	s_or_b64 s[56:57], s[56:57], s[8:9]
	v_cmp_eq_f32_e64 s[62:63], v36, v4
	v_addc_co_u32_e64 v0, s[56:57], v0, v68, s[56:57]
	v_cmp_lt_f32_e64 s[56:57], v36, v54
	s_or_b64 s[56:57], s[56:57], s[6:7]
	s_and_b64 s[6:7], s[76:77], s[62:63]
	v_cmp_ge_f32_e64 s[76:77], v28, v37
	v_addc_co_u32_e64 v67, s[56:57], v0, v67, s[56:57]
	s_nop 0
	v_cndmask_b32_e64 v0, 0, 1, s[76:77]
	v_cmp_ge_f32_e64 s[76:77], v42, v37
	v_cmp_lt_i32_e64 s[72:73], v29, v180
	v_cmp_lt_f32_e64 s[56:57], v36, v18
	v_cndmask_b32_e64 v68, 0, 1, s[76:77]
	v_cmp_ge_f32_e64 s[76:77], v40, v37
	s_or_b64 s[56:57], s[56:57], s[4:5]
	v_cmp_lt_f32_e64 s[62:63], v36, v4
	v_cndmask_b32_e64 v69, 0, 1, s[76:77]
	v_cmp_gt_f32_e64 s[76:77], v34, v37
	v_cmp_lt_i32_e64 s[86:87], v30, v180
	s_or_b64 s[6:7], s[62:63], s[6:7]
	v_cndmask_b32_e64 v70, 0, 1, s[76:77]
	v_cmp_gt_f32_e64 s[76:77], v13, v37
	v_cndmask_b32_e64 v66, 0, 1, s[6:7]
	v_cmp_lt_i32_e64 s[74:75], v17, v180
	v_cndmask_b32_e64 v71, 0, 1, s[76:77]
	v_cmp_eq_f32_e64 s[76:77], v37, v18
	s_and_b64 s[4:5], s[72:73], s[76:77]
	v_cmp_ge_f32_e64 s[72:73], v39, v37
	v_cmp_lt_i32_e64 s[66:67], v10, v180
	v_cmp_lt_i32_e64 s[88:89], v26, v180
	v_addc_co_u32_e64 v0, s[72:73], v68, v0, s[72:73]
	v_cmp_ge_f32_e64 s[72:73], v36, v37
	v_cmp_lt_i32_e64 s[80:81], v16, v180
	v_cmp_lt_i32_e64 s[92:93], v9, v180
	v_addc_co_u32_e64 v0, s[72:73], v0, v69, s[72:73]
	v_cmp_gt_f32_e64 s[72:73], v35, v37
	v_cmp_lt_i32_e64 s[90:91], v7, v180
	v_cmp_lt_i32_e64 s[64:65], v14, v180
	v_addc_co_u32_e64 v0, s[72:73], v0, v70, s[72:73]
	v_cmp_gt_f32_e64 s[72:73], v51, v37
	v_cmp_lt_i32_e64 s[68:69], v11, v180
	v_cmp_lt_i32_e64 s[70:71], v5, v180
	v_cndmask_b32_e64 v68, 0, 1, s[72:73]
	v_cmp_eq_f32_e64 s[72:73], v37, v31
	s_and_b64 s[6:7], s[86:87], s[72:73]
	v_cmp_gt_f32_e64 s[72:73], v49, v37
	v_cmp_lt_i32_e64 s[62:63], v15, v181
	v_cmp_lt_i32_e64 s[86:87], v17, v181
	v_cndmask_b32_e64 v69, 0, 1, s[72:73]
	v_cmp_gt_f32_e64 s[72:73], v52, v37
	v_cmp_lt_i32_e64 s[76:77], v12, v181
	v_cmp_lt_i32_e64 s[94:95], v30, v182
	v_addc_co_u32_e64 v0, s[72:73], v0, v68, s[72:73]
	v_cmp_gt_f32_e64 s[72:73], v50, v37
	s_nop 1
	v_addc_co_u32_e64 v0, s[72:73], v0, v69, s[72:73]
	v_cmp_gt_f32_e64 s[72:73], v43, v37
	s_nop 1
	v_cndmask_b32_e64 v68, 0, 1, s[72:73]
	v_cmp_gt_f32_e64 s[72:73], v33, v37
	s_nop 1
	v_addc_co_u32_e64 v0, s[72:73], v0, v68, s[72:73]
	v_cmp_gt_f32_e64 s[72:73], v3, v37
	s_nop 1
	v_addc_co_u32_e64 v0, s[72:73], v0, v71, s[72:73]
	v_cmp_eq_f32_e64 s[72:73], v37, v32
	s_and_b64 s[8:9], s[60:61], s[72:73]
	v_cmp_lt_f32_e64 s[60:61], v37, v32
	s_or_b64 s[8:9], s[60:61], s[8:9]
	v_cmp_eq_f32_e64 s[60:61], v37, v38
	v_cndmask_b32_e64 v68, 0, 1, s[8:9]
	s_and_b64 s[8:9], s[58:59], s[60:61]
	v_cmp_lt_f32_e64 s[58:59], v37, v38
	v_cmp_eq_f32_e64 s[60:61], v37, v48
	s_or_b64 s[58:59], s[58:59], s[8:9]
	s_and_b64 s[8:9], s[74:75], s[60:61]
	v_cmp_lt_f32_e64 s[60:61], v37, v48
	s_or_b64 s[8:9], s[60:61], s[8:9]
	v_cmp_eq_f32_e64 s[60:61], v37, v45
	v_addc_co_u32_e64 v0, s[58:59], v0, v68, s[58:59]
	v_cndmask_b32_e64 v69, 0, 1, s[8:9]
	s_and_b64 s[8:9], s[82:83], s[60:61]
	v_cmp_lt_f32_e64 s[58:59], v37, v45
	v_cmp_eq_f32_e64 s[60:61], v37, v47
	s_or_b64 s[58:59], s[58:59], s[8:9]
	s_and_b64 s[8:9], s[66:67], s[60:61]
	v_cmp_lt_f32_e64 s[60:61], v37, v47
	s_or_b64 s[8:9], s[60:61], s[8:9]
	v_cmp_eq_f32_e64 s[60:61], v37, v44
	v_addc_co_u32_e64 v0, s[58:59], v0, v69, s[58:59]
	v_cndmask_b32_e64 v68, 0, 1, s[8:9]
	s_and_b64 s[8:9], s[84:85], s[60:61]
	v_cmp_lt_f32_e64 s[58:59], v37, v44
	v_cmp_eq_f32_e64 s[60:61], v37, v53
	s_or_b64 s[58:59], s[58:59], s[8:9]
	s_and_b64 s[8:9], s[78:79], s[60:61]
	v_cmp_lt_f32_e64 s[60:61], v37, v53
	s_or_b64 s[8:9], s[60:61], s[8:9]
	v_cmp_eq_f32_e64 s[60:61], v37, v59
	v_addc_co_u32_e64 v0, s[58:59], v0, v68, s[58:59]
	v_cndmask_b32_e64 v69, 0, 1, s[8:9]
	s_and_b64 s[8:9], s[88:89], s[60:61]
	v_cmp_lt_f32_e64 s[58:59], v37, v59
	s_or_b64 s[58:59], s[58:59], s[8:9]
	v_cmp_eq_f32_e64 s[60:61], v37, v56
	s_and_b64 s[8:9], s[80:81], s[60:61]
	v_cmp_lt_f32_e64 s[60:61], v37, v56
	v_addc_co_u32_e64 v0, s[58:59], v0, v69, s[58:59]
	s_or_b64 s[8:9], s[60:61], s[8:9]
	v_cmp_lt_f32_e64 s[58:59], v37, v31
	v_cmp_eq_f32_e64 s[60:61], v37, v55
	s_or_b64 s[58:59], s[58:59], s[6:7]
	s_and_b64 s[6:7], s[92:93], s[60:61]
	v_cmp_lt_f32_e64 s[60:61], v37, v55
	s_or_b64 s[6:7], s[60:61], s[6:7]
	v_cmp_eq_f32_e64 s[88:89], v37, v54
	v_cndmask_b32_e64 v69, 0, 1, s[6:7]
	s_and_b64 s[6:7], s[90:91], s[88:89]
	v_cmp_eq_f32_e64 s[88:89], v37, v58
	v_cndmask_b32_e64 v68, 0, 1, s[8:9]
	s_and_b64 s[8:9], s[64:65], s[88:89]
	v_cmp_lt_f32_e64 s[64:65], v37, v58
	s_or_b64 s[8:9], s[64:65], s[8:9]
	v_cmp_eq_f32_e64 s[88:89], v37, v57
	v_addc_co_u32_e64 v0, s[58:59], v0, v68, s[58:59]
	v_cndmask_b32_e64 v70, 0, 1, s[8:9]
	s_and_b64 s[8:9], s[68:69], s[88:89]
	v_cmp_lt_f32_e64 s[58:59], v37, v57
	s_or_b64 s[58:59], s[58:59], s[8:9]
	v_cmp_ge_f32_e64 s[92:93], v28, v34
	v_addc_co_u32_e64 v0, s[58:59], v0, v70, s[58:59]
	v_cmp_lt_f32_e64 s[58:59], v37, v54
	s_or_b64 s[58:59], s[58:59], s[6:7]
	v_cmp_eq_f32_e64 s[68:69], v37, v4
	v_addc_co_u32_e64 v69, s[58:59], v0, v69, s[58:59]
	v_cndmask_b32_e64 v0, 0, 1, s[92:93]
	v_cmp_ge_f32_e64 s[92:93], v42, v34
	s_and_b64 s[6:7], s[70:71], s[68:69]
	v_cmp_lt_i32_e64 s[70:71], v29, v181
	v_cndmask_b32_e64 v70, 0, 1, s[92:93]
	v_cmp_ge_f32_e64 s[92:93], v40, v34
	v_cmp_lt_f32_e64 s[58:59], v37, v18
	s_or_b64 s[58:59], s[58:59], s[4:5]
	v_cndmask_b32_e64 v71, 0, 1, s[92:93]
	v_cmp_ge_f32_e64 s[92:93], v37, v34
	v_cmp_lt_f32_e64 s[68:69], v37, v4
	v_cmp_lt_i32_e64 s[84:85], v30, v181
	v_cndmask_b32_e64 v72, 0, 1, s[92:93]
	v_cmp_gt_f32_e64 s[92:93], v13, v34
	s_or_b64 s[6:7], s[68:69], s[6:7]
	v_cndmask_b32_e64 v68, 0, 1, s[6:7]
	v_cndmask_b32_e64 v73, 0, 1, s[92:93]
	v_cmp_eq_f32_e64 s[92:93], v34, v18
	s_and_b64 s[4:5], s[70:71], s[92:93]
	v_cmp_ge_f32_e64 s[70:71], v39, v34
	v_cmp_lt_i32_e64 s[72:73], v27, v181
	v_cmp_lt_i32_e64 s[82:83], v10, v181
	v_addc_co_u32_e64 v0, s[70:71], v70, v0, s[70:71]
	v_cmp_ge_f32_e64 s[70:71], v36, v34
	v_cmp_lt_i32_e64 s[66:67], v8, v181
	v_cmp_lt_i32_e64 s[78:79], v6, v181
	v_addc_co_u32_e64 v0, s[70:71], v0, v71, s[70:71]
	v_cmp_gt_f32_e64 s[70:71], v35, v34
	v_cmp_lt_i32_e64 s[74:75], v26, v181
	v_cmp_lt_i32_e64 s[90:91], v9, v181
	v_addc_co_u32_e64 v0, s[70:71], v0, v72, s[70:71]
	v_cmp_gt_f32_e64 s[70:71], v51, v34
	v_cmp_lt_i32_e64 s[80:81], v16, v181
	v_cmp_lt_i32_e64 s[88:89], v7, v181
	v_cndmask_b32_e64 v70, 0, 1, s[70:71]
	v_cmp_eq_f32_e64 s[70:71], v34, v31
	s_and_b64 s[6:7], s[84:85], s[70:71]
	v_cmp_gt_f32_e64 s[70:71], v49, v34
	v_cmp_lt_i32_e64 s[60:61], v14, v181
	v_cmp_lt_i32_e64 s[64:65], v11, v181
	v_cndmask_b32_e64 v71, 0, 1, s[70:71]
	v_cmp_gt_f32_e64 s[70:71], v52, v34
	v_cmp_lt_i32_e64 s[68:69], v5, v181
	v_cmp_lt_i32_e64 s[84:85], v27, v182
	v_addc_co_u32_e64 v0, s[70:71], v0, v70, s[70:71]
	v_cmp_gt_f32_e64 s[70:71], v50, v34
	s_nop 1
	v_addc_co_u32_e64 v0, s[70:71], v0, v71, s[70:71]
	v_cmp_gt_f32_e64 s[70:71], v43, v34
	s_nop 1
	v_cndmask_b32_e64 v70, 0, 1, s[70:71]
	v_cmp_gt_f32_e64 s[70:71], v33, v34
	s_nop 1
	v_addc_co_u32_e64 v0, s[70:71], v0, v70, s[70:71]
	v_cmp_gt_f32_e64 s[70:71], v3, v34
	s_nop 1
	v_addc_co_u32_e64 v0, s[70:71], v0, v73, s[70:71]
	v_cmp_eq_f32_e64 s[70:71], v34, v32
	s_and_b64 s[8:9], s[62:63], s[70:71]
	v_cmp_lt_f32_e64 s[62:63], v34, v32
	s_or_b64 s[8:9], s[62:63], s[8:9]
	v_cmp_eq_f32_e64 s[62:63], v34, v38
	v_cndmask_b32_e64 v70, 0, 1, s[8:9]
	s_and_b64 s[8:9], s[72:73], s[62:63]
	v_cmp_lt_f32_e64 s[62:63], v34, v38
	v_cmp_eq_f32_e64 s[72:73], v34, v48
	s_or_b64 s[62:63], s[62:63], s[8:9]
	s_and_b64 s[8:9], s[86:87], s[72:73]
	v_cmp_lt_f32_e64 s[72:73], v34, v48
	s_or_b64 s[8:9], s[72:73], s[8:9]
	v_cmp_eq_f32_e64 s[72:73], v34, v45
	v_addc_co_u32_e64 v0, s[62:63], v0, v70, s[62:63]
	v_cndmask_b32_e64 v71, 0, 1, s[8:9]
	s_and_b64 s[8:9], s[76:77], s[72:73]
	v_cmp_lt_f32_e64 s[62:63], v34, v45
	v_cmp_eq_f32_e64 s[72:73], v34, v47
	s_or_b64 s[62:63], s[62:63], s[8:9]
	s_and_b64 s[8:9], s[82:83], s[72:73]
	v_cmp_lt_f32_e64 s[72:73], v34, v47
	s_or_b64 s[8:9], s[72:73], s[8:9]
	v_cmp_eq_f32_e64 s[72:73], v34, v44
	v_addc_co_u32_e64 v0, s[62:63], v0, v71, s[62:63]
	v_cndmask_b32_e64 v70, 0, 1, s[8:9]
	s_and_b64 s[8:9], s[66:67], s[72:73]
	v_cmp_lt_f32_e64 s[62:63], v34, v44
	v_cmp_eq_f32_e64 s[72:73], v34, v53
	s_or_b64 s[62:63], s[62:63], s[8:9]
	s_and_b64 s[8:9], s[78:79], s[72:73]
	v_cmp_lt_f32_e64 s[72:73], v34, v53
	s_or_b64 s[8:9], s[72:73], s[8:9]
	v_cmp_eq_f32_e64 s[72:73], v34, v59
	v_addc_co_u32_e64 v0, s[62:63], v0, v70, s[62:63]
	v_cndmask_b32_e64 v71, 0, 1, s[8:9]
	s_and_b64 s[8:9], s[74:75], s[72:73]
	v_cmp_lt_f32_e64 s[62:63], v34, v59
	s_or_b64 s[62:63], s[62:63], s[8:9]
	v_cmp_eq_f32_e64 s[72:73], v34, v56
	v_addc_co_u32_e64 v0, s[62:63], v0, v71, s[62:63]
	v_cmp_lt_f32_e64 s[62:63], v34, v31
	s_or_b64 s[92:93], s[62:63], s[6:7]
	v_cmp_eq_f32_e64 s[62:63], v34, v55
	s_and_b64 s[6:7], s[90:91], s[62:63]
	v_cmp_lt_f32_e64 s[62:63], v34, v55
	s_and_b64 s[8:9], s[80:81], s[72:73]
	v_cmp_lt_f32_e64 s[72:73], v34, v56
	s_or_b64 s[6:7], s[62:63], s[6:7]
	v_cmp_eq_f32_e64 s[62:63], v34, v54
	s_or_b64 s[8:9], s[72:73], s[8:9]
	v_cndmask_b32_e64 v71, 0, 1, s[6:7]
	s_and_b64 s[6:7], s[88:89], s[62:63]
	v_cmp_eq_f32_e64 s[62:63], v34, v58
	v_cndmask_b32_e64 v70, 0, 1, s[8:9]
	s_and_b64 s[8:9], s[60:61], s[62:63]
	v_cmp_lt_f32_e64 s[60:61], v34, v58
	s_or_b64 s[8:9], s[60:61], s[8:9]
	v_cmp_eq_f32_e64 s[60:61], v34, v57
	v_cndmask_b32_e64 v72, 0, 1, s[8:9]
	s_and_b64 s[8:9], s[64:65], s[60:61]
	v_addc_co_u32_e64 v0, s[60:61], v0, v70, s[92:93]
	v_cmp_lt_f32_e64 s[60:61], v34, v57
	s_or_b64 s[60:61], s[60:61], s[8:9]
	v_cmp_eq_f32_e64 s[64:65], v34, v4
	v_addc_co_u32_e64 v0, s[60:61], v0, v72, s[60:61]
	v_cmp_lt_f32_e64 s[60:61], v34, v54
	s_or_b64 s[60:61], s[60:61], s[6:7]
	s_and_b64 s[6:7], s[68:69], s[64:65]
	v_cmp_ge_f32_e64 s[68:69], v28, v35
	v_addc_co_u32_e64 v71, s[60:61], v0, v71, s[60:61]
	s_nop 0
	v_cndmask_b32_e64 v0, 0, 1, s[68:69]
	v_cmp_ge_f32_e64 s[68:69], v42, v35
	v_cmp_lt_f32_e64 s[64:65], v34, v4
	s_or_b64 s[6:7], s[64:65], s[6:7]
	v_cndmask_b32_e64 v72, 0, 1, s[68:69]
	v_cmp_ge_f32_e64 s[68:69], v40, v35
	v_cmp_lt_i32_e64 s[64:65], v29, v182
	v_cmp_lt_f32_e64 s[60:61], v34, v18
	v_cndmask_b32_e64 v73, 0, 1, s[68:69]
	v_cmp_ge_f32_e64 s[68:69], v37, v35
	s_or_b64 s[50:51], s[60:61], s[4:5]
	v_cndmask_b32_e64 v70, 0, 1, s[6:7]
	v_cndmask_b32_e64 v74, 0, 1, s[68:69]
	v_cmp_gt_f32_e64 s[68:69], v13, v35
	v_cmp_lt_i32_e64 s[70:71], v15, v182
	v_cmp_lt_i32_e64 s[76:77], v17, v182
	v_cndmask_b32_e64 v75, 0, 1, s[68:69]
	v_cmp_eq_f32_e64 s[68:69], v35, v18
	s_and_b64 s[4:5], s[64:65], s[68:69]
	v_cmp_ge_f32_e64 s[64:65], v39, v35
	v_cmp_eq_f32_e64 s[68:69], v35, v48
	v_cmp_lt_i32_e64 s[86:87], v12, v182
	v_addc_co_u32_e64 v0, s[64:65], v72, v0, s[64:65]
	v_cmp_ge_f32_e64 s[64:65], v36, v35
	v_cmp_lt_i32_e64 s[66:67], v10, v182
	v_cmp_lt_i32_e64 s[82:83], v8, v182
	v_addc_co_u32_e64 v0, s[64:65], v0, v73, s[64:65]
	v_cmp_ge_f32_e64 s[64:65], v34, v35
	v_cmp_lt_i32_e64 s[78:79], v6, v182
	v_cmp_lt_i32_e64 s[80:81], v26, v182
	v_addc_co_u32_e64 v0, s[64:65], v0, v74, s[64:65]
	v_cmp_gt_f32_e64 s[64:65], v51, v35
	v_cmp_lt_i32_e64 s[88:89], v9, v182
	v_cmp_lt_i32_e64 s[72:73], v16, v182
	v_cndmask_b32_e64 v72, 0, 1, s[64:65]
	v_cmp_eq_f32_e64 s[64:65], v35, v31
	s_and_b64 s[6:7], s[94:95], s[64:65]
	v_cmp_gt_f32_e64 s[64:65], v49, v35
	v_cmp_lt_i32_e64 s[90:91], v7, v182
	v_cmp_lt_i32_e64 s[74:75], v14, v182
	v_cndmask_b32_e64 v73, 0, 1, s[64:65]
	v_cmp_gt_f32_e64 s[64:65], v52, v35
	v_cmp_lt_i32_e64 s[62:63], v11, v182
	v_cmp_lt_i32_e64 s[92:93], v5, v182
	v_addc_co_u32_e64 v0, s[64:65], v0, v72, s[64:65]
	v_cmp_gt_f32_e64 s[64:65], v50, v35
	v_cmp_lt_i32_e64 s[94:95], v29, v23
	s_nop 0
	v_addc_co_u32_e64 v0, s[64:65], v0, v73, s[64:65]
	v_cmp_gt_f32_e64 s[64:65], v43, v35
	s_nop 1
	v_cndmask_b32_e64 v72, 0, 1, s[64:65]
	v_cmp_gt_f32_e64 s[64:65], v33, v35
	s_nop 1
	v_addc_co_u32_e64 v0, s[64:65], v0, v72, s[64:65]
	v_cmp_gt_f32_e64 s[64:65], v3, v35
	s_nop 1
	v_addc_co_u32_e64 v0, s[64:65], v0, v75, s[64:65]
	v_cmp_eq_f32_e64 s[64:65], v35, v32
	s_and_b64 s[8:9], s[70:71], s[64:65]
	v_cmp_lt_f32_e64 s[64:65], v35, v32
	s_or_b64 s[8:9], s[64:65], s[8:9]
	v_cmp_eq_f32_e64 s[64:65], v35, v38
	v_cndmask_b32_e64 v72, 0, 1, s[8:9]
	s_and_b64 s[8:9], s[84:85], s[64:65]
	v_cmp_lt_f32_e64 s[64:65], v35, v38
	s_or_b64 s[64:65], s[64:65], s[8:9]
	s_and_b64 s[8:9], s[76:77], s[68:69]
	v_cmp_lt_f32_e64 s[68:69], v35, v48
	s_or_b64 s[8:9], s[68:69], s[8:9]
	v_cmp_eq_f32_e64 s[68:69], v35, v45
	v_addc_co_u32_e64 v0, s[64:65], v0, v72, s[64:65]
	v_cndmask_b32_e64 v73, 0, 1, s[8:9]
	s_and_b64 s[8:9], s[86:87], s[68:69]
	v_cmp_lt_f32_e64 s[64:65], v35, v45
	v_cmp_eq_f32_e64 s[70:71], v35, v47
	s_or_b64 s[64:65], s[64:65], s[8:9]
	s_and_b64 s[8:9], s[66:67], s[70:71]
	v_cmp_lt_f32_e64 s[66:67], v35, v47
	s_or_b64 s[8:9], s[66:67], s[8:9]
	v_cmp_eq_f32_e64 s[66:67], v35, v44
	v_addc_co_u32_e64 v0, s[64:65], v0, v73, s[64:65]
	v_cndmask_b32_e64 v72, 0, 1, s[8:9]
	s_and_b64 s[8:9], s[82:83], s[66:67]
	v_cmp_lt_f32_e64 s[64:65], v35, v44
	v_cmp_eq_f32_e64 s[66:67], v35, v53
	s_or_b64 s[64:65], s[64:65], s[8:9]
	s_and_b64 s[8:9], s[78:79], s[66:67]
	v_cmp_lt_f32_e64 s[66:67], v35, v53
	s_or_b64 s[8:9], s[66:67], s[8:9]
	v_cmp_eq_f32_e64 s[66:67], v35, v59
	v_addc_co_u32_e64 v0, s[64:65], v0, v72, s[64:65]
	v_cndmask_b32_e64 v73, 0, 1, s[8:9]
	s_and_b64 s[8:9], s[80:81], s[66:67]
	v_cmp_lt_f32_e64 s[64:65], v35, v59
	s_or_b64 s[78:79], s[64:65], s[8:9]
	v_addc_co_u32_e64 v0, s[78:79], v0, v73, s[78:79]
	v_cmp_lt_f32_e64 s[78:79], v35, v31
	v_cmp_eq_f32_e64 s[80:81], v35, v55
	v_cmp_eq_f32_e64 s[64:65], v35, v56
	s_or_b64 s[78:79], s[78:79], s[6:7]
	s_and_b64 s[6:7], s[88:89], s[80:81]
	v_cmp_lt_f32_e64 s[80:81], v35, v55
	s_and_b64 s[8:9], s[72:73], s[64:65]
	v_cmp_lt_f32_e64 s[64:65], v35, v56
	s_or_b64 s[6:7], s[80:81], s[6:7]
	v_cmp_eq_f32_e64 s[80:81], v35, v54
	s_or_b64 s[8:9], s[64:65], s[8:9]
	v_cndmask_b32_e64 v73, 0, 1, s[6:7]
	s_and_b64 s[6:7], s[90:91], s[80:81]
	v_cmp_eq_f32_e64 s[80:81], v35, v58
	v_cndmask_b32_e64 v72, 0, 1, s[8:9]
	s_and_b64 s[8:9], s[74:75], s[80:81]
	v_cmp_lt_f32_e64 s[74:75], v35, v58
	s_or_b64 s[8:9], s[74:75], s[8:9]
	v_cmp_eq_f32_e64 s[74:75], v35, v57
	v_cndmask_b32_e64 v74, 0, 1, s[8:9]
	s_and_b64 s[8:9], s[62:63], s[74:75]
	v_addc_co_u32_e64 v0, s[62:63], v0, v72, s[78:79]
	v_cmp_lt_f32_e64 s[62:63], v35, v57
	s_or_b64 s[62:63], s[62:63], s[8:9]
	v_cmp_eq_f32_e64 s[74:75], v35, v4
	v_addc_co_u32_e64 v0, s[62:63], v0, v74, s[62:63]
	v_cmp_lt_f32_e64 s[62:63], v35, v54
	s_or_b64 s[62:63], s[62:63], s[6:7]
	s_and_b64 s[6:7], s[92:93], s[74:75]
	v_cmp_ge_f32_e64 s[92:93], v28, v13
	v_addc_co_u32_e64 v73, s[62:63], v0, v73, s[62:63]
	s_nop 0
	v_cndmask_b32_e64 v0, 0, 1, s[92:93]
	v_cmp_ge_f32_e64 s[92:93], v42, v13
	v_cmp_lt_i32_e64 s[90:91], v30, v25
	v_cmp_lt_f32_e64 s[62:63], v35, v18
	v_cndmask_b32_e64 v74, 0, 1, s[92:93]
	v_cmp_ge_f32_e64 s[92:93], v40, v13
	s_or_b64 s[42:43], s[62:63], s[4:5]
	v_cmp_lt_f32_e64 s[74:75], v35, v4
	v_cndmask_b32_e64 v75, 0, 1, s[92:93]
	v_cmp_ge_f32_e64 s[92:93], v37, v13
	v_cmp_lt_i32_e64 s[88:89], v16, v25
	s_or_b64 s[6:7], s[74:75], s[6:7]
	v_cndmask_b32_e64 v76, 0, 1, s[92:93]
	v_cmp_ge_f32_e64 s[92:93], v35, v13
	v_cndmask_b32_e64 v72, 0, 1, s[6:7]
	v_cmp_lt_i32_e64 s[76:77], v15, v25
	v_cndmask_b32_e64 v89, 0, 1, s[92:93]
	v_cmp_ge_f32_e64 s[92:93], v39, v13
	v_cmp_lt_i32_e64 s[68:69], v27, v25
	v_cmp_lt_i32_e64 s[86:87], v17, v25
	v_addc_co_u32_e64 v0, s[92:93], v74, v0, s[92:93]
	v_cmp_ge_f32_e64 s[92:93], v36, v13
	v_cmp_lt_i32_e64 s[84:85], v12, v25
	v_cmp_lt_i32_e64 s[70:71], v10, v25
	v_addc_co_u32_e64 v0, s[92:93], v0, v75, s[92:93]
	v_cmp_ge_f32_e64 s[92:93], v34, v13
	v_cmp_lt_i32_e64 s[66:67], v8, v25
	v_cmp_lt_i32_e64 s[72:73], v6, v25
	v_addc_co_u32_e64 v90, s[92:93], v0, v76, s[92:93]
	v_cmp_ge_f32_e64 s[92:93], v39, v3
	v_cmp_lt_i32_e64 s[64:65], v26, v25
	v_cmp_lt_i32_e64 s[80:81], v14, v25
	v_cndmask_b32_e64 v74, 0, 1, s[92:93]
	v_cmp_ge_f32_e64 s[92:93], v40, v3
	v_cmp_lt_i32_e64 s[78:79], v11, v25
	v_cmp_lt_i32_e64 s[82:83], v9, v25
	v_cndmask_b32_e64 v76, 0, 1, s[92:93]
	v_cmp_ge_f32_e64 s[92:93], v28, v3
	v_cmp_lt_i32_e64 s[74:75], v7, v25
	s_nop 0
	v_cndmask_b32_e64 v77, 0, 1, s[92:93]
	v_cmp_ge_f32_e64 s[92:93], v42, v3
	s_nop 1
	v_cndmask_b32_e64 v78, 0, 1, s[92:93]
	v_cmp_ge_f32_e64 s[92:93], v34, v3
	s_nop 1
	v_cndmask_b32_e64 v79, 0, 1, s[92:93]
	v_cmp_ge_f32_e64 s[92:93], v35, v3
	s_nop 1
	v_cndmask_b32_e64 v81, 0, 1, s[92:93]
	v_cmp_ge_f32_e64 s[92:93], v37, v3
	s_nop 1
	v_cndmask_b32_e64 v82, 0, 1, s[92:93]
	v_cmp_ge_f32_e64 s[92:93], v36, v3
	s_nop 1
	v_cndmask_b32_e64 v83, 0, 1, s[92:93]
	v_cmp_eq_f32_e64 s[92:93], v51, v31
	s_and_b64 s[4:5], s[90:91], s[92:93]
	v_cmp_gt_f32_e64 s[90:91], v49, v51
	s_nop 1
	v_cndmask_b32_e64 v0, 0, 1, s[90:91]
	v_cmp_gt_f32_e64 s[90:91], v13, v51
	s_nop 1
	v_cndmask_b32_e64 v75, 0, 1, s[90:91]
	v_cmp_ge_f32_e64 s[90:91], v28, v51
	s_nop 1
	v_cndmask_b32_e64 v80, 0, 1, s[90:91]
	v_cmp_ge_f32_e64 s[90:91], v42, v51
	s_nop 1
	v_cndmask_b32_e64 v84, 0, 1, s[90:91]
	v_cmp_ge_f32_e64 s[90:91], v40, v51
	s_nop 1
	v_cndmask_b32_e64 v85, 0, 1, s[90:91]
	v_cmp_ge_f32_e64 s[90:91], v37, v51
	s_nop 1
	v_cndmask_b32_e64 v86, 0, 1, s[90:91]
	v_cmp_ge_f32_e64 s[90:91], v35, v51
	s_nop 1
	v_cndmask_b32_e64 v87, 0, 1, s[90:91]
	v_cmp_ge_f32_e64 s[90:91], v39, v51
	s_nop 1
	v_addc_co_u32_e64 v80, s[90:91], v84, v80, s[90:91]
	v_cmp_ge_f32_e64 s[90:91], v36, v51
	s_nop 1
	v_addc_co_u32_e64 v80, s[90:91], v80, v85, s[90:91]
	v_cmp_ge_f32_e64 s[90:91], v34, v51
	s_nop 1
	v_addc_co_u32_e64 v80, s[90:91], v80, v86, s[90:91]
	v_cmp_gt_f32_e64 s[90:91], v52, v51
	s_nop 1
	v_addc_co_u32_e64 v80, s[90:91], v80, v87, s[90:91]
	v_cmp_gt_f32_e64 s[90:91], v50, v51
	s_nop 1
	v_addc_co_u32_e64 v0, s[90:91], v80, v0, s[90:91]
	v_cmp_gt_f32_e64 s[90:91], v43, v51
	s_nop 1
	v_cndmask_b32_e64 v80, 0, 1, s[90:91]
	v_cmp_gt_f32_e64 s[90:91], v33, v51
	s_nop 1
	v_addc_co_u32_e64 v0, s[90:91], v0, v80, s[90:91]
	v_cmp_gt_f32_e64 s[90:91], v3, v51
	s_nop 1
	v_addc_co_u32_e64 v0, s[90:91], v0, v75, s[90:91]
	v_cmp_eq_f32_e64 s[90:91], v51, v56
	s_and_b64 s[6:7], s[88:89], s[90:91]
	v_cmp_lt_f32_e64 s[88:89], v51, v56
	s_or_b64 s[6:7], s[88:89], s[6:7]
	v_cmp_eq_f32_e64 s[90:91], v51, v32
	v_cndmask_b32_e64 v75, 0, 1, s[6:7]
	s_and_b64 s[6:7], s[76:77], s[90:91]
	v_cmp_lt_f32_e64 s[76:77], v51, v32
	s_or_b64 s[6:7], s[76:77], s[6:7]
	v_cmp_eq_f32_e64 s[76:77], v51, v38
	v_cndmask_b32_e64 v80, 0, 1, s[6:7]
	s_and_b64 s[6:7], s[68:69], s[76:77]
	v_cmp_lt_f32_e64 s[68:69], v51, v38
	s_or_b64 s[92:93], s[68:69], s[6:7]
	v_cmp_eq_f32_e64 s[68:69], v51, v48
	s_and_b64 s[6:7], s[86:87], s[68:69]
	v_cmp_lt_f32_e64 s[68:69], v51, v48
	s_or_b64 s[6:7], s[68:69], s[6:7]
	v_cmp_eq_f32_e64 s[68:69], v51, v45
	v_cndmask_b32_e64 v84, 0, 1, s[6:7]
	s_and_b64 s[6:7], s[84:85], s[68:69]
	v_addc_co_u32_e64 v0, s[84:85], v0, v80, s[92:93]
	v_cmp_lt_f32_e64 s[84:85], v51, v45
	s_or_b64 s[92:93], s[84:85], s[6:7]
	v_cmp_eq_f32_e64 s[84:85], v51, v47
	s_and_b64 s[6:7], s[70:71], s[84:85]
	v_cmp_lt_f32_e64 s[70:71], v51, v47
	s_or_b64 s[6:7], s[70:71], s[6:7]
	v_cmp_eq_f32_e64 s[70:71], v51, v44
	v_cndmask_b32_e64 v80, 0, 1, s[6:7]
	s_and_b64 s[6:7], s[66:67], s[70:71]
	v_addc_co_u32_e64 v0, s[66:67], v0, v84, s[92:93]
	v_cmp_lt_f32_e64 s[66:67], v51, v44
	v_cmp_eq_f32_e64 s[70:71], v51, v53
	s_or_b64 s[66:67], s[66:67], s[6:7]
	s_and_b64 s[6:7], s[72:73], s[70:71]
	v_cmp_lt_f32_e64 s[70:71], v51, v53
	s_or_b64 s[6:7], s[70:71], s[6:7]
	v_cmp_eq_f32_e64 s[70:71], v51, v59
	v_cndmask_b32_e64 v84, 0, 1, s[6:7]
	s_and_b64 s[6:7], s[64:65], s[70:71]
	v_addc_co_u32_e64 v0, s[64:65], v0, v80, s[66:67]
	v_cmp_lt_f32_e64 s[64:65], v51, v59
	s_or_b64 s[64:65], s[64:65], s[6:7]
	v_cmp_lt_i32_e64 s[90:91], v29, v25
	v_addc_co_u32_e64 v0, s[64:65], v0, v84, s[64:65]
	v_cmp_lt_f32_e64 s[64:65], v51, v31
	v_cmp_eq_f32_e64 s[92:93], v51, v18
	s_or_b64 s[64:65], s[64:65], s[4:5]
	s_and_b64 s[4:5], s[90:91], s[92:93]
	v_cmp_eq_f32_e64 s[90:91], v51, v58
	s_and_b64 s[6:7], s[80:81], s[90:91]
	v_cmp_lt_f32_e64 s[80:81], v51, v58
	s_or_b64 s[6:7], s[80:81], s[6:7]
	v_cmp_eq_f32_e64 s[90:91], v51, v57
	v_addc_co_u32_e64 v0, s[64:65], v0, v75, s[64:65]
	v_cndmask_b32_e64 v80, 0, 1, s[6:7]
	s_and_b64 s[6:7], s[78:79], s[90:91]
	v_cmp_lt_f32_e64 s[64:65], v51, v57
	v_cmp_eq_f32_e64 s[78:79], v51, v55
	s_or_b64 s[64:65], s[64:65], s[6:7]
	s_and_b64 s[6:7], s[82:83], s[78:79]
	v_cmp_lt_f32_e64 s[78:79], v51, v55
	s_or_b64 s[6:7], s[78:79], s[6:7]
	v_cmp_eq_f32_e64 s[78:79], v51, v54
	v_addc_co_u32_e64 v0, s[64:65], v0, v80, s[64:65]
	v_cndmask_b32_e64 v84, 0, 1, s[6:7]
	s_and_b64 s[6:7], s[74:75], s[78:79]
	v_cmp_lt_f32_e64 s[64:65], v51, v54
	s_or_b64 s[64:65], s[64:65], s[6:7]
	v_cmp_lt_i32_e64 s[88:89], v5, v25
	v_cmp_eq_f32_e64 s[74:75], v51, v4
	v_addc_co_u32_e64 v80, s[64:65], v0, v84, s[64:65]
	v_cmp_lt_i32_e64 s[92:93], v30, v23
	s_and_b64 s[6:7], s[88:89], s[74:75]
	v_cmp_lt_f32_e64 s[64:65], v51, v18
	v_cmp_eq_f32_e64 s[88:89], v52, v31
	s_or_b64 s[40:41], s[64:65], s[4:5]
	s_and_b64 s[4:5], s[92:93], s[88:89]
	v_cmp_gt_f32_e64 s[88:89], v49, v52
	v_cmp_lt_f32_e64 s[74:75], v51, v4
	v_cmp_lt_i32_e64 s[90:91], v16, v23
	v_cndmask_b32_e64 v0, 0, 1, s[88:89]
	v_cmp_gt_f32_e64 s[88:89], v13, v52
	s_or_b64 s[6:7], s[74:75], s[6:7]
	v_cndmask_b32_e64 v75, 0, 1, s[6:7]
	v_cndmask_b32_e64 v84, 0, 1, s[88:89]
	v_cmp_ge_f32_e64 s[88:89], v28, v52
	v_cmp_lt_i32_e64 s[76:77], v15, v23
	v_cmp_lt_i32_e64 s[68:69], v27, v23
	v_cndmask_b32_e64 v85, 0, 1, s[88:89]
	v_cmp_ge_f32_e64 s[88:89], v42, v52
	v_cmp_lt_i32_e64 s[86:87], v17, v23
	v_cmp_lt_i32_e64 s[84:85], v12, v23
	v_cndmask_b32_e64 v86, 0, 1, s[88:89]
	v_cmp_ge_f32_e64 s[88:89], v40, v52
	v_cmp_lt_i32_e64 s[72:73], v10, v23
	v_cmp_lt_i32_e64 s[70:71], v8, v23
	v_cndmask_b32_e64 v87, 0, 1, s[88:89]
	v_cmp_ge_f32_e64 s[88:89], v37, v52
	v_cmp_lt_i32_e64 s[66:67], v6, v23
	v_cmp_lt_i32_e64 s[80:81], v26, v23
	v_cndmask_b32_e64 v88, 0, 1, s[88:89]
	v_cmp_ge_f32_e64 s[88:89], v35, v52
	v_cmp_lt_i32_e64 s[78:79], v14, v23
	v_cmp_lt_i32_e64 s[82:83], v11, v23
	v_cndmask_b32_e64 v91, 0, 1, s[88:89]
	v_cmp_ge_f32_e64 s[88:89], v39, v52
	v_cmp_lt_i32_e64 s[74:75], v9, v23
	v_cmp_lt_i32_e64 s[92:93], v5, v23
	v_addc_co_u32_e64 v85, s[88:89], v86, v85, s[88:89]
	v_cmp_ge_f32_e64 s[88:89], v36, v52
	v_lshlrev_b32_e64 v25, v25, 1
	s_nop 0
	v_addc_co_u32_e64 v85, s[88:89], v85, v87, s[88:89]
	v_cmp_ge_f32_e64 s[88:89], v34, v52
	s_nop 1
	v_addc_co_u32_e64 v85, s[88:89], v85, v88, s[88:89]
	v_cmp_ge_f32_e64 s[88:89], v51, v52
	s_nop 1
	v_addc_co_u32_e64 v85, s[88:89], v85, v91, s[88:89]
	v_cmp_gt_f32_e64 s[88:89], v50, v52
	s_nop 1
	v_addc_co_u32_e64 v0, s[88:89], v85, v0, s[88:89]
	v_cmp_gt_f32_e64 s[88:89], v43, v52
	s_nop 1
	v_cndmask_b32_e64 v85, 0, 1, s[88:89]
	v_cmp_gt_f32_e64 s[88:89], v33, v52
	s_nop 1
	v_addc_co_u32_e64 v0, s[88:89], v0, v85, s[88:89]
	v_cmp_gt_f32_e64 s[88:89], v3, v52
	s_nop 1
	v_addc_co_u32_e64 v0, s[88:89], v0, v84, s[88:89]
	v_cmp_eq_f32_e64 s[88:89], v52, v56
	s_and_b64 s[6:7], s[90:91], s[88:89]
	v_cmp_lt_f32_e64 s[88:89], v52, v56
	s_or_b64 s[6:7], s[88:89], s[6:7]
	v_cmp_eq_f32_e64 s[88:89], v52, v32
	v_cndmask_b32_e64 v84, 0, 1, s[6:7]
	s_and_b64 s[6:7], s[76:77], s[88:89]
	v_cmp_lt_f32_e64 s[76:77], v52, v32
	s_or_b64 s[6:7], s[76:77], s[6:7]
	v_cmp_eq_f32_e64 s[76:77], v52, v38
	v_cndmask_b32_e64 v85, 0, 1, s[6:7]
	s_and_b64 s[6:7], s[68:69], s[76:77]
	v_cmp_lt_f32_e64 s[68:69], v52, v38
	v_cmp_eq_f32_e64 s[76:77], v52, v48
	s_or_b64 s[68:69], s[68:69], s[6:7]
	s_and_b64 s[6:7], s[86:87], s[76:77]
	v_cmp_lt_f32_e64 s[76:77], v52, v48
	s_or_b64 s[6:7], s[76:77], s[6:7]
	v_cmp_eq_f32_e64 s[76:77], v52, v45
	v_addc_co_u32_e64 v0, s[68:69], v0, v85, s[68:69]
	v_cndmask_b32_e64 v86, 0, 1, s[6:7]
	s_and_b64 s[6:7], s[84:85], s[76:77]
	v_cmp_lt_f32_e64 s[68:69], v52, v45
	v_cmp_eq_f32_e64 s[84:85], v52, v47
	s_or_b64 s[68:69], s[68:69], s[6:7]
	s_and_b64 s[6:7], s[72:73], s[84:85]
	v_cmp_lt_f32_e64 s[72:73], v52, v47
	s_or_b64 s[6:7], s[72:73], s[6:7]
	v_cmp_eq_f32_e64 s[72:73], v52, v44
	v_addc_co_u32_e64 v0, s[68:69], v0, v86, s[68:69]
	v_cndmask_b32_e64 v85, 0, 1, s[6:7]
	s_and_b64 s[6:7], s[70:71], s[72:73]
	v_cmp_lt_f32_e64 s[68:69], v52, v44
	v_cmp_eq_f32_e64 s[70:71], v52, v53
	s_or_b64 s[68:69], s[68:69], s[6:7]
	s_and_b64 s[6:7], s[66:67], s[70:71]
	v_cmp_lt_f32_e64 s[66:67], v52, v53
	s_or_b64 s[6:7], s[66:67], s[6:7]
	v_cmp_eq_f32_e64 s[66:67], v52, v59
	v_cndmask_b32_e64 v86, 0, 1, s[6:7]
	s_and_b64 s[6:7], s[80:81], s[66:67]
	v_addc_co_u32_e64 v0, s[66:67], v0, v85, s[68:69]
	v_cmp_lt_f32_e64 s[66:67], v52, v59
	s_or_b64 s[66:67], s[66:67], s[6:7]
	v_cmp_eq_f32_e64 s[72:73], v52, v18
	v_addc_co_u32_e64 v0, s[66:67], v0, v86, s[66:67]
	v_cmp_lt_f32_e64 s[66:67], v52, v31
	s_or_b64 s[66:67], s[66:67], s[4:5]
	s_and_b64 s[4:5], s[94:95], s[72:73]
	v_cmp_eq_f32_e64 s[72:73], v52, v58
	s_and_b64 s[6:7], s[78:79], s[72:73]
	v_cmp_lt_f32_e64 s[72:73], v52, v58
	s_or_b64 s[6:7], s[72:73], s[6:7]
	v_cmp_eq_f32_e64 s[72:73], v52, v57
	v_addc_co_u32_e64 v0, s[66:67], v0, v84, s[66:67]
	v_cndmask_b32_e64 v85, 0, 1, s[6:7]
	s_and_b64 s[6:7], s[82:83], s[72:73]
	v_cmp_lt_f32_e64 s[66:67], v52, v57
	v_cmp_eq_f32_e64 s[80:81], v52, v55
	s_or_b64 s[66:67], s[66:67], s[6:7]
	s_and_b64 s[6:7], s[74:75], s[80:81]
	v_cmp_lt_f32_e64 s[74:75], v52, v55
	v_cmp_lt_i32_e64 s[90:91], v7, v23
	s_or_b64 s[6:7], s[74:75], s[6:7]
	v_cmp_eq_f32_e64 s[74:75], v52, v54
	v_addc_co_u32_e64 v0, s[66:67], v0, v85, s[66:67]
	v_cndmask_b32_e64 v86, 0, 1, s[6:7]
	s_and_b64 s[6:7], s[90:91], s[74:75]
	v_cmp_lt_f32_e64 s[66:67], v52, v54
	s_or_b64 s[66:67], s[66:67], s[6:7]
	v_cmp_eq_f32_e64 s[74:75], v52, v4
	s_and_b64 s[6:7], s[92:93], s[74:75]
	v_addc_co_u32_e64 v85, s[66:67], v0, v86, s[66:67]
	v_cmp_ge_f32_e64 s[92:93], v52, v49
	v_cmp_lt_i32_e64 s[90:91], v30, v21
	v_cmp_lt_f32_e64 s[66:67], v52, v18
	v_cndmask_b32_e64 v0, 0, 1, s[92:93]
	v_cmp_eq_f32_e64 s[92:93], v49, v31
	s_or_b64 s[38:39], s[66:67], s[4:5]
	s_and_b64 s[4:5], s[90:91], s[92:93]
	v_cmp_gt_f32_e64 s[90:91], v13, v49
	v_cmp_lt_f32_e64 s[74:75], v52, v4
	v_cmp_lt_i32_e64 s[82:83], v16, v21
	v_cndmask_b32_e64 v86, 0, 1, s[90:91]
	v_cmp_ge_f32_e64 s[90:91], v28, v49
	s_or_b64 s[6:7], s[74:75], s[6:7]
	v_cndmask_b32_e64 v84, 0, 1, s[6:7]
	v_cndmask_b32_e64 v87, 0, 1, s[90:91]
	v_cmp_ge_f32_e64 s[90:91], v42, v49
	v_cmp_lt_i32_e64 s[76:77], v15, v21
	v_cmp_lt_i32_e64 s[86:87], v27, v21
	v_cndmask_b32_e64 v88, 0, 1, s[90:91]
	v_cmp_ge_f32_e64 s[90:91], v40, v49
	v_cmp_lt_i32_e64 s[84:85], v17, v21
	v_cmp_lt_i32_e64 s[88:89], v12, v21
	v_cndmask_b32_e64 v91, 0, 1, s[90:91]
	v_cmp_ge_f32_e64 s[90:91], v37, v49
	v_cmp_lt_i32_e64 s[70:71], v10, v21
	v_cmp_lt_i32_e64 s[68:69], v8, v21
	v_cndmask_b32_e64 v92, 0, 1, s[90:91]
	v_cmp_ge_f32_e64 s[90:91], v35, v49
	v_cmp_lt_i32_e64 s[78:79], v6, v21
	v_cmp_lt_i32_e64 s[72:73], v26, v21
	v_cndmask_b32_e64 v93, 0, 1, s[90:91]
	v_cmp_ge_f32_e64 s[90:91], v39, v49
	v_cmp_lt_i32_e64 s[94:95], v29, v21
	v_cmp_lt_i32_e64 s[80:81], v14, v21
	v_addc_co_u32_e64 v87, s[90:91], v88, v87, s[90:91]
	v_cmp_ge_f32_e64 s[90:91], v36, v49
	v_cmp_lt_i32_e64 s[74:75], v11, v21
	v_cmp_lt_i32_e64 s[92:93], v5, v21
	v_addc_co_u32_e64 v87, s[90:91], v87, v91, s[90:91]
	v_cmp_ge_f32_e64 s[90:91], v34, v49
	v_lshlrev_b32_e64 v23, v23, 1
	s_nop 0
	v_addc_co_u32_e64 v87, s[90:91], v87, v92, s[90:91]
	v_cmp_ge_f32_e64 s[90:91], v51, v49
	s_nop 1
	v_addc_co_u32_e64 v87, s[90:91], v87, v93, s[90:91]
	v_cmp_gt_f32_e64 s[90:91], v50, v49
	s_nop 1
	v_addc_co_u32_e64 v0, s[90:91], v87, v0, s[90:91]
	v_cmp_gt_f32_e64 s[90:91], v43, v49
	s_nop 1
	v_cndmask_b32_e64 v87, 0, 1, s[90:91]
	v_cmp_gt_f32_e64 s[90:91], v33, v49
	s_nop 1
	v_addc_co_u32_e64 v0, s[90:91], v0, v87, s[90:91]
	v_cmp_gt_f32_e64 s[90:91], v3, v49
	s_nop 1
	v_addc_co_u32_e64 v0, s[90:91], v0, v86, s[90:91]
	v_cmp_eq_f32_e64 s[90:91], v49, v56
	s_and_b64 s[6:7], s[82:83], s[90:91]
	v_cmp_lt_f32_e64 s[82:83], v49, v56
	s_or_b64 s[6:7], s[82:83], s[6:7]
	v_cmp_eq_f32_e64 s[90:91], v49, v32
	v_cndmask_b32_e64 v86, 0, 1, s[6:7]
	s_and_b64 s[6:7], s[76:77], s[90:91]
	v_cmp_lt_f32_e64 s[76:77], v49, v32
	s_or_b64 s[6:7], s[76:77], s[6:7]
	v_cmp_eq_f32_e64 s[76:77], v49, v38
	v_cndmask_b32_e64 v87, 0, 1, s[6:7]
	s_and_b64 s[6:7], s[86:87], s[76:77]
	v_cmp_lt_f32_e64 s[76:77], v49, v38
	v_cmp_eq_f32_e64 s[86:87], v49, v48
	s_or_b64 s[76:77], s[76:77], s[6:7]
	s_and_b64 s[6:7], s[84:85], s[86:87]
	v_cmp_lt_f32_e64 s[84:85], v49, v48
	s_or_b64 s[6:7], s[84:85], s[6:7]
	v_cmp_eq_f32_e64 s[84:85], v49, v45
	v_addc_co_u32_e64 v0, s[76:77], v0, v87, s[76:77]
	v_cndmask_b32_e64 v88, 0, 1, s[6:7]
	s_and_b64 s[6:7], s[88:89], s[84:85]
	v_cmp_lt_f32_e64 s[76:77], v49, v45
	v_cmp_eq_f32_e64 s[84:85], v49, v47
	s_or_b64 s[76:77], s[76:77], s[6:7]
	s_and_b64 s[6:7], s[70:71], s[84:85]
	v_cmp_lt_f32_e64 s[70:71], v49, v47
	s_or_b64 s[6:7], s[70:71], s[6:7]
	v_cmp_eq_f32_e64 s[70:71], v49, v44
	v_cndmask_b32_e64 v87, 0, 1, s[6:7]
	s_and_b64 s[6:7], s[68:69], s[70:71]
	v_addc_co_u32_e64 v0, s[68:69], v0, v88, s[76:77]
	v_cmp_lt_f32_e64 s[68:69], v49, v44
	v_cmp_eq_f32_e64 s[70:71], v49, v53
	s_or_b64 s[68:69], s[68:69], s[6:7]
	s_and_b64 s[6:7], s[78:79], s[70:71]
	v_cmp_lt_f32_e64 s[70:71], v49, v53
	s_or_b64 s[6:7], s[70:71], s[6:7]
	v_cmp_eq_f32_e64 s[70:71], v49, v59
	v_addc_co_u32_e64 v0, s[68:69], v0, v87, s[68:69]
	v_cndmask_b32_e64 v88, 0, 1, s[6:7]
	s_and_b64 s[6:7], s[72:73], s[70:71]
	v_cmp_lt_f32_e64 s[68:69], v49, v59
	s_or_b64 s[68:69], s[68:69], s[6:7]
	v_cmp_eq_f32_e64 s[72:73], v49, v18
	v_addc_co_u32_e64 v0, s[68:69], v0, v88, s[68:69]
	v_cmp_lt_f32_e64 s[68:69], v49, v31
	s_or_b64 s[68:69], s[68:69], s[4:5]
	s_and_b64 s[4:5], s[94:95], s[72:73]
	v_cmp_eq_f32_e64 s[72:73], v49, v58
	s_and_b64 s[6:7], s[80:81], s[72:73]
	v_cmp_lt_f32_e64 s[72:73], v49, v58
	s_or_b64 s[6:7], s[72:73], s[6:7]
	v_cmp_eq_f32_e64 s[72:73], v49, v57
	v_addc_co_u32_e64 v0, s[68:69], v0, v86, s[68:69]
	v_cmp_lt_i32_e64 s[82:83], v9, v21
	v_cndmask_b32_e64 v87, 0, 1, s[6:7]
	s_and_b64 s[6:7], s[74:75], s[72:73]
	v_cmp_lt_f32_e64 s[68:69], v49, v57
	v_cmp_eq_f32_e64 s[74:75], v49, v55
	s_or_b64 s[68:69], s[68:69], s[6:7]
	s_and_b64 s[6:7], s[82:83], s[74:75]
	v_cmp_lt_f32_e64 s[74:75], v49, v55
	v_cmp_lt_i32_e64 s[90:91], v7, v21
	s_or_b64 s[6:7], s[74:75], s[6:7]
	v_cmp_eq_f32_e64 s[74:75], v49, v54
	v_addc_co_u32_e64 v0, s[68:69], v0, v87, s[68:69]
	v_cndmask_b32_e64 v88, 0, 1, s[6:7]
	s_and_b64 s[6:7], s[90:91], s[74:75]
	v_cmp_lt_f32_e64 s[68:69], v49, v54
	s_or_b64 s[68:69], s[68:69], s[6:7]
	v_cmp_eq_f32_e64 s[82:83], v49, v4
	s_and_b64 s[6:7], s[92:93], s[82:83]
	v_addc_co_u32_e64 v87, s[68:69], v0, v88, s[68:69]
	v_cmp_ge_f32_e64 s[92:93], v52, v50
	v_cmp_lt_i32_e64 s[90:91], v30, v20
	v_cmp_lt_f32_e64 s[68:69], v49, v18
	v_cndmask_b32_e64 v0, 0, 1, s[92:93]
	v_cmp_eq_f32_e64 s[92:93], v50, v31
	s_or_b64 s[36:37], s[68:69], s[4:5]
	s_and_b64 s[4:5], s[90:91], s[92:93]
	v_cmp_gt_f32_e64 s[90:91], v13, v50
	v_cmp_lt_f32_e64 s[82:83], v49, v4
	v_cmp_lt_i32_e64 s[74:75], v16, v20
	v_cndmask_b32_e64 v88, 0, 1, s[90:91]
	v_cmp_ge_f32_e64 s[90:91], v28, v50
	s_or_b64 s[6:7], s[82:83], s[6:7]
	v_cndmask_b32_e64 v86, 0, 1, s[6:7]
	v_cndmask_b32_e64 v91, 0, 1, s[90:91]
	v_cmp_ge_f32_e64 s[90:91], v42, v50
	v_cmp_lt_i32_e64 s[86:87], v15, v20
	v_cmp_lt_i32_e64 s[84:85], v27, v20
	v_cndmask_b32_e64 v92, 0, 1, s[90:91]
	v_cmp_ge_f32_e64 s[90:91], v40, v50
	v_cmp_lt_i32_e64 s[88:89], v17, v20
	v_cmp_lt_i32_e64 s[78:79], v12, v20
	v_cndmask_b32_e64 v93, 0, 1, s[90:91]
	v_cmp_ge_f32_e64 s[90:91], v37, v50
	v_cmp_lt_i32_e64 s[70:71], v10, v20
	v_cmp_lt_i32_e64 s[76:77], v8, v20
	v_cndmask_b32_e64 v94, 0, 1, s[90:91]
	v_cmp_ge_f32_e64 s[90:91], v35, v50
	v_cmp_lt_i32_e64 s[72:73], v6, v20
	v_cmp_lt_i32_e64 s[80:81], v26, v20
	v_cndmask_b32_e64 v95, 0, 1, s[90:91]
	v_cmp_ge_f32_e64 s[90:91], v39, v50
	v_cmp_lt_i32_e64 s[82:83], v14, v20
	v_lshlrev_b32_e64 v21, v21, 1
	v_addc_co_u32_e64 v91, s[90:91], v92, v91, s[90:91]
	v_cmp_ge_f32_e64 s[90:91], v36, v50
	s_nop 1
	v_addc_co_u32_e64 v91, s[90:91], v91, v93, s[90:91]
	v_cmp_ge_f32_e64 s[90:91], v34, v50
	s_nop 1
	v_addc_co_u32_e64 v91, s[90:91], v91, v94, s[90:91]
	v_cmp_ge_f32_e64 s[90:91], v51, v50
	s_nop 1
	v_addc_co_u32_e64 v91, s[90:91], v91, v95, s[90:91]
	v_cmp_ge_f32_e64 s[90:91], v49, v50
	s_nop 1
	v_addc_co_u32_e64 v0, s[90:91], v91, v0, s[90:91]
	v_cmp_gt_f32_e64 s[90:91], v43, v50
	s_nop 1
	v_cndmask_b32_e64 v91, 0, 1, s[90:91]
	v_cmp_gt_f32_e64 s[90:91], v33, v50
	s_nop 1
	v_addc_co_u32_e64 v0, s[90:91], v0, v91, s[90:91]
	v_cmp_gt_f32_e64 s[90:91], v3, v50
	s_nop 1
	v_addc_co_u32_e64 v0, s[90:91], v0, v88, s[90:91]
	v_cmp_eq_f32_e64 s[90:91], v50, v56
	s_and_b64 s[6:7], s[74:75], s[90:91]
	v_cmp_lt_f32_e64 s[74:75], v50, v56
	s_or_b64 s[6:7], s[74:75], s[6:7]
	v_cmp_eq_f32_e64 s[74:75], v50, v32
	v_cndmask_b32_e64 v88, 0, 1, s[6:7]
	s_and_b64 s[6:7], s[86:87], s[74:75]
	v_cmp_lt_f32_e64 s[74:75], v50, v32
	s_or_b64 s[6:7], s[74:75], s[6:7]
	v_cmp_eq_f32_e64 s[74:75], v50, v38
	v_cndmask_b32_e64 v91, 0, 1, s[6:7]
	s_and_b64 s[6:7], s[84:85], s[74:75]
	v_cmp_lt_f32_e64 s[74:75], v50, v38
	v_cmp_eq_f32_e64 s[84:85], v50, v48
	s_or_b64 s[74:75], s[74:75], s[6:7]
	s_and_b64 s[6:7], s[88:89], s[84:85]
	v_cmp_lt_f32_e64 s[84:85], v50, v48
	s_or_b64 s[6:7], s[84:85], s[6:7]
	v_cmp_eq_f32_e64 s[88:89], v50, v45
	v_addc_co_u32_e64 v0, s[74:75], v0, v91, s[74:75]
	v_cndmask_b32_e64 v92, 0, 1, s[6:7]
	s_and_b64 s[6:7], s[78:79], s[88:89]
	v_cmp_lt_f32_e64 s[74:75], v50, v45
	v_cmp_eq_f32_e64 s[78:79], v50, v47
	s_or_b64 s[74:75], s[74:75], s[6:7]
	s_and_b64 s[6:7], s[70:71], s[78:79]
	v_cmp_lt_f32_e64 s[70:71], v50, v47
	s_or_b64 s[6:7], s[70:71], s[6:7]
	v_cmp_eq_f32_e64 s[78:79], v50, v44
	v_addc_co_u32_e64 v0, s[74:75], v0, v92, s[74:75]
	v_cndmask_b32_e64 v91, 0, 1, s[6:7]
	s_and_b64 s[6:7], s[76:77], s[78:79]
	v_cmp_lt_f32_e64 s[74:75], v50, v44
	s_or_b64 s[76:77], s[74:75], s[6:7]
	v_cmp_eq_f32_e64 s[74:75], v50, v53
	s_and_b64 s[6:7], s[72:73], s[74:75]
	v_cmp_lt_f32_e64 s[72:73], v50, v53
	s_or_b64 s[6:7], s[72:73], s[6:7]
	v_cmp_eq_f32_e64 s[72:73], v50, v59
	v_addc_co_u32_e64 v0, s[76:77], v0, v91, s[76:77]
	v_cndmask_b32_e64 v92, 0, 1, s[6:7]
	s_and_b64 s[6:7], s[80:81], s[72:73]
	v_cmp_lt_f32_e64 s[76:77], v50, v59
	s_or_b64 s[80:81], s[76:77], s[6:7]
	v_addc_co_u32_e64 v0, s[80:81], v0, v92, s[80:81]
	v_cmp_lt_f32_e64 s[80:81], v50, v31
	v_cmp_lt_i32_e64 s[70:71], v29, v20
	s_or_b64 s[92:93], s[80:81], s[4:5]
	v_cmp_eq_f32_e64 s[80:81], v50, v18
	s_and_b64 s[4:5], s[70:71], s[80:81]
	v_cmp_eq_f32_e64 s[70:71], v50, v58
	s_and_b64 s[6:7], s[82:83], s[70:71]
	v_cmp_lt_f32_e64 s[70:71], v50, v58
	v_cmp_lt_i32_e64 s[90:91], v11, v20
	s_or_b64 s[6:7], s[70:71], s[6:7]
	v_cmp_eq_f32_e64 s[70:71], v50, v57
	v_cndmask_b32_e64 v91, 0, 1, s[6:7]
	s_and_b64 s[6:7], s[90:91], s[70:71]
	v_addc_co_u32_e64 v0, s[70:71], v0, v88, s[92:93]
	v_cmp_lt_i32_e64 s[86:87], v9, v20
	v_cmp_lt_f32_e64 s[70:71], v50, v57
	v_cmp_eq_f32_e64 s[90:91], v50, v55
	s_or_b64 s[70:71], s[70:71], s[6:7]
	s_and_b64 s[6:7], s[86:87], s[90:91]
	v_cmp_lt_f32_e64 s[86:87], v50, v55
	v_cmp_lt_i32_e64 s[84:85], v7, v20
	s_or_b64 s[6:7], s[86:87], s[6:7]
	v_cmp_eq_f32_e64 s[90:91], v50, v54
	v_addc_co_u32_e64 v0, s[70:71], v0, v91, s[70:71]
	v_cndmask_b32_e64 v88, 0, 1, s[6:7]
	s_and_b64 s[6:7], s[84:85], s[90:91]
	v_cmp_lt_f32_e64 s[70:71], v50, v54
	v_cmp_lt_i32_e64 s[88:89], v5, v20
	s_or_b64 s[70:71], s[70:71], s[6:7]
	v_cmp_eq_f32_e64 s[90:91], v50, v4
	s_and_b64 s[6:7], s[88:89], s[90:91]
	v_cmp_lt_f32_e64 s[90:91], v50, v18
	v_addc_co_u32_e64 v88, s[70:71], v0, v88, s[70:71]
	s_or_b64 s[70:71], s[90:91], s[4:5]
	v_cmp_ge_f32_e64 s[90:91], v52, v13
	v_cmp_lt_i32_e64 s[84:85], v30, v19
	v_cmp_lt_f32_e64 s[88:89], v50, v4
	v_cndmask_b32_e64 v0, 0, 1, s[90:91]
	v_cmp_eq_f32_e64 s[90:91], v13, v31
	s_and_b64 s[90:91], s[84:85], s[90:91]
	v_cmp_ge_f32_e64 s[84:85], v50, v13
	s_or_b64 s[6:7], s[88:89], s[6:7]
	v_cmp_lt_i32_e64 s[88:89], v30, v2
	v_cndmask_b32_e64 v91, 0, 1, s[84:85]
	v_cmp_gt_f32_e64 s[84:85], v51, v28
	v_cmp_lt_i32_e64 s[82:83], v29, v24
	v_cmp_lt_i32_e64 s[86:87], v29, v22
	v_cndmask_b32_e64 v92, 0, 1, s[84:85]
	v_cmp_eq_f32_e64 s[84:85], v28, v31
	s_and_b64 s[92:93], s[44:45], s[84:85]
	v_cmp_gt_f32_e64 s[44:45], v49, v28
	v_cmp_lt_i32_e64 s[84:85], v29, v2
	v_cmp_lt_i32_e64 s[78:79], v30, v24
	v_cndmask_b32_e64 v93, 0, 1, s[44:45]
	v_cmp_gt_f32_e64 s[44:45], v52, v28
	v_cmp_lt_i32_e64 s[80:81], v30, v22
	v_cmp_lt_i32_e64 s[74:75], v9, v24
	v_addc_co_u32_e64 v46, s[44:45], v46, v92, s[44:45]
	v_cmp_gt_f32_e64 s[44:45], v50, v28
	v_cmp_lt_i32_e64 s[72:73], v7, v24
	v_cmp_lt_i32_e64 s[76:77], v5, v24
	v_addc_co_u32_e64 v46, s[44:45], v46, v93, s[44:45]
	v_cmp_ge_f32_e64 s[44:45], v51, v13
	v_cndmask_b32_e64 v30, 0, 1, s[6:7]
	v_lshlrev_b32_e64 v20, v20, 1
	v_addc_co_u32_e64 v89, s[44:45], v90, v89, s[44:45]
	v_cmp_ge_f32_e64 s[44:45], v49, v13
	s_nop 1
	v_addc_co_u32_e64 v0, s[44:45], v89, v0, s[44:45]
	v_cmp_eq_f32_e64 s[44:45], v3, v31
	s_and_b64 s[88:89], s[88:89], s[44:45]
	v_cmp_ge_f32_e64 s[44:45], v51, v3
	s_nop 1
	v_cndmask_b32_e64 v89, 0, 1, s[44:45]
	v_cmp_ge_f32_e64 s[44:45], v50, v3
	s_nop 1
	v_cndmask_b32_e64 v90, 0, 1, s[44:45]
	v_cmp_ge_f32_e64 s[44:45], v52, v3
	s_nop 1
	v_cndmask_b32_e64 v92, 0, 1, s[44:45]
	v_cmp_ge_f32_e64 s[44:45], v49, v3
	s_nop 1
	v_cndmask_b32_e64 v93, 0, 1, s[44:45]
	v_cmp_eq_f32_e64 s[44:45], v3, v18
	s_and_b64 s[4:5], s[84:85], s[44:45]
	v_cmp_lt_f32_e64 s[44:45], v3, v18
	s_or_b64 s[4:5], s[44:45], s[4:5]
	v_cmp_gt_f32_e64 s[44:45], v13, v43
	s_nop 1
	v_cndmask_b32_e64 v29, 0, 1, s[44:45]
	v_cmp_eq_f32_e64 s[44:45], v43, v18
	s_and_b64 s[84:85], s[82:83], s[44:45]
	v_cmp_gt_f32_e64 s[44:45], v13, v33
	s_nop 1
	v_cndmask_b32_e64 v94, 0, 1, s[44:45]
	v_cmp_eq_f32_e64 s[44:45], v33, v18
	s_and_b64 s[82:83], s[86:87], s[44:45]
	v_cmp_ge_f32_e64 s[44:45], v33, v13
	s_nop 1
	v_cndmask_b32_e64 v95, 0, 1, s[44:45]
	v_cmp_gt_f32_e64 s[44:45], v43, v28
	s_nop 1
	v_cndmask_b32_e64 v96, 0, 1, s[44:45]
	v_cmp_ge_f32_e64 s[44:45], v28, v43
	s_nop 1
	v_cndmask_b32_e64 v97, 0, 1, s[44:45]
	v_cmp_ge_f32_e64 s[44:45], v42, v43
	s_nop 1
	v_cndmask_b32_e64 v102, 0, 1, s[44:45]
	v_cmp_ge_f32_e64 s[44:45], v40, v43
	s_nop 1
	v_cndmask_b32_e64 v103, 0, 1, s[44:45]
	v_cmp_ge_f32_e64 s[44:45], v37, v43
	s_nop 1
	v_cndmask_b32_e64 v104, 0, 1, s[44:45]
	v_cmp_ge_f32_e64 s[44:45], v35, v43
	s_nop 1
	v_cndmask_b32_e64 v105, 0, 1, s[44:45]
	v_cmp_ge_f32_e64 s[44:45], v39, v43
	s_nop 1
	v_addc_co_u32_e64 v97, s[44:45], v102, v97, s[44:45]
	v_cmp_ge_f32_e64 s[44:45], v36, v43
	s_nop 1
	v_addc_co_u32_e64 v97, s[44:45], v97, v103, s[44:45]
	v_cmp_ge_f32_e64 s[44:45], v34, v43
	s_nop 1
	v_addc_co_u32_e64 v97, s[44:45], v97, v104, s[44:45]
	v_cmp_ge_f32_e64 s[44:45], v28, v33
	s_nop 1
	v_cndmask_b32_e64 v102, 0, 1, s[44:45]
	v_cmp_ge_f32_e64 s[44:45], v42, v33
	s_nop 1
	v_cndmask_b32_e64 v42, 0, 1, s[44:45]
	v_cmp_ge_f32_e64 s[44:45], v40, v33
	s_nop 1
	v_cndmask_b32_e64 v40, 0, 1, s[44:45]
	v_cmp_ge_f32_e64 s[44:45], v37, v33
	s_nop 1
	v_cndmask_b32_e64 v37, 0, 1, s[44:45]
	v_cmp_ge_f32_e64 s[44:45], v35, v33
	s_nop 1
	v_cndmask_b32_e64 v35, 0, 1, s[44:45]
	v_cmp_ge_f32_e64 s[44:45], v39, v33
	s_nop 1
	v_addc_co_u32_e64 v39, s[44:45], v42, v102, s[44:45]
	v_cmp_ge_f32_e64 s[44:45], v36, v33
	s_nop 1
	v_addc_co_u32_e64 v36, s[44:45], v39, v40, s[44:45]
	v_cmp_ge_f32_e64 s[44:45], v34, v33
	s_nop 1
	v_addc_co_u32_e64 v34, s[44:45], v36, v37, s[44:45]
	v_cmp_ge_f32_e64 s[44:45], v52, v43
	s_nop 1
	v_cndmask_b32_e64 v36, 0, 1, s[44:45]
	v_cmp_eq_f32_e64 s[44:45], v43, v31
	s_and_b64 s[46:47], s[78:79], s[44:45]
	v_cmp_ge_f32_e64 s[44:45], v50, v43
	v_cmp_ge_f32_e64 s[78:79], v13, v3
	s_nop 0
	v_cndmask_b32_e64 v37, 0, 1, s[44:45]
	v_cmp_ge_f32_e64 s[44:45], v52, v33
	s_nop 1
	v_cndmask_b32_e64 v39, 0, 1, s[44:45]
	v_cmp_eq_f32_e64 s[44:45], v33, v31
	s_and_b64 s[80:81], s[80:81], s[44:45]
	v_cmp_ge_f32_e64 s[44:45], v50, v33
	v_cndmask_b32_e64 v50, 0, 1, s[4:5]
	s_nop 0
	v_cndmask_b32_e64 v40, 0, 1, s[44:45]
	v_cmp_gt_f32_e64 s[44:45], v33, v28
	s_nop 1
	v_addc_co_u32_e64 v42, s[44:45], v46, v96, s[44:45]
	v_cmp_gt_f32_e64 s[44:45], v3, v28
	s_nop 1
	v_addc_co_u32_e64 v42, s[44:45], v42, v41, s[44:45]
	v_cmp_ge_f32_e64 s[44:45], v51, v43
	s_nop 1
	v_addc_co_u32_e64 v41, s[44:45], v97, v105, s[44:45]
	v_cmp_ge_f32_e64 s[44:45], v49, v43
	s_nop 1
	v_addc_co_u32_e64 v36, s[44:45], v41, v36, s[44:45]
	v_cmp_gt_f32_e64 s[44:45], v33, v43
	s_nop 1
	v_addc_co_u32_e64 v36, s[44:45], v36, v37, s[44:45]
	v_cmp_gt_f32_e64 s[44:45], v3, v43
	s_nop 1
	v_addc_co_u32_e64 v46, s[44:45], v36, v29, s[44:45]
	v_cmp_ge_f32_e64 s[44:45], v51, v33
	v_cndmask_b32_e64 v51, 0, 1, s[78:79]
	v_cmp_eq_f32_e64 s[78:79], v43, v55
	v_addc_co_u32_e64 v29, s[44:45], v34, v35, s[44:45]
	v_cmp_ge_f32_e64 s[44:45], v49, v33
	s_and_b64 s[4:5], s[74:75], s[78:79]
	v_cmp_lt_f32_e64 s[74:75], v43, v55
	v_addc_co_u32_e64 v29, s[44:45], v29, v39, s[44:45]
	v_cmp_ge_f32_e64 s[44:45], v43, v33
	v_cmp_eq_f32_e64 s[78:79], v43, v54
	s_or_b64 s[4:5], s[74:75], s[4:5]
	v_addc_co_u32_e64 v29, s[44:45], v29, v40, s[44:45]
	v_cmp_gt_f32_e64 s[44:45], v3, v33
	s_and_b64 s[78:79], s[72:73], s[78:79]
	v_cmp_eq_f32_e64 s[72:73], v43, v4
	v_addc_co_u32_e64 v34, s[44:45], v29, v94, s[44:45]
	v_cmp_ge_f32_e64 s[44:45], v43, v13
	v_cndmask_b32_e64 v40, 0, 1, s[4:5]
	s_and_b64 s[4:5], s[76:77], s[72:73]
	v_addc_co_u32_e64 v0, s[44:45], v0, v91, s[44:45]
	v_cmp_gt_f32_e64 s[44:45], v3, v13
	v_cmp_lt_f32_e64 s[72:73], v43, v4
	s_or_b64 s[4:5], s[72:73], s[4:5]
	v_addc_co_u32_e64 v29, s[44:45], v0, v95, s[44:45]
	v_cmp_ge_f32_e64 s[44:45], v43, v3
	v_cmp_eq_f32_e64 s[76:77], v33, v55
	v_cmp_lt_i32_e64 s[74:75], v7, v22
	v_cndmask_b32_e64 v0, 0, 1, s[44:45]
	v_cmp_ge_f32_e64 s[44:45], v33, v3
	v_cndmask_b32_e64 v41, 0, 1, s[4:5]
	v_cmp_lt_i32_e64 s[72:73], v5, v22
	v_cndmask_b32_e64 v49, 0, 1, s[44:45]
	v_cmp_lt_i32_e64 s[44:45], v9, v22
	s_and_b64 s[4:5], s[44:45], s[76:77]
	v_cmp_lt_f32_e64 s[44:45], v33, v55
	v_cmp_eq_f32_e64 s[76:77], v33, v54
	s_or_b64 s[4:5], s[44:45], s[4:5]
	s_and_b64 s[76:77], s[74:75], s[76:77]
	v_cmp_eq_f32_e64 s[74:75], v33, v4
	v_cndmask_b32_e64 v37, 0, 1, s[4:5]
	s_and_b64 s[4:5], s[72:73], s[74:75]
	v_cmp_lt_f32_e64 s[72:73], v33, v4
	v_cmp_lt_i32_e64 s[44:45], v9, v19
	s_or_b64 s[4:5], s[72:73], s[4:5]
	v_cmp_eq_f32_e64 s[74:75], v13, v55
	v_cmp_lt_i32_e64 s[72:73], v7, v19
	v_cndmask_b32_e64 v39, 0, 1, s[4:5]
	s_and_b64 s[4:5], s[44:45], s[74:75]
	v_cmp_lt_f32_e64 s[44:45], v13, v55
	v_cmp_eq_f32_e64 s[74:75], v13, v54
	s_or_b64 s[4:5], s[44:45], s[4:5]
	v_cmp_lt_i32_e64 s[44:45], v5, v19
	s_and_b64 s[74:75], s[72:73], s[74:75]
	v_cmp_eq_f32_e64 s[72:73], v13, v4
	v_cndmask_b32_e64 v35, 0, 1, s[4:5]
	s_and_b64 s[4:5], s[44:45], s[72:73]
	v_cmp_lt_f32_e64 s[44:45], v13, v4
	s_or_b64 s[4:5], s[44:45], s[4:5]
	v_cmp_eq_f32_e64 s[72:73], v28, v32
	v_cndmask_b32_e64 v36, 0, 1, s[4:5]
	s_and_b64 s[4:5], s[30:31], s[72:73]
	v_cmp_lt_f32_e64 s[30:31], v28, v32
	v_cmp_eq_f32_e64 s[72:73], v28, v38
	s_or_b64 s[4:5], s[30:31], s[4:5]
	s_and_b64 s[10:11], s[24:25], s[72:73]
	v_cmp_eq_f32_e64 s[24:25], v28, v48
	v_cndmask_b32_e64 v52, 0, 1, s[4:5]
	s_and_b64 s[4:5], s[26:27], s[24:25]
	v_cmp_lt_f32_e64 s[24:25], v28, v48
	v_cmp_eq_f32_e64 s[26:27], v28, v45
	s_or_b64 s[4:5], s[24:25], s[4:5]
	s_and_b64 s[8:9], s[20:21], s[26:27]
	v_cmp_eq_f32_e64 s[20:21], v28, v47
	v_cmp_lt_i32_e64 s[44:45], v8, v175
	v_cndmask_b32_e64 v91, 0, 1, s[4:5]
	s_and_b64 s[4:5], s[22:23], s[20:21]
	v_cmp_lt_f32_e64 s[20:21], v28, v47
	v_cmp_eq_f32_e64 s[22:23], v28, v44
	v_cmp_lt_i32_e64 s[30:31], v6, v175
	s_or_b64 s[4:5], s[20:21], s[4:5]
	s_and_b64 s[44:45], s[44:45], s[22:23]
	v_cmp_eq_f32_e64 s[22:23], v28, v53
	v_cmp_lt_i32_e64 s[24:25], v26, v175
	v_cndmask_b32_e64 v94, 0, 1, s[4:5]
	s_and_b64 s[4:5], s[30:31], s[22:23]
	v_cmp_lt_f32_e64 s[22:23], v28, v53
	v_cmp_eq_f32_e64 s[26:27], v28, v59
	v_cmp_lt_i32_e64 s[20:21], v9, v175
	s_or_b64 s[4:5], s[22:23], s[4:5]
	s_and_b64 s[26:27], s[24:25], s[26:27]
	v_cmp_eq_f32_e64 s[24:25], v28, v55
	v_cmp_lt_i32_e64 s[22:23], v7, v175
	v_cndmask_b32_e64 v95, 0, 1, s[4:5]
	s_and_b64 s[4:5], s[20:21], s[24:25]
	v_cmp_lt_f32_e64 s[20:21], v28, v55
	v_cmp_eq_f32_e64 s[24:25], v28, v54
	s_or_b64 s[4:5], s[20:21], s[4:5]
	v_cmp_lt_i32_e64 s[20:21], v5, v175
	s_and_b64 s[30:31], s[22:23], s[24:25]
	v_cmp_eq_f32_e64 s[22:23], v28, v4
	v_cndmask_b32_e64 v96, 0, 1, s[4:5]
	s_and_b64 s[4:5], s[20:21], s[22:23]
	v_cmp_lt_f32_e64 s[20:21], v28, v4
	s_or_b64 s[4:5], s[20:21], s[4:5]
	v_cmp_lt_i32_e64 s[20:21], v15, v24
	v_cmp_eq_f32_e64 s[22:23], v43, v32
	v_cndmask_b32_e64 v97, 0, 1, s[4:5]
	s_and_b64 s[4:5], s[20:21], s[22:23]
	v_cmp_lt_f32_e64 s[20:21], v43, v32
	s_or_b64 s[4:5], s[20:21], s[4:5]
	v_cmp_lt_i32_e64 s[20:21], v27, v24
	v_cmp_eq_f32_e64 s[22:23], v43, v38
	s_and_b64 s[24:25], s[20:21], s[22:23]
	v_cmp_lt_i32_e64 s[20:21], v17, v24
	v_cmp_eq_f32_e64 s[22:23], v43, v48
	v_cndmask_b32_e64 v102, 0, 1, s[4:5]
	s_and_b64 s[4:5], s[20:21], s[22:23]
	v_cmp_lt_f32_e64 s[20:21], v43, v48
	s_or_b64 s[4:5], s[20:21], s[4:5]
	v_cmp_lt_i32_e64 s[20:21], v12, v24
	v_cmp_eq_f32_e64 s[22:23], v43, v45
	s_and_b64 s[48:49], s[20:21], s[22:23]
	v_cmp_lt_i32_e64 s[20:21], v10, v24
	v_cmp_eq_f32_e64 s[22:23], v43, v47
	v_cndmask_b32_e64 v103, 0, 1, s[4:5]
	s_and_b64 s[4:5], s[20:21], s[22:23]
	v_cmp_lt_f32_e64 s[20:21], v43, v47
	s_or_b64 s[4:5], s[20:21], s[4:5]
	v_cmp_lt_i32_e64 s[20:21], v8, v24
	v_cmp_eq_f32_e64 s[22:23], v43, v44
	s_and_b64 s[6:7], s[20:21], s[22:23]
	v_cmp_lt_i32_e64 s[20:21], v6, v24
	v_cmp_eq_f32_e64 s[22:23], v43, v53
	v_cndmask_b32_e64 v104, 0, 1, s[4:5]
	s_and_b64 s[4:5], s[20:21], s[22:23]
	v_cmp_lt_f32_e64 s[20:21], v43, v53
	s_or_b64 s[4:5], s[20:21], s[4:5]
	v_cmp_lt_i32_e64 s[20:21], v26, v24
	v_cmp_eq_f32_e64 s[22:23], v43, v59
	v_cndmask_b32_e64 v105, 0, 1, s[4:5]
	s_and_b64 s[4:5], s[20:21], s[22:23]
	v_cmp_lt_i32_e64 s[20:21], v15, v22
	v_cmp_eq_f32_e64 s[22:23], v33, v32
	s_and_b64 s[22:23], s[20:21], s[22:23]
	v_cmp_lt_f32_e64 s[20:21], v33, v32
	s_or_b64 s[20:21], s[20:21], s[22:23]
	v_cmp_eq_f32_e64 s[22:23], v33, v38
	v_cndmask_b32_e64 v106, 0, 1, s[20:21]
	v_cmp_lt_i32_e64 s[20:21], v27, v22
	s_and_b64 s[72:73], s[20:21], s[22:23]
	v_cmp_lt_i32_e64 s[20:21], v17, v22
	v_cmp_eq_f32_e64 s[22:23], v33, v48
	s_and_b64 s[22:23], s[20:21], s[22:23]
	v_cmp_lt_f32_e64 s[20:21], v33, v48
	s_or_b64 s[20:21], s[20:21], s[22:23]
	v_cmp_eq_f32_e64 s[22:23], v33, v45
	v_cndmask_b32_e64 v107, 0, 1, s[20:21]
	v_cmp_lt_i32_e64 s[20:21], v12, v22
	s_and_b64 s[86:87], s[20:21], s[22:23]
	v_cmp_lt_i32_e64 s[20:21], v10, v22
	v_cmp_eq_f32_e64 s[22:23], v33, v47
	s_and_b64 s[22:23], s[20:21], s[22:23]
	v_cmp_lt_f32_e64 s[20:21], v33, v47
	s_or_b64 s[20:21], s[20:21], s[22:23]
	v_cmp_eq_f32_e64 s[22:23], v33, v44
	v_cndmask_b32_e64 v108, 0, 1, s[20:21]
	v_cmp_lt_i32_e64 s[20:21], v8, v22
	s_and_b64 s[94:95], s[20:21], s[22:23]
	v_cmp_lt_i32_e64 s[20:21], v6, v22
	v_cmp_eq_f32_e64 s[22:23], v33, v53
	s_and_b64 s[22:23], s[20:21], s[22:23]
	v_cmp_lt_f32_e64 s[20:21], v33, v53
	s_or_b64 s[20:21], s[20:21], s[22:23]
	v_cmp_eq_f32_e64 s[22:23], v33, v59
	v_cndmask_b32_e64 v109, 0, 1, s[20:21]
	v_cmp_lt_i32_e64 s[20:21], v26, v22
	s_and_b64 s[66:67], s[20:21], s[22:23]
	v_cmp_lt_i32_e64 s[20:21], v15, v19
	v_cmp_eq_f32_e64 s[22:23], v13, v32
	s_and_b64 s[22:23], s[20:21], s[22:23]
	v_cmp_lt_f32_e64 s[20:21], v13, v32
	s_or_b64 s[20:21], s[20:21], s[22:23]
	v_cmp_eq_f32_e64 s[22:23], v13, v38
	v_cndmask_b32_e64 v110, 0, 1, s[20:21]
	v_cmp_lt_i32_e64 s[20:21], v27, v19
	s_and_b64 s[68:69], s[20:21], s[22:23]
	v_cmp_lt_i32_e64 s[20:21], v17, v19
	v_cmp_eq_f32_e64 s[22:23], v13, v48
	s_and_b64 s[22:23], s[20:21], s[22:23]
	v_cmp_lt_f32_e64 s[20:21], v13, v48
	s_or_b64 s[20:21], s[20:21], s[22:23]
	v_cmp_eq_f32_e64 s[22:23], v13, v45
	v_cndmask_b32_e64 v111, 0, 1, s[20:21]
	v_cmp_lt_i32_e64 s[20:21], v12, v19
	s_and_b64 s[64:65], s[20:21], s[22:23]
	v_cmp_lt_i32_e64 s[20:21], v10, v19
	v_cmp_eq_f32_e64 s[22:23], v13, v47
	s_and_b64 s[22:23], s[20:21], s[22:23]
	v_cmp_lt_f32_e64 s[20:21], v13, v47
	s_or_b64 s[20:21], s[20:21], s[22:23]
	v_cmp_eq_f32_e64 s[22:23], v13, v44
	v_cndmask_b32_e64 v112, 0, 1, s[20:21]
	v_cmp_lt_i32_e64 s[20:21], v8, v19
	s_and_b64 s[62:63], s[20:21], s[22:23]
	v_cmp_lt_i32_e64 s[20:21], v6, v19
	v_cmp_eq_f32_e64 s[22:23], v13, v53
	s_and_b64 s[22:23], s[20:21], s[22:23]
	v_cmp_lt_f32_e64 s[20:21], v13, v53
	s_or_b64 s[20:21], s[20:21], s[22:23]
	v_cmp_eq_f32_e64 s[22:23], v13, v59
	v_cndmask_b32_e64 v113, 0, 1, s[20:21]
	v_cmp_lt_i32_e64 s[20:21], v26, v19
	s_and_b64 s[60:61], s[20:21], s[22:23]
	v_cmp_eq_f32_e64 s[20:21], v3, v38
	v_cmp_lt_i32_e64 s[22:23], v27, v2
	s_and_b64 s[0:1], s[22:23], s[20:21]
	v_cmp_eq_f32_e64 s[20:21], v3, v59
	v_cmp_lt_i32_e64 s[22:23], v26, v2
	s_and_b64 s[2:3], s[22:23], s[20:21]
	v_cmp_lt_f32_e64 s[20:21], v3, v38
	s_or_b64 s[0:1], s[20:21], s[0:1]
	v_cmp_lt_f32_e64 s[20:21], v3, v59
	v_cndmask_b32_e64 v26, 0, 1, s[0:1]
	s_or_b64 s[0:1], s[20:21], s[2:3]
	v_cmp_lt_i32_e64 s[20:21], v16, v24
	v_cmp_eq_f32_e64 s[22:23], v43, v56
	v_cndmask_b32_e64 v27, 0, 1, s[0:1]
	s_and_b64 s[0:1], s[20:21], s[22:23]
	v_cmp_lt_f32_e64 s[20:21], v43, v56
	s_or_b64 s[0:1], s[20:21], s[0:1]
	v_cmp_lt_i32_e64 s[20:21], v14, v24
	v_cmp_eq_f32_e64 s[22:23], v43, v58
	v_cndmask_b32_e64 v114, 0, 1, s[0:1]
	s_and_b64 s[0:1], s[20:21], s[22:23]
	v_cmp_lt_f32_e64 s[20:21], v43, v58
	s_or_b64 s[0:1], s[20:21], s[0:1]
	v_cmp_lt_i32_e64 s[20:21], v11, v24
	v_cmp_eq_f32_e64 s[22:23], v43, v57
	v_cndmask_b32_e64 v115, 0, 1, s[0:1]
	s_and_b64 s[0:1], s[20:21], s[22:23]
	v_cmp_lt_f32_e64 s[20:21], v43, v38
	s_or_b64 s[20:21], s[20:21], s[24:25]
	v_cmp_lt_i32_e64 s[22:23], v16, v22
	v_addc_co_u32_e64 v46, s[20:21], v46, v102, s[20:21]
	v_cmp_lt_f32_e64 s[20:21], v43, v45
	s_or_b64 s[20:21], s[20:21], s[48:49]
	v_cmp_eq_f32_e64 s[24:25], v33, v56
	v_addc_co_u32_e64 v46, s[20:21], v46, v103, s[20:21]
	v_cmp_lt_f32_e64 s[20:21], v43, v44
	s_or_b64 s[20:21], s[20:21], s[6:7]
	s_movk_i32 s2, 0xff
	v_addc_co_u32_e64 v46, s[20:21], v46, v104, s[20:21]
	v_cmp_lt_f32_e64 s[20:21], v43, v59
	s_or_b64 s[20:21], s[20:21], s[4:5]
	v_add_u16_e32 v0, v0, v50
	v_addc_co_u32_e64 v46, s[20:21], v46, v105, s[20:21]
	v_cmp_lt_f32_e64 s[20:21], v43, v31
	s_or_b64 s[20:21], s[20:21], s[46:47]
	v_lshlrev_b32_e64 v24, v24, 1
	v_addc_co_u32_e64 v46, s[20:21], v46, v114, s[20:21]
	v_cmp_lt_f32_e64 s[20:21], v43, v57
	s_or_b64 s[20:21], s[20:21], s[0:1]
	s_and_b64 s[0:1], s[22:23], s[24:25]
	v_cmp_lt_f32_e64 s[22:23], v33, v56
	s_or_b64 s[0:1], s[22:23], s[0:1]
	v_cmp_lt_i32_e64 s[22:23], v14, v22
	v_cmp_eq_f32_e64 s[24:25], v33, v58
	v_cndmask_b32_e64 v102, 0, 1, s[0:1]
	s_and_b64 s[0:1], s[22:23], s[24:25]
	v_cmp_lt_f32_e64 s[22:23], v33, v58
	s_or_b64 s[0:1], s[22:23], s[0:1]
	v_cmp_lt_i32_e64 s[22:23], v11, v22
	v_cmp_eq_f32_e64 s[24:25], v33, v57
	s_and_b64 s[46:47], s[22:23], s[24:25]
	v_cmp_lt_i32_e64 s[22:23], v16, v19
	v_cmp_eq_f32_e64 s[24:25], v13, v56
	v_cndmask_b32_e64 v103, 0, 1, s[0:1]
	s_and_b64 s[0:1], s[22:23], s[24:25]
	v_cmp_lt_f32_e64 s[22:23], v13, v56
	s_or_b64 s[0:1], s[22:23], s[0:1]
	v_cmp_lt_i32_e64 s[22:23], v14, v19
	v_cmp_eq_f32_e64 s[24:25], v13, v58
	v_cndmask_b32_e64 v104, 0, 1, s[0:1]
	s_and_b64 s[0:1], s[22:23], s[24:25]
	v_cmp_lt_f32_e64 s[22:23], v13, v58
	s_or_b64 s[0:1], s[22:23], s[0:1]
	v_cmp_lt_i32_e64 s[22:23], v11, v19
	v_cmp_eq_f32_e64 s[24:25], v13, v57
	s_and_b64 s[48:49], s[22:23], s[24:25]
	v_cmp_lt_i32_e64 s[22:23], v16, v175
	v_cmp_eq_f32_e64 s[24:25], v28, v56
	v_cndmask_b32_e64 v105, 0, 1, s[0:1]
	s_and_b64 s[0:1], s[22:23], s[24:25]
	v_cmp_lt_f32_e64 s[22:23], v28, v56
	s_or_b64 s[0:1], s[22:23], s[0:1]
	v_cmp_lt_i32_e64 s[22:23], v14, v175
	v_cmp_eq_f32_e64 s[24:25], v28, v58
	v_cndmask_b32_e64 v114, 0, 1, s[0:1]
	s_and_b64 s[0:1], s[22:23], s[24:25]
	v_cmp_lt_f32_e64 s[22:23], v28, v58
	s_or_b64 s[0:1], s[22:23], s[0:1]
	v_cmp_lt_i32_e64 s[22:23], v11, v175
	v_cmp_eq_f32_e64 s[24:25], v28, v57
	v_cndmask_b32_e64 v116, 0, 1, s[0:1]
	s_and_b64 s[0:1], s[22:23], s[24:25]
	v_cmp_lt_f32_e64 s[22:23], v28, v38
	s_or_b64 s[22:23], s[22:23], s[10:11]
	v_cmp_lt_f32_e64 s[24:25], v13, v31
	v_addc_co_u32_e64 v42, s[22:23], v42, v52, s[22:23]
	v_cmp_lt_f32_e64 s[22:23], v28, v45
	s_or_b64 s[22:23], s[22:23], s[8:9]
	v_lshlrev_b32_e64 v52, v177, 1
	v_addc_co_u32_e64 v42, s[22:23], v42, v91, s[22:23]
	v_cmp_lt_f32_e64 s[22:23], v28, v44
	s_or_b64 s[22:23], s[22:23], s[44:45]
	v_lshlrev_b32_e64 v91, v178, 1
	v_addc_co_u32_e64 v42, s[22:23], v42, v94, s[22:23]
	v_cmp_lt_f32_e64 s[22:23], v28, v59
	s_or_b64 s[22:23], s[22:23], s[26:27]
	v_lshlrev_b32_e64 v94, v179, 1
	v_addc_co_u32_e64 v42, s[22:23], v42, v95, s[22:23]
	v_cmp_lt_f32_e64 s[22:23], v28, v31
	s_or_b64 s[22:23], s[22:23], s[92:93]
	v_lshlrev_b32_e64 v95, v180, 1
	v_addc_co_u32_e64 v42, s[22:23], v42, v114, s[22:23]
	v_cmp_lt_f32_e64 s[22:23], v28, v57
	s_or_b64 s[22:23], s[22:23], s[0:1]
	v_readlane_b32 s0, v255, 46
	v_addc_co_u32_e64 v42, s[22:23], v42, v116, s[22:23]
	v_cmp_lt_f32_e64 s[22:23], v28, v54
	s_or_b64 s[22:23], s[22:23], s[30:31]
	v_readlane_b32 s1, v255, 47
	v_addc_co_u32_e64 v42, s[22:23], v42, v96, s[22:23]
	v_cmp_lt_f32_e64 s[22:23], v28, v18
	s_or_b64 s[22:23], s[22:23], s[0:1]
	v_lshlrev_b32_e64 v96, v181, 1
	v_addc_co_u32_e64 v28, s[22:23], v42, v97, s[22:23]
	v_cmp_lt_u32_e64 s[22:23], 7, v28
	s_or_b64 s[0:1], s[34:35], s[22:23]
	v_addc_co_u32_e64 v60, s[22:23], v61, v60, s[12:13]
	v_cmp_lt_u32_e64 s[22:23], 7, v60
	v_lshlrev_b16_e32 v60, 2, v74
	v_lshlrev_b16_e32 v61, 3, v76
	v_or_b32_e32 v60, v61, v60
	v_lshlrev_b16_e32 v61, 1, v77
	v_or_b32_e32 v61, v78, v61
	v_bitop3_b16 v60, v61, v60, 3 bitop3:0xec
	v_lshlrev_b16_e32 v61, 2, v79
	v_lshlrev_b16_e32 v74, 3, v81
	v_or_b32_e32 v61, v74, v61
	v_lshlrev_b16_e32 v74, 1, v82
	v_or_b32_e32 v74, v83, v74
	v_bitop3_b16 v61, v74, v61, 3 bitop3:0xec
	v_lshlrev_b16_e32 v61, 4, v61
	v_bitop3_b16 v60, v60, v61, 15 bitop3:0xec
	v_addc_co_u32_e64 v61, s[26:27], v63, v62, s[52:53]
	v_cmp_lt_u32_e64 s[26:27], 7, v61
	v_lshlrev_b16_e32 v61, 1, v89
	v_lshlrev_b16_e32 v62, 2, v92
	v_lshlrev_b16_e32 v63, 3, v93
	v_bitop3_b16 v61, v90, 3, v61 bitop3:0xc8
	v_or_b32_e32 v62, v63, v62
	v_bitop3_b16 v61, v61, 15, v62 bitop3:0xc8
	v_lshlrev_b32_e64 v42, v175, 1
	v_lshlrev_b16_e32 v61, 8, v61
	v_cndmask_b32_e64 v28, v42, 0, s[0:1]
	v_lshlrev_b32_e64 v42, v176, 1
	s_or_b64 s[0:1], s[28:29], s[22:23]
	v_bitop3_b16 v60, v60, v61, s2 bitop3:0xec
	v_addc_co_u32_e64 v61, s[28:29], v65, v64, s[54:55]
	v_cndmask_b32_e64 v42, v42, 0, s[0:1]
	s_or_b64 s[0:1], s[18:19], s[26:27]
	v_cmp_lt_u32_e64 s[28:29], 7, v61
	v_cmp_lt_f32_e64 s[18:19], v3, v31
	v_cndmask_b32_e64 v52, v52, 0, s[0:1]
	s_or_b64 s[0:1], s[16:17], s[28:29]
	v_cmp_lt_f32_e64 s[28:29], v33, v31
	v_add_u16_e32 v31, v49, v51
	v_add_u16_e32 v0, v31, v0
	v_addc_co_u32_e64 v31, s[30:31], v67, v66, s[56:57]
	v_cmp_lt_u32_e64 s[30:31], 7, v31
	v_cmp_lt_f32_e64 s[22:23], v13, v18
	v_cmp_lt_f32_e64 s[26:27], v43, v18
	v_cmp_lt_f32_e64 s[16:17], v33, v18
	v_cndmask_b32_e64 v18, v91, 0, s[0:1]
	s_or_b64 s[0:1], s[14:15], s[30:31]
	v_cmp_lt_f32_e64 s[30:31], v43, v54
	v_cndmask_b32_e64 v31, v94, 0, s[0:1]
	v_addc_co_u32_e64 v43, s[34:35], v69, v68, s[58:59]
	v_readlane_b32 s0, v255, 40
	v_cmp_lt_u32_e64 s[34:35], 7, v43
	v_readlane_b32 s1, v255, 41
	s_or_b64 s[0:1], s[0:1], s[34:35]
	v_addc_co_u32_e64 v49, s[44:45], v71, v70, s[50:51]
	v_cndmask_b32_e64 v43, v95, 0, s[0:1]
	v_readlane_b32 s0, v255, 42
	v_cmp_lt_u32_e64 s[44:45], 7, v49
	v_readlane_b32 s1, v255, 43
	s_or_b64 s[0:1], s[0:1], s[44:45]
	v_addc_co_u32_e64 v50, s[10:11], v73, v72, s[42:43]
	v_cndmask_b32_e64 v49, v96, 0, s[0:1]
	v_readlane_b32 s0, v255, 44
	v_cmp_lt_u32_e64 s[10:11], 7, v50
	v_readlane_b32 s1, v255, 45
	v_lshlrev_b32_e64 v97, v182, 1
	s_or_b64 s[0:1], s[0:1], s[10:11]
	v_cmp_lt_f32_e64 s[34:35], v33, v38
	v_cndmask_b32_e64 v50, v97, 0, s[0:1]
	v_cmp_lt_f32_e64 s[54:55], v13, v38
	v_addc_co_u32_e64 v38, s[8:9], v80, v75, s[40:41]
	v_readlane_b32 s0, v255, 52
	v_cmp_lt_u32_e64 s[8:9], 7, v38
	v_readlane_b32 s1, v255, 53
	s_or_b64 s[0:1], s[0:1], s[8:9]
	v_addc_co_u32_e64 v38, s[8:9], v85, v84, s[38:39]
	v_cndmask_b32_e64 v25, v25, 0, s[0:1]
	v_readlane_b32 s0, v255, 54
	v_cmp_lt_u32_e64 s[8:9], 7, v38
	v_readlane_b32 s1, v255, 55
	s_or_b64 s[0:1], s[0:1], s[8:9]
	v_cmp_lt_i32_e64 s[10:11], v17, v2
	v_cndmask_b32_e64 v23, v23, 0, s[0:1]
	v_addc_co_u32_e64 v17, s[8:9], v87, v86, s[36:37]
	v_readlane_b32 s0, v255, 48
	v_cmp_lt_u32_e64 s[8:9], 7, v17
	v_readlane_b32 s1, v255, 49
	s_or_b64 s[0:1], s[0:1], s[8:9]
	v_cmp_lt_i32_e64 s[8:9], v15, v2
	v_addc_co_u32_e64 v15, s[58:59], v88, v30, s[70:71]
	v_cmp_lt_u32_e64 s[58:59], 7, v15
	v_addc_co_u32_e64 v15, s[20:21], v46, v115, s[20:21]
	v_cmp_lt_f32_e64 s[12:13], v13, v54
	v_cmp_lt_f32_e64 s[42:43], v13, v45
	v_cmp_lt_f32_e64 s[56:57], v13, v44
	v_cmp_lt_f32_e64 s[40:41], v13, v59
	v_cmp_lt_f32_e64 s[20:21], v13, v57
	v_or_b32_e32 v13, v42, v28
	v_cmp_lt_i32_e64 s[38:39], v16, v2
	v_cndmask_b32_e64 v16, v21, 0, s[0:1]
	v_readlane_b32 s0, v255, 50
	v_or3_b32 v13, v13, v52, v18
	v_readlane_b32 s1, v255, 51
	v_or3_b32 v13, v13, v31, v43
	s_or_b64 s[0:1], s[0:1], s[58:59]
	v_or3_b32 v13, v13, v49, v50
	v_cmp_lt_i32_e64 s[36:37], v14, v2
	v_cndmask_b32_e64 v14, v20, 0, s[0:1]
	v_or3_b32 v13, v13, v25, v23
	s_or_b64 s[30:31], s[30:31], s[78:79]
	v_or3_b32 v13, v13, v16, v14
	v_addc_co_u32_e64 v14, s[30:31], v15, v40, s[30:31]
	s_or_b64 s[26:27], s[26:27], s[84:85]
	v_addc_co_u32_e64 v14, s[26:27], v14, v41, s[26:27]
	v_cmp_lt_u32_e64 s[26:27], 7, v14
	s_or_b64 s[0:1], s[96:97], s[26:27]
	s_or_b64 s[26:27], s[34:35], s[72:73]
	v_cmp_lt_f32_e64 s[44:45], v33, v45
	v_addc_co_u32_e64 v15, s[26:27], v34, v106, s[26:27]
	s_or_b64 s[26:27], s[44:45], s[86:87]
	v_cmp_lt_f32_e64 s[50:51], v33, v44
	v_addc_co_u32_e64 v15, s[26:27], v15, v107, s[26:27]
	s_or_b64 s[26:27], s[50:51], s[94:95]
	v_cmp_lt_f32_e64 s[52:53], v33, v59
	v_addc_co_u32_e64 v15, s[26:27], v15, v108, s[26:27]
	s_or_b64 s[26:27], s[52:53], s[66:67]
	s_nop 0
	v_addc_co_u32_e64 v15, s[26:27], v15, v109, s[26:27]
	s_or_b64 s[26:27], s[28:29], s[80:81]
	v_cmp_lt_f32_e64 s[58:59], v33, v57
	v_addc_co_u32_e64 v15, s[26:27], v15, v102, s[26:27]
	v_cmp_lt_f32_e64 s[14:15], v33, v54
	s_or_b64 s[26:27], s[58:59], s[46:47]
	v_addc_co_u32_e64 v15, s[26:27], v15, v103, s[26:27]
	s_or_b64 s[14:15], s[14:15], s[76:77]
	v_addc_co_u32_e64 v15, s[14:15], v15, v37, s[14:15]
	s_or_b64 s[14:15], s[16:17], s[82:83]
	v_cndmask_b32_e64 v14, v24, 0, s[0:1]
	v_addc_co_u32_e64 v15, s[14:15], v15, v39, s[14:15]
	v_readlane_b32 s0, v255, 56
	v_cmp_lt_u32_e64 s[14:15], 7, v15
	v_readlane_b32 s1, v255, 57
	v_lshlrev_b32_e64 v22, v22, 1
	s_or_b64 s[0:1], s[0:1], s[14:15]
	v_cndmask_b32_e64 v15, v22, 0, s[0:1]
	s_or_b64 s[14:15], s[54:55], s[68:69]
	v_or3_b32 v13, v13, v14, v15
	v_addc_co_u32_e64 v14, s[14:15], v29, v110, s[14:15]
	s_or_b64 s[14:15], s[42:43], s[64:65]
	s_nop 0
	v_addc_co_u32_e64 v14, s[14:15], v14, v111, s[14:15]
	s_or_b64 s[14:15], s[56:57], s[62:63]
	s_nop 0
	v_addc_co_u32_e64 v14, s[14:15], v14, v112, s[14:15]
	s_or_b64 s[14:15], s[40:41], s[60:61]
	s_nop 0
	v_addc_co_u32_e64 v14, s[14:15], v14, v113, s[14:15]
	s_or_b64 s[14:15], s[24:25], s[90:91]
	s_nop 0
	v_addc_co_u32_e64 v14, s[14:15], v14, v104, s[14:15]
	s_or_b64 s[14:15], s[20:21], s[48:49]
	s_nop 0
	v_addc_co_u32_e64 v14, s[14:15], v14, v105, s[14:15]
	s_or_b64 s[12:13], s[12:13], s[74:75]
	v_readlane_b32 s0, v255, 38
	v_addc_co_u32_e64 v14, s[12:13], v14, v35, s[12:13]
	v_readlane_b32 s1, v255, 39
	s_or_b64 s[12:13], s[22:23], s[0:1]
	v_addc_co_u32_e64 v14, s[12:13], v14, v36, s[12:13]
	v_readlane_b32 s0, v255, 34
	v_cmp_lt_u32_e64 s[12:13], 7, v14
	v_readlane_b32 s1, v255, 35
	v_lshlrev_b32_e64 v19, v19, 1
	s_or_b64 s[0:1], s[0:1], s[12:13]
	v_cmp_eq_f32_e64 s[14:15], v3, v56
	v_cndmask_b32_e64 v14, v19, 0, s[0:1]
	v_cmp_lt_f32_e64 s[6:7], v3, v56
	v_cmp_eq_f32_e64 s[16:17], v3, v48
	s_and_b64 s[0:1], s[38:39], s[14:15]
	v_cmp_lt_f32_e64 s[12:13], v3, v48
	s_and_b64 s[2:3], s[10:11], s[16:17]
	s_or_b64 s[0:1], s[6:7], s[0:1]
	v_cndmask_b32_e64 v15, 0, 1, s[0:1]
	s_or_b64 s[0:1], s[12:13], s[2:3]
	v_cmp_eq_f32_e64 s[12:13], v3, v58
	v_cndmask_b32_e64 v16, 0, 1, s[0:1]
	v_cmp_lt_f32_e64 s[6:7], v3, v58
	v_cmp_eq_f32_e64 s[14:15], v3, v32
	s_and_b64 s[0:1], s[36:37], s[12:13]
	v_cmp_lt_f32_e64 s[10:11], v3, v32
	s_and_b64 s[2:3], s[8:9], s[14:15]
	s_or_b64 s[0:1], s[6:7], s[0:1]
	v_cndmask_b32_e64 v17, 0, 1, s[0:1]
	s_or_b64 s[0:1], s[10:11], s[2:3]
	v_cmp_eq_f32_e64 s[10:11], v3, v57
	v_cmp_lt_i32_e64 s[16:17], v11, v2
	v_cndmask_b32_e64 v18, 0, 1, s[0:1]
	v_cmp_lt_f32_e64 s[6:7], v3, v57
	v_cmp_eq_f32_e64 s[12:13], v3, v45
	v_cmp_lt_i32_e64 s[14:15], v12, v2
	s_and_b64 s[0:1], s[16:17], s[10:11]
	v_cmp_lt_f32_e64 s[8:9], v3, v45
	s_and_b64 s[2:3], s[14:15], s[12:13]
	s_or_b64 s[0:1], s[6:7], s[0:1]
	v_cndmask_b32_e64 v11, 0, 1, s[0:1]
	s_or_b64 s[0:1], s[8:9], s[2:3]
	v_cmp_eq_f32_e64 s[10:11], v3, v55
	v_cmp_lt_i32_e64 s[16:17], v9, v2
	v_cndmask_b32_e64 v12, 0, 1, s[0:1]
	v_cmp_lt_f32_e64 s[6:7], v3, v55
	v_cmp_eq_f32_e64 s[12:13], v3, v47
	v_cmp_lt_i32_e64 s[14:15], v10, v2
	s_and_b64 s[0:1], s[16:17], s[10:11]
	v_cmp_lt_f32_e64 s[8:9], v3, v47
	s_and_b64 s[2:3], s[14:15], s[12:13]
	s_or_b64 s[0:1], s[6:7], s[0:1]
	v_cndmask_b32_e64 v9, 0, 1, s[0:1]
	s_or_b64 s[0:1], s[8:9], s[2:3]
	v_cmp_eq_f32_e64 s[10:11], v3, v54
	v_cmp_lt_i32_e64 s[16:17], v7, v2
	v_cndmask_b32_e64 v10, 0, 1, s[0:1]
	v_cmp_lt_f32_e64 s[6:7], v3, v54
	v_cmp_eq_f32_e64 s[12:13], v3, v44
	v_cmp_lt_i32_e64 s[14:15], v8, v2
	s_and_b64 s[0:1], s[16:17], s[10:11]
	v_cmp_lt_f32_e64 s[8:9], v3, v44
	s_and_b64 s[2:3], s[14:15], s[12:13]
	s_or_b64 s[0:1], s[6:7], s[0:1]
	v_cndmask_b32_e64 v7, 0, 1, s[0:1]
	s_or_b64 s[0:1], s[8:9], s[2:3]
	v_cmp_eq_f32_e64 s[10:11], v3, v4
	v_cmp_lt_i32_e64 s[16:17], v5, v2
	v_cndmask_b32_e64 v8, 0, 1, s[0:1]
	v_cmp_lt_f32_e64 s[6:7], v3, v4
	v_cmp_eq_f32_e64 s[12:13], v3, v53
	v_cmp_lt_i32_e64 s[14:15], v6, v2
	s_and_b64 s[0:1], s[16:17], s[10:11]
	v_cmp_lt_f32_e64 s[8:9], v3, v53
	s_and_b64 s[2:3], s[14:15], s[12:13]
	s_or_b64 s[0:1], s[6:7], s[0:1]
	v_cndmask_b32_e64 v3, 0, 1, s[0:1]
	s_or_b64 s[0:1], s[8:9], s[2:3]
	v_cndmask_b32_e64 v4, 0, 1, s[0:1]
	s_or_b64 s[0:1], s[18:19], s[88:89]
	v_and_b32_e32 v60, 0xffff, v60
	v_add_u16_e32 v5, v27, v15
	v_cndmask_b32_e64 v15, 0, 1, s[0:1]
	v_add_u16_e32 v6, v26, v16
	v_bcnt_u32_b32 v16, v60, v18
	v_add_u16_e32 v15, v15, v17
	v_add_u16_e32 v9, v11, v9
	v_add_u16_e32 v10, v12, v10
	v_add_u16_e32 v3, v7, v3
	v_add_u16_e32 v4, v8, v4
	v_add_u16_e32 v6, v6, v16
	v_add_u16_e32 v5, v5, v15
	v_add_u16_e32 v3, v9, v3
	v_add_u16_e32 v4, v10, v4
	v_add_u16_e32 v4, v6, v4
	v_add_u16_e32 v3, v5, v3
	v_add3_u32 v0, v4, v3, v0
	v_readlane_b32 s0, v255, 36
	v_cmp_lt_u32_e64 s[6:7], 7, v0
	v_readlane_b32 s1, v255, 37
	v_lshlrev_b32_e64 v0, v2, 1
	s_or_b64 s[0:1], s[0:1], s[6:7]
	v_cndmask_b32_e64 v0, v0, 0, s[0:1]
	v_or3_b32 v2, v13, v14, v0
	ds_bpermute_b32 v3, v183, v2
	s_and_saveexec_b64 s[4:5], vcc
	s_cbranch_execz .LBB0_557
	v_readlane_b32 s2, v255, 32
	s_lshl_b32 s0, s2, 3
	s_and_b32 s0, s0, 0xfffff800
	v_or_b32_e32 v4, s0, v174
	v_readlane_b32 s0, v255, 12
	v_ashrrev_i32_e32 v5, 31, v4
	v_readlane_b32 s1, v255, 13
	s_waitcnt lgkmcnt(0)
	v_or_b32_e32 v0, v2, v3
	v_lshl_add_u64 v[2:3], v[4:5], 4, s[0:1]
	s_lshr_b32 s0, s2, 4
	v_readlane_b32 s2, v255, 10
	v_readlane_b32 s3, v255, 11
	s_mov_b32 s1, s3
	s_and_b32 s2, s0, 12
	v_writelane_b32 v255, s0, 10
	v_lshl_add_u64 v[2:3], v[2:3], 0, s[2:3]
	global_store_dword v[2:3], v0, off nt
	v_writelane_b32 v255, s1, 11
	s_branch .LBB0_557

.LBB0_1006:
	s_waitcnt vmcnt(2)
	v_lshl_add_u64 v[14:15], s[12:13], 0, v[10:11]
	v_add_co_u32_e32 v18, vcc, 0x49800000, v14
	v_lshl_add_u64 v[12:13], s[10:11], 0, v[10:11]
	s_nop 0
	v_addc_co_u32_e32 v19, vcc, 0, v15, vcc
	v_add_co_u32_e32 v12, vcc, 0xf003000, v12
	global_load_dwordx4 v[20:23], v[18:19], off
	global_load_dwordx4 v[28:31], v[18:19], off offset:1024
	global_load_dwordx4 v[40:43], v[18:19], off offset:2048
	global_load_dwordx4 v[52:55], v[18:19], off offset:3072
	v_addc_co_u32_e32 v13, vcc, 0, v13, vcc
	global_load_dwordx4 v[60:63], v[12:13], off
	global_load_dwordx4 v[66:69], v[12:13], off offset:1024
	global_load_dwordx4 v[74:77], v[12:13], off offset:2048
	global_load_dwordx4 v[78:81], v[12:13], off offset:3072
	v_add_co_u32_e64 v16, s[4:5], s7, v14
	s_add_i32 s6, s6, s8
	s_nop 0
	v_addc_co_u32_e64 v17, s[4:5], 0, v15, s[4:5]
	s_add_u32 s10, s10, s16
	s_addc_u32 s11, s11, s17
	s_add_u32 s12, s12, s14
	s_addc_u32 s13, s13, s15
	s_cmpk_lt_i32 s6, 0x4000
	s_waitcnt vmcnt(7)
	v_lshlrev_b32_e32 v34, 16, v20
	v_and_b32_e32 v35, 0xffff0000, v20
	v_lshlrev_b32_e32 v18, 16, v22
	v_and_b32_e32 v19, 0xffff0000, v22
	v_lshlrev_b32_e32 v24, 16, v21
	v_and_b32_e32 v25, 0xffff0000, v21
	s_waitcnt vmcnt(6)
	v_lshlrev_b32_e32 v46, 16, v28
	v_and_b32_e32 v47, 0xffff0000, v28
	s_waitcnt vmcnt(5)
	v_lshlrev_b32_e32 v56, 16, v40
	v_and_b32_e32 v57, 0xffff0000, v40
	s_waitcnt vmcnt(4)
	v_lshlrev_b32_e32 v64, 16, v52
	v_and_b32_e32 v65, 0xffff0000, v52
	s_waitcnt vmcnt(3)
	v_lshlrev_b32_e32 v22, 16, v62
	v_pk_mul_f32 v[88:89], v[34:35], v[34:35]
	v_lshlrev_b32_e32 v14, 16, v23
	v_and_b32_e32 v15, 0xffff0000, v23
	v_lshlrev_b32_e32 v20, 16, v31
	v_and_b32_e32 v21, 0xffff0000, v31
	v_lshlrev_b32_e32 v26, 16, v30
	v_and_b32_e32 v27, 0xffff0000, v30
	v_lshlrev_b32_e32 v36, 16, v29
	v_and_b32_e32 v37, 0xffff0000, v29
	v_lshlrev_b32_e32 v28, 16, v43
	v_and_b32_e32 v29, 0xffff0000, v43
	v_lshlrev_b32_e32 v38, 16, v42
	v_and_b32_e32 v39, 0xffff0000, v42
	v_lshlrev_b32_e32 v48, 16, v41
	v_and_b32_e32 v49, 0xffff0000, v41
	v_lshlrev_b32_e32 v40, 16, v55
	v_and_b32_e32 v41, 0xffff0000, v55
	v_lshlrev_b32_e32 v50, 16, v54
	v_and_b32_e32 v51, 0xffff0000, v54
	v_lshlrev_b32_e32 v58, 16, v53
	v_and_b32_e32 v59, 0xffff0000, v53
	v_lshlrev_b32_e32 v12, 16, v63
	v_and_b32_e32 v13, 0xffff0000, v63
	v_and_b32_e32 v23, 0xffff0000, v62
	v_lshlrev_b32_e32 v32, 16, v61
	v_and_b32_e32 v33, 0xffff0000, v61
	v_pk_mul_f32 v[86:87], v[24:25], v[24:25]
	v_lshlrev_b32_e32 v44, 16, v60
	v_and_b32_e32 v45, 0xffff0000, v60
	s_waitcnt vmcnt(2)
	v_lshlrev_b32_e32 v30, 16, v69
	v_and_b32_e32 v31, 0xffff0000, v69
	v_lshlrev_b32_e32 v42, 16, v68
	v_and_b32_e32 v43, 0xffff0000, v68
	v_lshlrev_b32_e32 v54, 16, v67
	v_and_b32_e32 v55, 0xffff0000, v67
	v_lshlrev_b32_e32 v62, 16, v66
	v_and_b32_e32 v63, 0xffff0000, v66
	v_pk_mul_f32 v[96:97], v[46:47], v[46:47]
	s_waitcnt vmcnt(1)
	v_lshlrev_b32_e32 v60, 16, v76
	v_and_b32_e32 v61, 0xffff0000, v76
	v_lshlrev_b32_e32 v68, 16, v75
	v_and_b32_e32 v69, 0xffff0000, v75
	v_lshlrev_b32_e32 v102, 16, v74
	v_and_b32_e32 v103, 0xffff0000, v74
	v_pk_mul_f32 v[74:75], v[56:57], v[56:57]
	s_waitcnt vmcnt(0)
	v_lshlrev_b32_e32 v108, 16, v79
	v_and_b32_e32 v109, 0xffff0000, v79
	v_lshlrev_b32_e32 v112, 16, v78
	v_and_b32_e32 v113, 0xffff0000, v78
	v_pk_mul_f32 v[78:79], v[64:65], v[64:65]
	v_mul_f32_e32 v0, 0xbfb8aa3b, v22
	v_add_f32_e32 v88, v88, v89
	v_pk_mul_f32 v[94:95], v[36:37], v[36:37]
	v_lshlrev_b32_e32 v52, 16, v77
	v_pk_mul_f32 v[100:101], v[48:49], v[48:49]
	v_pk_mul_f32 v[110:111], v[58:59], v[58:59]
	v_mul_f32_e32 v114, 0xbfb8aa3b, v23
	v_mul_f32_e32 v115, 0xbfb8aa3b, v32
	v_mul_f32_e32 v116, 0xbfb8aa3b, v33
	v_mul_f32_e32 v89, 0xbfb8aa3b, v12
	v_mul_f32_e32 v119, 0xbfb8aa3b, v13
	v_mul_f32_e32 v120, 0xbfb8aa3b, v42
	v_mul_f32_e32 v121, 0xbfb8aa3b, v43
	v_mul_f32_e32 v122, 0xbfb8aa3b, v54
	v_mul_f32_e32 v123, 0xbfb8aa3b, v55
	v_mul_f32_e32 v124, 0xbfb8aa3b, v62
	v_mul_f32_e32 v125, 0xbfb8aa3b, v63
	v_add_f32_e32 v96, v96, v97
	v_mul_f32_e32 v97, 0xbfb8aa3b, v30
	v_mul_f32_e32 v126, 0xbfb8aa3b, v31
	v_mul_f32_e32 v127, 0xbfb8aa3b, v60
	v_mul_f32_e32 v128, 0xbfb8aa3b, v61
	v_mul_f32_e32 v129, 0xbfb8aa3b, v68
	v_mul_f32_e32 v130, 0xbfb8aa3b, v69
	v_add_f32_e32 v74, v74, v75
	v_add_f32_e32 v78, v78, v79
	v_exp_f32_e32 v0, v0
	v_add_f32_e32 v86, v86, v88
	v_pk_mul_f32 v[84:85], v[18:19], v[18:19]
	v_lshlrev_b32_e32 v66, 16, v81
	v_mul_f32_e32 v117, 0xbfb8aa3b, v44
	v_mul_f32_e32 v118, 0xbfb8aa3b, v45
	v_mul_f32_e32 v131, 0xbfb8aa3b, v102
	v_mul_f32_e32 v132, 0xbfb8aa3b, v103
	v_mul_f32_e32 v75, 0xbfb8aa3b, v52
	v_exp_f32_e32 v114, v114
	v_exp_f32_e32 v115, v115
	v_exp_f32_e32 v116, v116
	v_exp_f32_e32 v88, v89
	v_exp_f32_e32 v89, v119
	v_exp_f32_e32 v119, v120
	v_exp_f32_e32 v120, v121
	v_exp_f32_e32 v121, v122
	v_exp_f32_e32 v122, v123
	v_exp_f32_e32 v123, v124
	v_exp_f32_e32 v124, v125
	v_add_f32_e32 v94, v94, v96
	v_exp_f32_e32 v96, v97
	v_exp_f32_e32 v97, v126
	v_exp_f32_e32 v125, v127
	v_exp_f32_e32 v126, v128
	v_exp_f32_e32 v127, v129
	v_exp_f32_e32 v128, v130
	v_add_f32_e32 v74, v100, v74
	v_add_f32_e32 v78, v110, v78
	v_add_f32_e32 v86, v87, v86
	v_pk_mul_f32 v[92:93], v[26:27], v[26:27]
	v_and_b32_e32 v53, 0xffff0000, v77
	v_pk_mul_f32 v[76:77], v[38:39], v[38:39]
	v_and_b32_e32 v67, 0xffff0000, v81
	v_lshlrev_b32_e32 v106, 16, v80
	v_and_b32_e32 v107, 0xffff0000, v80
	v_pk_mul_f32 v[80:81], v[50:51], v[50:51]
	v_mul_f32_e32 v79, 0xbfb8aa3b, v66
	v_exp_f32_e32 v117, v117
	v_exp_f32_e32 v118, v118
	v_exp_f32_e32 v129, v131
	v_exp_f32_e32 v130, v132
	v_exp_f32_e32 v75, v75
	v_add_f32_e32 v87, v95, v94
	v_add_f32_e32 v74, v101, v74
	v_add_f32_e32 v78, v111, v78
	v_add_f32_e32 v84, v84, v86
	v_pk_mul_f32 v[82:83], v[14:15], v[14:15]
	v_exp_f32_e32 v79, v79
	v_add_f32_e32 v86, v92, v87
	v_add_f32_e32 v74, v76, v74
	v_add_f32_e32 v76, v80, v78
	v_add_f32_e32 v78, v85, v84
	v_pk_mul_f32 v[90:91], v[20:21], v[20:21]
	v_pk_mul_f32 v[98:99], v[28:29], v[28:29]
	v_pk_mul_f32 v[104:105], v[40:41], v[40:41]
	v_add_f32_e32 v80, v93, v86
	v_add_f32_e32 v74, v77, v74
	v_add_f32_e32 v76, v81, v76
	v_add_f32_e32 v0, 1.0, v0
	v_add_f32_e32 v82, v82, v78
	v_add_f32_e32 v77, 1.0, v114
	v_add_f32_e32 v81, 1.0, v115
	v_add_f32_e32 v84, 1.0, v116
	v_add_f32_e32 v92, 1.0, v120
	v_add_f32_e32 v93, 1.0, v121
	v_add_f32_e32 v90, v90, v80
	v_add_f32_e32 v114, 1.0, v126
	v_add_f32_e32 v115, 1.0, v127
	v_add_f32_e32 v116, 1.0, v128
	v_add_f32_e32 v98, v98, v74
	v_add_f32_e32 v104, v104, v76
	v_rcp_f32_e32 v74, v0
	v_add_f32_e32 v0, v83, v82
	v_add_f32_e32 v85, 1.0, v117
	v_add_f32_e32 v86, 1.0, v118
	v_add_f32_e32 v87, 1.0, v88
	v_add_f32_e32 v88, 1.0, v89
	v_add_f32_e32 v89, 1.0, v119
	v_add_f32_e32 v94, 1.0, v122
	v_add_f32_e32 v95, 1.0, v123
	v_add_f32_e32 v96, 1.0, v96
	v_add_f32_e32 v117, 1.0, v129
	v_add_f32_e32 v118, 1.0, v130
	v_add_f32_e32 v119, 1.0, v75
	v_rcp_f32_e32 v75, v77
	v_rcp_f32_e32 v77, v84
	v_rcp_f32_e32 v83, v92
	v_rcp_f32_e32 v84, v93
	v_add_f32_e32 v128, v91, v90
	v_rcp_f32_e32 v91, v114
	v_rcp_f32_e32 v92, v115
	v_rcp_f32_e32 v93, v116
	v_add_f32_e32 v114, v99, v98
	v_add_f32_e32 v115, v105, v104
	ds_bpermute_b32 v116, v70, v0
	v_mul_f32_e32 v134, 0xbfb8aa3b, v106
	v_add_f32_e32 v126, 1.0, v79
	v_rcp_f32_e32 v76, v81
	v_rcp_f32_e32 v78, v85
	v_rcp_f32_e32 v79, v86
	v_rcp_f32_e32 v81, v88
	v_rcp_f32_e32 v85, v94
	v_rcp_f32_e32 v86, v95
	v_rcp_f32_e32 v88, v96
	v_rcp_f32_e32 v94, v117
	v_rcp_f32_e32 v95, v118
	v_rcp_f32_e32 v96, v119
	ds_bpermute_b32 v117, v70, v128
	ds_bpermute_b32 v118, v70, v114
	ds_bpermute_b32 v119, v70, v115
	v_exp_f32_e32 v131, v134
	s_waitcnt lgkmcnt(3)
	v_add_f32_e32 v0, v0, v116
	s_waitcnt lgkmcnt(2)
	v_add_f32_e32 v116, v128, v117
	s_waitcnt lgkmcnt(1)
	v_add_f32_e32 v114, v114, v118
	v_add_f32_e32 v120, 1.0, v131
	s_waitcnt lgkmcnt(0)
	v_add_f32_e32 v115, v115, v119
	ds_bpermute_b32 v117, v71, v0
	v_rcp_f32_e32 v98, v120
	ds_bpermute_b32 v118, v71, v116
	ds_bpermute_b32 v119, v71, v114
	ds_bpermute_b32 v120, v71, v115
	s_waitcnt lgkmcnt(3)
	v_add_f32_e32 v0, v0, v117
	ds_bpermute_b32 v117, v72, v0
	s_waitcnt lgkmcnt(3)
	v_add_f32_e32 v116, v116, v118
	s_waitcnt lgkmcnt(2)
	v_add_f32_e32 v114, v114, v119
	s_waitcnt lgkmcnt(1)
	v_add_f32_e32 v115, v115, v120
	ds_bpermute_b32 v118, v72, v116
	ds_bpermute_b32 v119, v72, v114
	ds_bpermute_b32 v120, v72, v115
	s_waitcnt lgkmcnt(3)
	v_add_f32_e32 v0, v0, v117
	ds_bpermute_b32 v117, v73, v0
	s_waitcnt lgkmcnt(3)
	v_add_f32_e32 v116, v116, v118
	s_waitcnt lgkmcnt(2)
	v_add_f32_e32 v114, v114, v119
	s_waitcnt lgkmcnt(1)
	v_add_f32_e32 v115, v115, v120
	ds_bpermute_b32 v118, v73, v116
	ds_bpermute_b32 v119, v73, v114
	ds_bpermute_b32 v120, v73, v115
	v_mul_f32_e32 v133, 0xbfb8aa3b, v53
	v_mul_f32_e32 v135, 0xbfb8aa3b, v107
	v_mul_f32_e32 v136, 0xbfb8aa3b, v108
	v_mul_f32_e32 v137, 0xbfb8aa3b, v109
	v_mul_f32_e32 v138, 0xbfb8aa3b, v112
	v_mul_f32_e32 v139, 0xbfb8aa3b, v113
	v_mul_f32_e32 v140, 0xbfb8aa3b, v67
	s_waitcnt lgkmcnt(3)
	v_add_f32_e32 v0, v0, v117
	v_exp_f32_e32 v100, v133
	v_exp_f32_e32 v132, v135
	v_exp_f32_e32 v133, v136
	v_exp_f32_e32 v134, v137
	v_exp_f32_e32 v135, v138
	v_exp_f32_e32 v136, v139
	v_exp_f32_e32 v110, v140
	s_waitcnt lgkmcnt(2)
	v_add_f32_e32 v116, v116, v118
	s_waitcnt lgkmcnt(1)
	v_add_f32_e32 v114, v114, v119
	s_waitcnt lgkmcnt(0)
	v_add_f32_e32 v115, v115, v120
	v_fmamk_f32 v0, v0, 0x3c000000, v1
	v_fmamk_f32 v116, v116, 0x3c000000, v1
	v_fmamk_f32 v117, v114, 0x3c000000, v1
	v_fmamk_f32 v115, v115, 0x3c000000, v1
	v_rsq_f32_e32 v0, v0
	v_rsq_f32_e32 v114, v116
	v_rsq_f32_e32 v116, v117
	v_rsq_f32_e32 v118, v115
	v_add_f32_e32 v101, 1.0, v124
	v_add_f32_e32 v97, 1.0, v97
	v_add_f32_e32 v111, 1.0, v125
	v_add_f32_e32 v100, 1.0, v100
	v_add_f32_e32 v121, 1.0, v132
	v_add_f32_e32 v122, 1.0, v133
	v_add_f32_e32 v123, 1.0, v134
	v_add_f32_e32 v124, 1.0, v135
	v_add_f32_e32 v125, 1.0, v136
	v_add_f32_e32 v127, 1.0, v110
	v_rcp_f32_e32 v80, v87
	v_rcp_f32_e32 v82, v89
	v_rcp_f32_e32 v87, v101
	v_rcp_f32_e32 v89, v97
	v_rcp_f32_e32 v90, v111
	v_rcp_f32_e32 v97, v100
	v_rcp_f32_e32 v99, v121
	v_rcp_f32_e32 v100, v122
	v_rcp_f32_e32 v101, v123
	v_rcp_f32_e32 v110, v124
	v_rcp_f32_e32 v111, v125
	v_rcp_f32_e32 v104, v126
	v_rcp_f32_e32 v105, v127
	v_pk_mul_f32 v[34:35], v[0:1], v[34:35] op_sel_hi:[0,1]
	v_pk_mul_f32 v[24:25], v[0:1], v[24:25] op_sel_hi:[0,1]
	v_pk_mul_f32 v[18:19], v[0:1], v[18:19] op_sel_hi:[0,1]
	v_pk_mul_f32 v[14:15], v[0:1], v[14:15] op_sel_hi:[0,1]
	v_pk_mul_f32 v[46:47], v[114:115], v[46:47] op_sel_hi:[0,1]
	v_pk_mul_f32 v[36:37], v[114:115], v[36:37] op_sel_hi:[0,1]
	v_pk_mul_f32 v[26:27], v[114:115], v[26:27] op_sel_hi:[0,1]
	v_pk_mul_f32 v[20:21], v[114:115], v[20:21] op_sel_hi:[0,1]
	v_pk_mul_f32 v[56:57], v[116:117], v[56:57] op_sel_hi:[0,1]
	v_pk_mul_f32 v[48:49], v[116:117], v[48:49] op_sel_hi:[0,1]
	v_pk_mul_f32 v[38:39], v[116:117], v[38:39] op_sel_hi:[0,1]
	v_pk_mul_f32 v[28:29], v[116:117], v[28:29] op_sel_hi:[0,1]
	v_pk_mul_f32 v[64:65], v[118:119], v[64:65] op_sel_hi:[0,1]
	v_pk_mul_f32 v[58:59], v[118:119], v[58:59] op_sel_hi:[0,1]
	v_pk_mul_f32 v[50:51], v[118:119], v[50:51] op_sel_hi:[0,1]
	v_pk_mul_f32 v[40:41], v[118:119], v[40:41] op_sel_hi:[0,1]
	v_pk_mul_f32 v[34:35], v[2:3], v[34:35]
	v_pk_mul_f32 v[24:25], v[4:5], v[24:25]
	v_pk_mul_f32 v[18:19], v[6:7], v[18:19]
	v_pk_mul_f32 v[14:15], v[8:9], v[14:15]
	v_pk_mul_f32 v[46:47], v[2:3], v[46:47]
	v_pk_mul_f32 v[36:37], v[4:5], v[36:37]
	v_pk_mul_f32 v[26:27], v[6:7], v[26:27]
	v_pk_mul_f32 v[20:21], v[8:9], v[20:21]
	v_pk_mul_f32 v[56:57], v[2:3], v[56:57]
	v_pk_mul_f32 v[48:49], v[4:5], v[48:49]
	v_pk_mul_f32 v[38:39], v[6:7], v[38:39]
	v_pk_mul_f32 v[28:29], v[8:9], v[28:29]
	v_pk_mul_f32 v[64:65], v[2:3], v[64:65]
	v_pk_mul_f32 v[58:59], v[4:5], v[58:59]
	v_pk_mul_f32 v[50:51], v[6:7], v[50:51]
	v_pk_mul_f32 v[40:41], v[8:9], v[40:41]
	v_pk_mul_f32 v[34:35], v[34:35], v[44:45]
	v_pk_mul_f32 v[24:25], v[24:25], v[32:33]
	v_pk_mul_f32 v[18:19], v[18:19], v[22:23]
	v_pk_mul_f32 v[12:13], v[14:15], v[12:13]
	v_pk_mul_f32 v[14:15], v[46:47], v[62:63]
	v_pk_mul_f32 v[22:23], v[36:37], v[54:55]
	v_pk_mul_f32 v[26:27], v[26:27], v[42:43]
	v_pk_mul_f32 v[20:21], v[20:21], v[30:31]
	v_pk_mul_f32 v[30:31], v[56:57], v[102:103]
	v_pk_mul_f32 v[32:33], v[48:49], v[68:69]
	v_pk_mul_f32 v[36:37], v[38:39], v[60:61]
	v_pk_mul_f32 v[28:29], v[28:29], v[52:53]
	v_pk_mul_f32 v[38:39], v[64:65], v[112:113]
	v_pk_mul_f32 v[42:43], v[58:59], v[108:109]
	v_pk_mul_f32 v[44:45], v[50:51], v[106:107]
	v_pk_mul_f32 v[40:41], v[40:41], v[66:67]
	v_pk_mul_f32 v[34:35], v[78:79], v[34:35]
	v_pk_mul_f32 v[24:25], v[76:77], v[24:25]
	v_pk_mul_f32 v[18:19], v[74:75], v[18:19]
	v_pk_mul_f32 v[46:47], v[80:81], v[12:13]
	v_pk_mul_f32 v[48:49], v[86:87], v[14:15]
	v_pk_mul_f32 v[22:23], v[84:85], v[22:23]
	v_pk_mul_f32 v[26:27], v[82:83], v[26:27]
	v_pk_mul_f32 v[50:51], v[88:89], v[20:21]
	v_pk_mul_f32 v[30:31], v[94:95], v[30:31]
	v_pk_mul_f32 v[32:33], v[92:93], v[32:33]
	v_pk_mul_f32 v[36:37], v[90:91], v[36:37]
	v_pk_mul_f32 v[28:29], v[96:97], v[28:29]
	v_pk_mul_f32 v[38:39], v[110:111], v[38:39]
	v_pk_mul_f32 v[42:43], v[100:101], v[42:43]
	v_pk_mul_f32 v[44:45], v[98:99], v[44:45]
	v_pk_mul_f32 v[40:41], v[104:105], v[40:41]
	v_cvt_pk_bf16_f32 v12, v34, v35
	v_cvt_pk_bf16_f32 v13, v24, v25
	v_cvt_pk_bf16_f32 v14, v18, v19
	v_cvt_pk_bf16_f32 v15, v46, v47
	v_cvt_pk_bf16_f32 v18, v48, v49
	v_cvt_pk_bf16_f32 v19, v22, v23
	v_cvt_pk_bf16_f32 v20, v26, v27
	v_cvt_pk_bf16_f32 v21, v50, v51
	v_cvt_pk_bf16_f32 v22, v30, v31
	v_cvt_pk_bf16_f32 v23, v32, v33
	v_cvt_pk_bf16_f32 v24, v36, v37
	v_cvt_pk_bf16_f32 v25, v28, v29
	v_cvt_pk_bf16_f32 v26, v38, v39
	v_cvt_pk_bf16_f32 v27, v42, v43
	v_cvt_pk_bf16_f32 v28, v44, v45
	v_cvt_pk_bf16_f32 v29, v40, v41
	global_store_dwordx4 v[16:17], v[12:15], off nt
	global_store_dwordx4 v[16:17], v[18:21], off offset:1024 nt
	global_store_dwordx4 v[16:17], v[22:25], off offset:2048 nt
	global_store_dwordx4 v[16:17], v[26:29], off offset:3072 nt
	s_cbranch_scc1 .LBB0_1006

.LBB0_1639:
	s_ashr_i32 s9, s8, 31
	s_lshl_b64 s[18:19], s[8:9], 2
	s_add_u32 s20, s15, s18
	s_addc_u32 s21, s16, s19
	global_load_dwordx2 v[30:31], v[26:27], off offset:2560
	global_load_dwordx2 v[28:29], v[26:27], off offset:3072
	global_load_dwordx2 v[38:39], v[26:27], off offset:3584
	global_load_dwordx2 v[42:43], v[26:27], off
	global_load_dwordx2 v[48:49], v[26:27], off offset:512
	global_load_dwordx2 v[44:45], v[26:27], off offset:1024
	global_load_dwordx2 v[40:41], v[26:27], off offset:1536
	global_load_dwordx2 v[32:33], v[26:27], off offset:2048
	global_load_dwordx4 v[4:7], v11, s[20:21]
	s_add_u32 s20, s11, s18
	s_addc_u32 s21, s12, s19
	s_add_u32 s18, s13, s18
	s_addc_u32 s19, s14, s19
	global_load_dword v60, v11, s[20:21]
	global_load_dword v73, v11, s[18:19]
	s_add_i32 s20, s8, 1
	s_ashr_i32 s21, s20, 31
	s_lshl_b64 s[18:19], s[20:21], 2
	s_add_u32 s20, s11, s18
	s_addc_u32 s21, s12, s19
	global_load_dwordx3 v[8:10], v11, s[20:21]
	s_add_u32 s18, s13, s18
	s_addc_u32 s19, s14, s19
	global_load_dword v88, v11, s[18:19]
	s_add_i32 s20, s8, 2
	s_ashr_i32 s21, s20, 31
	s_lshl_b64 s[18:19], s[20:21], 2
	s_add_u32 s18, s13, s18
	s_addc_u32 s19, s14, s19
	global_load_dwordx2 v[46:47], v11, s[18:19]
	global_load_dwordx4 v[0:3], v[14:15], off
	s_add_i32 s4, s4, s6
	s_add_i32 s8, s8, s17
	v_lshl_add_u64 v[26:27], v[26:27], 0, s[2:3]
	s_cmpk_lt_i32 s4, 0x4000
	s_waitcnt vmcnt(14)
	v_lshlrev_b32_e32 v70, 16, v30
	v_and_b32_e32 v71, 0xffff0000, v30
	s_waitcnt vmcnt(13)
	v_lshlrev_b32_e32 v34, 16, v29
	v_and_b32_e32 v72, 0xffff0000, v29
	s_waitcnt vmcnt(10)
	v_lshlrev_b32_e32 v51, 16, v49
	v_lshlrev_b32_e32 v50, 16, v48
	s_waitcnt vmcnt(8)
	v_lshlrev_b32_e32 v55, 16, v41
	v_lshlrev_b32_e32 v54, 16, v40
	v_and_b32_e32 v57, 0xffff0000, v41
	v_and_b32_e32 v56, 0xffff0000, v40
	s_waitcnt vmcnt(7)
	v_lshlrev_b32_e32 v74, 16, v33
	v_and_b32_e32 v75, 0xffff0000, v33
	v_lshlrev_b32_e32 v40, 16, v32
	v_and_b32_e32 v41, 0xffff0000, v32
	v_lshlrev_b32_e32 v32, 16, v31
	v_and_b32_e32 v33, 0xffff0000, v31
	s_waitcnt vmcnt(6)
	v_pk_mul_f32 v[76:77], v[4:5], s[10:11] op_sel:[1,0] op_sel_hi:[0,0]
	v_mov_b32_e32 v31, v4
	v_mov_b32_e32 v4, v6
	v_pk_mul_f32 v[78:79], v[4:5], s[10:11] op_sel_hi:[1,0]
	v_mov_b32_e32 v4, v7
	s_waitcnt vmcnt(5)
	v_lshlrev_b32_e32 v60, 2, v60
	v_mov_b32_e32 v30, v6
	v_mov_b32_e32 v58, v7
	v_mov_b32_e32 v59, v6
	v_pk_mul_f32 v[6:7], v[4:5], s[10:11] op_sel_hi:[1,0]
	v_add_u32_e32 v4, s5, v60
	ds_read_b32 v4, v4
	s_waitcnt vmcnt(3)
	v_lshlrev_b32_e32 v8, 2, v8
	v_lshlrev_b32_e32 v9, 2, v9
	v_lshlrev_b32_e32 v10, 2, v10
	v_add_u32_e32 v8, s5, v8
	v_add_u32_e32 v9, s5, v9
	v_add_u32_e32 v10, s5, v10
	ds_read_b32 v89, v8
	s_waitcnt lgkmcnt(1)
	v_add_u32_e32 v8, v73, v4
	ds_read_b32 v4, v9
	ds_read_b32 v10, v10
	v_ashrrev_i32_e32 v9, 31, v8
	v_lshlrev_b64 v[8:9], 11, v[8:9]
	v_lshl_add_u64 v[8:9], v[12:13], 0, v[8:9]
	global_load_dword v73, v[8:9], off
	global_load_dword v91, v[8:9], off offset:256
	global_load_dword v95, v[8:9], off offset:512
	global_load_dword v99, v[8:9], off offset:768
	global_load_dword v101, v[8:9], off offset:1024
	global_load_dword v103, v[8:9], off offset:1280
	global_load_dword v107, v[8:9], off offset:1536
	global_load_dword v109, v[8:9], off offset:1792
	s_waitcnt vmcnt(10) lgkmcnt(2)
	v_add_u32_e32 v8, v88, v89
	s_waitcnt vmcnt(9) lgkmcnt(1)
	v_add_u32_e32 v46, v46, v4
	s_waitcnt lgkmcnt(0)
	v_add_u32_e32 v88, v47, v10
	v_ashrrev_i32_e32 v9, 31, v8
	v_ashrrev_i32_e32 v47, 31, v46
	v_ashrrev_i32_e32 v89, 31, v88
	v_lshlrev_b64 v[8:9], 11, v[8:9]
	v_lshlrev_b64 v[46:47], 11, v[46:47]
	v_lshlrev_b64 v[88:89], 11, v[88:89]
	v_lshl_add_u64 v[8:9], v[12:13], 0, v[8:9]
	v_lshl_add_u64 v[46:47], v[12:13], 0, v[46:47]
	v_lshl_add_u64 v[88:89], v[12:13], 0, v[88:89]
	global_load_dword v4, v[8:9], off
	global_load_dword v10, v[8:9], off offset:256
	global_load_dword v111, v[8:9], off offset:512
	global_load_dword v113, v[8:9], off offset:768
	global_load_dword v115, v[8:9], off offset:1024
	global_load_dword v117, v[8:9], off offset:1280
	global_load_dword v118, v[8:9], off offset:1536
	global_load_dword v124, v[8:9], off offset:1792
	global_load_dword v126, v[46:47], off
	global_load_dword v128, v[46:47], off offset:256
	global_load_dword v141, v[46:47], off offset:512
	global_load_dword v145, v[46:47], off offset:768
	global_load_dword v147, v[46:47], off offset:1024
	global_load_dword v149, v[46:47], off offset:1280
	global_load_dword v153, v[46:47], off offset:1536
	global_load_dword v155, v[46:47], off offset:1792
	global_load_dword v157, v[88:89], off
	global_load_dword v159, v[88:89], off offset:256
	global_load_dword v161, v[88:89], off offset:512
	global_load_dword v162, v[88:89], off offset:768
	global_load_dword v164, v[88:89], off offset:1024
	global_load_dword v184, v[88:89], off offset:1280
	global_load_dword v185, v[88:89], off offset:1536
	global_load_dword v186, v[88:89], off offset:1792
	v_lshlrev_b32_e32 v53, 16, v45
	v_lshlrev_b32_e32 v52, 16, v44
	v_pk_mul_f32 v[30:31], v[30:31], s[10:11] op_sel_hi:[1,0]
	v_lshlrev_b32_e32 v69, 16, v38
	v_and_b32_e32 v29, 0xffff0000, v38
	v_lshlrev_b32_e32 v37, 16, v39
	v_and_b32_e32 v35, 0xffff0000, v39
	v_lshlrev_b32_e32 v38, 16, v42
	v_and_b32_e32 v39, 0xffff0000, v42
	v_lshlrev_b32_e32 v42, 16, v43
	v_and_b32_e32 v43, 0xffff0000, v43
	v_and_b32_e32 v49, 0xffff0000, v49
	v_and_b32_e32 v48, 0xffff0000, v48
	v_and_b32_e32 v45, 0xffff0000, v45
	v_and_b32_e32 v44, 0xffff0000, v44
	v_lshlrev_b32_e32 v36, 16, v28
	v_mov_b32_e32 v80, v31
	v_mov_b32_e32 v81, v7
	v_and_b32_e32 v28, 0xffff0000, v28
	v_mov_b32_e32 v83, v31
	v_mov_b32_e32 v86, v30
	v_mov_b32_e32 v82, v7
	v_mov_b32_e32 v87, v6
	v_pk_mul_f32 v[58:59], v[58:59], s[10:11] op_sel_hi:[1,0]
	v_mov_b32_e32 v84, v30
	v_mov_b32_e32 v85, v7
	v_mov_b32_e32 v61, v30
	v_mov_b32_e32 v60, v6
	v_mov_b32_e32 v5, v6
	s_waitcnt vmcnt(31)
	v_cvt_f32_fp8_e32 v8, v73
	s_waitcnt vmcnt(30)
	v_cvt_f32_fp8_e32 v88, v91
	v_cvt_f32_fp8_sdwa v89, v91 src0_sel:BYTE_2
	s_waitcnt vmcnt(29)
	v_cvt_f32_fp8_e32 v92, v95
	v_cvt_f32_fp8_sdwa v93, v95 src0_sel:BYTE_2
	s_waitcnt vmcnt(28)
	v_cvt_f32_fp8_e32 v96, v99
	v_cvt_f32_fp8_sdwa v98, v99 src0_sel:BYTE_1
	v_cvt_f32_fp8_sdwa v97, v99 src0_sel:BYTE_2
	v_cvt_f32_fp8_sdwa v99, v99 src0_sel:BYTE_3
	s_waitcnt vmcnt(27)
	v_cvt_f32_fp8_e32 v100, v101
	v_cvt_f32_fp8_sdwa v102, v101 src0_sel:BYTE_1
	v_cvt_f32_fp8_sdwa v104, v101 src0_sel:BYTE_2
	v_cvt_f32_fp8_sdwa v105, v101 src0_sel:BYTE_3
	s_waitcnt vmcnt(26)
	v_cvt_f32_fp8_e32 v106, v103
	v_cvt_f32_fp8_sdwa v108, v103 src0_sel:BYTE_1
	v_cvt_f32_fp8_sdwa v110, v103 src0_sel:BYTE_2
	v_cvt_f32_fp8_sdwa v112, v103 src0_sel:BYTE_3
	s_waitcnt vmcnt(25)
	v_cvt_f32_fp8_sdwa v101, v107 src0_sel:BYTE_2
	s_waitcnt vmcnt(24)
	v_cvt_f32_fp8_e32 v103, v109
	v_cvt_f32_fp8_sdwa v9, v73 src0_sel:BYTE_1
	v_cvt_f32_fp8_sdwa v46, v73 src0_sel:BYTE_2
	v_cvt_f32_fp8_sdwa v47, v73 src0_sel:BYTE_3
	v_cvt_f32_fp8_sdwa v90, v91 src0_sel:BYTE_1
	v_cvt_f32_fp8_sdwa v91, v91 src0_sel:BYTE_3
	v_cvt_f32_fp8_sdwa v94, v95 src0_sel:BYTE_1
	v_cvt_f32_fp8_sdwa v95, v95 src0_sel:BYTE_3
	v_cvt_f32_fp8_e32 v73, v107
	v_fmac_f32_e32 v34, v31, v101
	v_mul_f32_e32 v187, v31, v103
	v_pk_fma_f32 v[50:51], v[30:31], v[88:89], v[50:51] op_sel:[1,0,0]
	v_pk_fma_f32 v[52:53], v[30:31], v[92:93], v[52:53] op_sel:[1,0,0]
	v_pk_fma_f32 v[54:55], v[30:31], v[96:97], v[54:55] op_sel:[1,0,0]
	v_pk_fma_f32 v[56:57], v[30:31], v[98:99], v[56:57] op_sel:[1,0,0]
	s_waitcnt vmcnt(22)
	v_cvt_f32_fp8_e32 v88, v10
	v_cvt_f32_fp8_sdwa v89, v10 src0_sel:BYTE_2
	s_waitcnt vmcnt(21)
	v_cvt_f32_fp8_e32 v92, v111
	v_cvt_f32_fp8_sdwa v93, v111 src0_sel:BYTE_2
	s_waitcnt vmcnt(20)
	v_cvt_f32_fp8_e32 v96, v113
	v_cvt_f32_fp8_sdwa v98, v113 src0_sel:BYTE_1
	v_cvt_f32_fp8_sdwa v97, v113 src0_sel:BYTE_2
	v_cvt_f32_fp8_sdwa v99, v113 src0_sel:BYTE_3
	s_waitcnt vmcnt(19)
	v_cvt_f32_fp8_e32 v101, v115
	v_cvt_f32_fp8_sdwa v103, v115 src0_sel:BYTE_1
	v_cvt_f32_fp8_sdwa v114, v107 src0_sel:BYTE_1
	v_cvt_f32_fp8_sdwa v116, v107 src0_sel:BYTE_3
	v_cvt_f32_fp8_sdwa v119, v109 src0_sel:BYTE_1
	v_cvt_f32_fp8_sdwa v121, v109 src0_sel:BYTE_2
	v_cvt_f32_fp8_sdwa v123, v109 src0_sel:BYTE_3
	v_pk_fma_f32 v[48:49], v[30:31], v[90:91], v[48:49] op_sel:[1,0,0]
	v_pk_fma_f32 v[44:45], v[30:31], v[94:95], v[44:45] op_sel:[1,0,0]
	v_pk_fma_f32 v[8:9], v[30:31], v[8:9], v[38:39] op_sel:[1,0,0]
	v_pk_fma_f32 v[38:39], v[30:31], v[46:47], v[42:43] op_sel:[1,0,0]
	v_pk_fma_f32 v[42:43], v[30:31], v[104:105], v[74:75] op_sel:[1,0,0]
	v_cvt_f32_fp8_e32 v46, v4
	v_cvt_f32_fp8_sdwa v47, v4 src0_sel:BYTE_1
	v_cvt_f32_fp8_sdwa v74, v4 src0_sel:BYTE_2
	v_cvt_f32_fp8_sdwa v75, v4 src0_sel:BYTE_3
	v_cvt_f32_fp8_sdwa v90, v10 src0_sel:BYTE_1
	v_cvt_f32_fp8_sdwa v91, v10 src0_sel:BYTE_3
	v_cvt_f32_fp8_sdwa v94, v111 src0_sel:BYTE_1
	v_cvt_f32_fp8_sdwa v95, v111 src0_sel:BYTE_3
	v_cvt_f32_fp8_sdwa v104, v115 src0_sel:BYTE_2
	v_cvt_f32_fp8_sdwa v105, v115 src0_sel:BYTE_3
	s_waitcnt vmcnt(18)
	v_cvt_f32_fp8_e32 v107, v117
	v_cvt_f32_fp8_sdwa v109, v117 src0_sel:BYTE_1
	v_cvt_f32_fp8_sdwa v111, v117 src0_sel:BYTE_2
	v_cvt_f32_fp8_sdwa v113, v117 src0_sel:BYTE_3
	s_waitcnt vmcnt(17)
	v_cvt_f32_fp8_e32 v120, v118
	v_cvt_f32_fp8_sdwa v115, v118 src0_sel:BYTE_1
	v_cvt_f32_fp8_sdwa v117, v118 src0_sel:BYTE_3
	s_waitcnt vmcnt(14)
	v_cvt_f32_fp8_e32 v134, v128
	v_cvt_f32_fp8_sdwa v135, v128 src0_sel:BYTE_2
	s_waitcnt vmcnt(13)
	v_cvt_f32_fp8_e32 v138, v141
	v_cvt_f32_fp8_sdwa v139, v141 src0_sel:BYTE_2
	s_waitcnt vmcnt(12)
	v_cvt_f32_fp8_e32 v142, v145
	v_cvt_f32_fp8_sdwa v144, v145 src0_sel:BYTE_1
	v_cvt_f32_fp8_sdwa v143, v145 src0_sel:BYTE_2
	v_cvt_f32_fp8_sdwa v145, v145 src0_sel:BYTE_3
	v_cvt_f32_fp8_sdwa v122, v118 src0_sel:BYTE_2
	v_cvt_f32_fp8_e32 v4, v124
	v_cvt_f32_fp8_e32 v130, v126
	v_cvt_f32_fp8_sdwa v131, v126 src0_sel:BYTE_1
	v_cvt_f32_fp8_sdwa v132, v126 src0_sel:BYTE_2
	v_cvt_f32_fp8_sdwa v133, v126 src0_sel:BYTE_3
	v_cvt_f32_fp8_sdwa v136, v128 src0_sel:BYTE_1
	v_cvt_f32_fp8_sdwa v137, v128 src0_sel:BYTE_3
	s_waitcnt vmcnt(11)
	v_cvt_f32_fp8_e32 v146, v147
	v_cvt_f32_fp8_sdwa v148, v147 src0_sel:BYTE_1
	v_cvt_f32_fp8_sdwa v150, v147 src0_sel:BYTE_2
	v_cvt_f32_fp8_sdwa v151, v147 src0_sel:BYTE_3
	s_waitcnt vmcnt(10)
	v_cvt_f32_fp8_e32 v118, v149
	v_cvt_f32_fp8_sdwa v152, v149 src0_sel:BYTE_1
	v_cvt_f32_fp8_sdwa v154, v149 src0_sel:BYTE_2
	v_cvt_f32_fp8_sdwa v156, v149 src0_sel:BYTE_3
	s_waitcnt vmcnt(8)
	v_cvt_f32_fp8_sdwa v10, v155 src0_sel:BYTE_1
	s_waitcnt vmcnt(3)
	v_cvt_f32_fp8_e32 v147, v164
	v_cvt_f32_fp8_sdwa v149, v164 src0_sel:BYTE_1
	v_fmac_f32_e32 v36, v31, v73
	v_cvt_f32_fp8_sdwa v127, v124 src0_sel:BYTE_2
	v_cvt_f32_fp8_e32 v126, v153
	v_cvt_f32_fp8_sdwa v158, v153 src0_sel:BYTE_1
	v_cvt_f32_fp8_sdwa v128, v153 src0_sel:BYTE_2
	v_cvt_f32_fp8_sdwa v160, v153 src0_sel:BYTE_3
	v_cvt_f32_fp8_e32 v73, v155
	v_cvt_f32_fp8_sdwa v163, v155 src0_sel:BYTE_2
	v_cvt_f32_fp8_sdwa v165, v155 src0_sel:BYTE_3
	v_cvt_f32_fp8_e32 v166, v157
	v_cvt_f32_fp8_sdwa v167, v157 src0_sel:BYTE_1
	v_cvt_f32_fp8_sdwa v168, v157 src0_sel:BYTE_2
	v_cvt_f32_fp8_sdwa v169, v157 src0_sel:BYTE_3
	v_cvt_f32_fp8_e32 v170, v159
	v_cvt_f32_fp8_sdwa v172, v159 src0_sel:BYTE_1
	v_cvt_f32_fp8_sdwa v171, v159 src0_sel:BYTE_2
	v_cvt_f32_fp8_sdwa v173, v159 src0_sel:BYTE_3
	v_cvt_f32_fp8_e32 v174, v161
	v_cvt_f32_fp8_sdwa v176, v161 src0_sel:BYTE_1
	v_cvt_f32_fp8_sdwa v175, v161 src0_sel:BYTE_2
	v_cvt_f32_fp8_sdwa v177, v161 src0_sel:BYTE_3
	s_waitcnt vmcnt(2)
	v_cvt_f32_fp8_sdwa v153, v184 src0_sel:BYTE_1
	v_cvt_f32_fp8_sdwa v155, v184 src0_sel:BYTE_2
	v_cvt_f32_fp8_sdwa v157, v184 src0_sel:BYTE_3
	s_waitcnt vmcnt(1)
	v_cvt_f32_fp8_sdwa v159, v185 src0_sel:BYTE_1
	v_cvt_f32_fp8_sdwa v161, v185 src0_sel:BYTE_3
	v_cvt_f32_fp8_sdwa v140, v141 src0_sel:BYTE_1
	v_cvt_f32_fp8_sdwa v141, v141 src0_sel:BYTE_3
	v_cvt_f32_fp8_e32 v178, v162
	v_cvt_f32_fp8_sdwa v180, v162 src0_sel:BYTE_1
	v_cvt_f32_fp8_sdwa v179, v162 src0_sel:BYTE_2
	v_cvt_f32_fp8_sdwa v181, v162 src0_sel:BYTE_3
	v_cvt_f32_fp8_e32 v162, v185
	v_pk_mul_f32 v[100:101], v[80:81], v[100:101]
	v_pk_mul_f32 v[102:103], v[80:81], v[102:103]
	v_pk_fma_f32 v[50:51], v[6:7], v[88:89], v[50:51] op_sel:[1,0,0]
	v_pk_fma_f32 v[52:53], v[6:7], v[92:93], v[52:53] op_sel:[1,0,0]
	v_pk_fma_f32 v[54:55], v[6:7], v[96:97], v[54:55] op_sel:[1,0,0]
	v_pk_fma_f32 v[56:57], v[6:7], v[98:99], v[56:57] op_sel:[1,0,0]
	v_cvt_f32_fp8_sdwa v125, v124 src0_sel:BYTE_1
	v_cvt_f32_fp8_sdwa v129, v124 src0_sel:BYTE_3
	v_cvt_f32_fp8_e32 v124, v184
	s_waitcnt vmcnt(0)
	v_cvt_f32_fp8_sdwa v188, v186 src0_sel:BYTE_2
	v_pk_mul_f32 v[106:107], v[80:81], v[106:107]
	v_pk_mul_f32 v[108:109], v[80:81], v[108:109]
	v_pk_mul_f32 v[110:111], v[80:81], v[110:111]
	v_pk_mul_f32 v[112:113], v[80:81], v[112:113]
	v_pk_fma_f32 v[36:37], v[76:77], v[120:121], v[36:37]
	v_pk_mul_f32 v[76:77], v[80:81], v[114:115]
	v_pk_mul_f32 v[80:81], v[80:81], v[116:117]
	v_pk_fma_f32 v[48:49], v[6:7], v[90:91], v[48:49] op_sel:[1,0,0]
	v_pk_fma_f32 v[8:9], v[6:7], v[46:47], v[8:9] op_sel:[1,0,0]
	v_pk_fma_f32 v[38:39], v[6:7], v[74:75], v[38:39] op_sel:[1,0,0]
	v_pk_fma_f32 v[46:47], v[30:31], v[134:135], v[50:51] op_sel_hi:[0,1,1]
	v_pk_fma_f32 v[50:51], v[30:31], v[138:139], v[52:53] op_sel_hi:[0,1,1]
	v_pk_fma_f32 v[52:53], v[30:31], v[142:143], v[54:55] op_sel_hi:[0,1,1]
	v_pk_fma_f32 v[54:55], v[30:31], v[144:145], v[56:57] op_sel_hi:[0,1,1]
	v_mov_b32_e32 v56, v100
	v_mov_b32_e32 v57, v102
	v_cvt_f32_fp8_sdwa v182, v164 src0_sel:BYTE_2
	v_cvt_f32_fp8_sdwa v183, v164 src0_sel:BYTE_3
	v_cvt_f32_fp8_sdwa v164, v185 src0_sel:BYTE_2
	v_pk_fma_f32 v[34:35], v[82:83], v[122:123], v[34:35]
	v_mul_f32_e32 v189, v7, v4
	v_mul_f32_e32 v83, v30, v10
	v_pk_mul_f32 v[114:115], v[86:87], v[146:147]
	v_pk_mul_f32 v[116:117], v[86:87], v[148:149]
	v_add_f32_e32 v4, v106, v70
	v_add_f32_e32 v10, v108, v71
	v_add_f32_e32 v76, v76, v28
	v_add_f32_e32 v72, v80, v72
	v_pk_fma_f32 v[48:49], v[30:31], v[136:137], v[48:49] op_sel_hi:[0,1,1]
	v_pk_fma_f32 v[8:9], v[30:31], v[130:131], v[8:9] op_sel_hi:[0,1,1]
	v_pk_fma_f32 v[38:39], v[30:31], v[132:133], v[38:39] op_sel_hi:[0,1,1]
	v_mov_b32_e32 v102, v101
	v_pk_add_f32 v[40:41], v[56:57], v[40:41]
	v_pk_mul_f32 v[120:121], v[86:87], v[152:153]
	v_pk_mul_f32 v[122:123], v[86:87], v[154:155]
	v_pk_mul_f32 v[146:147], v[86:87], v[156:157]
	v_pk_mul_f32 v[148:149], v[86:87], v[158:159]
	v_pk_mul_f32 v[86:87], v[86:87], v[160:161]
	v_pk_fma_f32 v[44:45], v[6:7], v[94:95], v[44:45] op_sel:[1,0,0]
	v_pk_fma_f32 v[36:37], v[78:79], v[126:127], v[36:37]
	v_mov_b32_e32 v70, v114
	v_mov_b32_e32 v71, v116
	v_mov_b32_e32 v74, v110
	v_mov_b32_e32 v75, v112
	v_add_f32_e32 v28, v4, v107
	v_add_f32_e32 v4, v10, v109
	v_add_f32_e32 v10, v76, v77
	v_add_f32_e32 v72, v72, v81
	v_pk_fma_f32 v[48:49], v[6:7], v[172:173], v[48:49] op_sel_hi:[0,1,1]
	v_pk_fma_f32 v[8:9], v[6:7], v[166:167], v[8:9] op_sel_hi:[0,1,1]
	v_pk_fma_f32 v[38:39], v[6:7], v[168:169], v[38:39] op_sel_hi:[0,1,1]
	v_pk_add_f32 v[40:41], v[40:41], v[102:103]
	v_cvt_f32_fp8_e32 v184, v186
	v_pk_fma_f32 v[44:45], v[30:31], v[140:141], v[44:45] op_sel_hi:[0,1,1]
	v_mov_b32_e32 v116, v115
	v_mov_b32_e32 v112, v111
	v_pk_fma_f32 v[36:37], v[58:59], v[162:163], v[36:37]
	v_pk_fma_f32 v[46:47], v[6:7], v[170:171], v[46:47] op_sel_hi:[0,1,1]
	v_pk_add_f32 v[32:33], v[74:75], v[32:33]
	v_pk_fma_f32 v[28:29], v[30:31], v[118:119], v[28:29]
	v_add_f32_e32 v75, v10, v148
	v_add_f32_e32 v76, v72, v86
	v_pk_mul_f32 v[56:57], v[48:49], v[48:49]
	v_mul_f32_e32 v10, v9, v9
	v_mul_f32_e32 v72, v39, v39
	v_pk_add_f32 v[40:41], v[40:41], v[70:71]
	v_cvt_f32_fp8_sdwa v185, v186 src0_sel:BYTE_1
	v_cvt_f32_fp8_sdwa v186, v186 src0_sel:BYTE_3
	v_mul_f32_e32 v153, v6, v188
	v_pk_fma_f32 v[42:43], v[6:7], v[104:105], v[42:43] op_sel:[1,0,0]
	v_pk_fma_f32 v[34:35], v[84:85], v[128:129], v[34:35]
	v_mov_b32_e32 v78, v122
	v_mov_b32_e32 v79, v146
	v_pk_fma_f32 v[44:45], v[6:7], v[176:177], v[44:45] op_sel_hi:[0,1,1]
	v_mov_b32_e32 v152, v36
	v_pk_add_f32 v[32:33], v[32:33], v[112:113]
	v_pk_fma_f32 v[28:29], v[6:7], v[124:125], v[28:29]
	v_add_f32_e32 v96, v75, v149
	v_add_f32_e32 v97, v76, v87
	v_pk_fma_f32 v[56:57], v[46:47], v[46:47], v[56:57]
	v_pk_fma_f32 v[76:77], v[8:9], v[8:9], v[10:11] op_sel_hi:[1,1,0]
	v_pk_fma_f32 v[80:81], v[38:39], v[38:39], v[72:73] op_sel_hi:[1,1,0]
	v_pk_add_f32 v[40:41], v[40:41], v[116:117]
	v_pk_fma_f32 v[42:43], v[30:31], v[150:151], v[42:43] op_sel_hi:[0,1,1]
	v_mov_b32_e32 v146, v123
	v_pk_fma_f32 v[34:35], v[60:61], v[164:165], v[34:35]
	v_pk_fma_f32 v[50:51], v[6:7], v[174:175], v[50:51] op_sel_hi:[0,1,1]
	v_pk_fma_f32 v[54:55], v[6:7], v[180:181], v[54:55] op_sel_hi:[0,1,1]
	v_add_f32_e32 v4, v4, v120
	v_pk_mul_f32 v[58:59], v[44:45], v[44:45]
	v_pk_add_f32 v[84:85], v[36:37], v[152:153]
	v_pk_add_f32 v[32:33], v[32:33], v[78:79]
	v_mov_b32_e32 v77, v187
	v_mov_b32_e32 v81, v69
	v_pk_add_f32 v[56:57], v[56:57], v[56:57] op_sel:[0,1] op_sel_hi:[1,0]
	v_mov_b32_e32 v82, v28
	v_mul_f32_e32 v10, v96, v96
	v_mul_f32_e32 v72, v97, v97
	v_pk_mov_b32 v[30:31], v[40:41], v[30:31] op_sel:[1,0]
	v_pk_fma_f32 v[52:53], v[6:7], v[178:179], v[52:53] op_sel_hi:[0,1,1]
	v_pk_fma_f32 v[42:43], v[6:7], v[182:183], v[42:43] op_sel_hi:[0,1,1]
	v_pk_mul_f32 v[60:61], v[54:55], v[54:55]
	v_add_f32_e32 v4, v4, v121
	v_pk_fma_f32 v[58:59], v[50:51], v[50:51], v[58:59]
	v_pk_mul_f32 v[70:71], v[28:29], v[28:29]
	v_pk_mul_f32 v[78:79], v[84:85], v[84:85]
	v_pk_add_f32 v[32:33], v[32:33], v[146:147]
	v_pk_add_f32 v[76:77], v[76:77], v[80:81]
	v_mov_b32_e32 v57, v189
	v_pk_add_f32 v[80:81], v[28:29], v[82:83]
	v_pk_fma_f32 v[82:83], v[36:37], v[36:37], v[10:11]
	v_pk_fma_f32 v[90:91], v[34:35], v[34:35], v[72:73]
	v_mov_b32_e32 v72, v30
	v_mul_f32_e32 v156, v6, v184
	v_mul_f32_e32 v74, v43, v43
	v_pk_fma_f32 v[60:61], v[52:53], v[52:53], v[60:61]
	v_pk_add_f32 v[58:59], v[58:59], v[58:59] op_sel:[0,1] op_sel_hi:[1,0]
	v_mov_b32_e32 v184, v4
	v_pk_mul_f32 v[92:93], v[40:41], v[40:41]
	v_pk_mul_f32 v[94:95], v[32:33], v[32:33]
	v_pk_add_f32 v[56:57], v[76:77], v[56:57]
	v_mov_b32_e32 v71, v81
	v_mov_b32_e32 v83, v79
	v_pk_mul_f32 v[78:79], v[30:31], v[72:73]
	v_mul_f32_e32 v155, v6, v186
	v_pk_fma_f32 v[74:75], v[42:43], v[42:43], v[74:75] op_sel_hi:[1,1,0]
	v_pk_add_f32 v[60:61], v[60:61], v[60:61] op_sel:[0,1] op_sel_hi:[1,0]
	v_pk_mov_b32 v[6:7], v[32:33], v[6:7] op_sel:[1,0]
	v_mov_b32_e32 v95, v81
	v_pk_fma_f32 v[70:71], v[4:5], v[184:185], v[70:71]
	v_mov_b32_e32 v93, v57
	v_mov_b32_e32 v184, v33
	v_mov_b32_e32 v59, v79
	v_mov_b32_e32 v154, v34
	v_mov_b32_e32 v75, v156
	v_mov_b32_e32 v61, v156
	v_pk_fma_f32 v[30:31], v[30:31], v[72:73], v[92:93]
	v_pk_fma_f32 v[6:7], v[6:7], v[184:185], v[94:95]
	v_pk_add_f32 v[56:57], v[56:57], v[58:59]
	v_pk_add_f32 v[86:87], v[34:35], v[154:155]
	v_pk_add_f32 v[30:31], v[30:31], v[74:75]
	v_pk_add_f32 v[58:59], v[70:71], v[6:7]
	v_pk_mul_f32 v[6:7], v[70:71], v[6:7]
	v_pk_add_f32 v[56:57], v[56:57], v[60:61]
	v_pk_mul_f32 v[88:89], v[86:87], v[86:87]
	v_mov_b32_e32 v59, v7
	v_pk_add_f32 v[6:7], v[56:57], v[30:31]
	v_pk_mul_f32 v[30:31], v[56:57], v[30:31]
	v_mov_b32_e32 v91, v89
	v_mov_b32_e32 v7, v31
	v_pk_add_f32 v[76:77], v[82:83], v[90:91]
	v_pk_add_f32 v[6:7], v[6:7], v[58:59]
	v_mov_b32_e32 v29, v4
	v_pk_add_f32 v[6:7], v[6:7], v[76:77]
	v_mov_b32_e32 v37, v96
	v_add_f32_e32 v5, v6, v7
	ds_bpermute_b32 v6, v62, v5
	v_mov_b32_e32 v35, v97
	v_mov_b32_e32 v86, v85
	v_mov_b32_e32 v70, v57
	s_waitcnt lgkmcnt(0)
	v_add_f32_e32 v5, v5, v6
	ds_bpermute_b32 v6, v63, v5
	s_waitcnt lgkmcnt(0)
	v_add_f32_e32 v5, v5, v6
	ds_bpermute_b32 v6, v64, v5
	s_waitcnt lgkmcnt(0)
	v_add_f32_e32 v5, v5, v6
	ds_bpermute_b32 v6, v65, v5
	s_waitcnt lgkmcnt(0)
	v_add_f32_e32 v5, v5, v6
	ds_bpermute_b32 v6, v66, v5
	s_waitcnt lgkmcnt(0)
	v_add_f32_e32 v5, v5, v6
	ds_bpermute_b32 v6, v67, v5
	s_waitcnt lgkmcnt(0)
	v_add_f32_e32 v5, v5, v6
	v_fmamk_f32 v5, v5, 0x3a000000, v68
	v_rsq_f32_e32 v6, v5
	s_nop 0
	v_pk_mul_f32 v[8:9], v[8:9], v[6:7] op_sel_hi:[1,0]
	v_pk_mul_f32 v[30:31], v[38:39], v[6:7] op_sel_hi:[1,0]
	v_pk_mul_f32 v[0:1], v[0:1], v[8:9]
	v_pk_mul_f32 v[2:3], v[2:3], v[30:31]
	global_store_dwordx4 v[24:25], v[0:3], off offset:-4096 nt
	global_load_dwordx4 v[0:3], v[14:15], off offset:1024
	v_mov_b32_e32 v8, v46
	v_mov_b32_e32 v9, v48
	v_mov_b32_e32 v48, v47
	v_pk_mul_f32 v[8:9], v[8:9], v[6:7] op_sel_hi:[1,0]
	v_pk_mul_f32 v[30:31], v[48:49], v[6:7] op_sel_hi:[1,0]
	v_pk_mul_f32 v[4:5], v[32:33], v[6:7] op_sel_hi:[1,0]
	s_waitcnt vmcnt(0)
	v_pk_mul_f32 v[0:1], v[0:1], v[8:9]
	v_pk_mul_f32 v[2:3], v[2:3], v[30:31]
	global_store_dwordx4 v[24:25], v[0:3], off offset:-3072 nt
	global_load_dwordx4 v[0:3], v[14:15], off offset:2048
	v_mov_b32_e32 v8, v50
	v_mov_b32_e32 v9, v44
	v_mov_b32_e32 v44, v51
	v_pk_mul_f32 v[8:9], v[8:9], v[6:7] op_sel_hi:[1,0]
	v_pk_mul_f32 v[30:31], v[44:45], v[6:7] op_sel_hi:[1,0]
	s_waitcnt vmcnt(0)
	v_pk_mul_f32 v[0:1], v[0:1], v[8:9]
	v_pk_mul_f32 v[2:3], v[2:3], v[30:31]
	global_store_dwordx4 v[24:25], v[0:3], off offset:-2048 nt
	global_load_dwordx4 v[0:3], v[14:15], off offset:3072
	v_mov_b32_e32 v8, v52
	v_mov_b32_e32 v9, v54
	v_mov_b32_e32 v54, v53
	v_pk_mul_f32 v[8:9], v[8:9], v[6:7] op_sel_hi:[1,0]
	v_pk_mul_f32 v[30:31], v[54:55], v[6:7] op_sel_hi:[1,0]
	s_waitcnt vmcnt(0)
	v_pk_mul_f32 v[0:1], v[8:9], v[0:1]
	v_pk_mul_f32 v[2:3], v[30:31], v[2:3]
	global_store_dwordx4 v[24:25], v[0:3], off offset:-1024 nt
	global_load_dwordx4 v[0:3], v[16:17], off
	v_pk_mul_f32 v[8:9], v[42:43], v[6:7] op_sel_hi:[1,0]
	v_pk_mul_f32 v[30:31], v[40:41], v[6:7] op_sel_hi:[1,0]
	s_waitcnt vmcnt(0)
	v_pk_mul_f32 v[2:3], v[8:9], v[2:3]
	v_pk_mul_f32 v[0:1], v[30:31], v[0:1]
	global_store_dwordx4 v[24:25], v[0:3], off nt
	global_load_dwordx4 v[0:3], v[18:19], off
	v_pk_mul_f32 v[8:9], v[28:29], v[6:7] op_sel_hi:[1,0]
	s_waitcnt vmcnt(0)
	v_pk_mul_f32 v[2:3], v[4:5], v[2:3]
	v_pk_mul_f32 v[0:1], v[8:9], v[0:1]
	global_store_dwordx4 v[24:25], v[0:3], off offset:1024 nt
	global_load_dwordx4 v[0:3], v[20:21], off
	v_pk_mul_f32 v[4:5], v[34:35], v[6:7] op_sel_hi:[1,0]
	v_pk_mul_f32 v[8:9], v[36:37], v[6:7] op_sel_hi:[1,0]
	s_waitcnt vmcnt(0)
	v_pk_mul_f32 v[2:3], v[4:5], v[2:3]
	v_pk_mul_f32 v[0:1], v[8:9], v[0:1]
	global_store_dwordx4 v[24:25], v[0:3], off offset:2048 nt
	global_load_dwordx4 v[0:3], v[22:23], off
	v_pk_mul_f32 v[4:5], v[70:71], v[6:7] op_sel_hi:[1,0]
	v_pk_mul_f32 v[6:7], v[86:87], v[6:7] op_sel_hi:[1,0]
	s_waitcnt vmcnt(0)
	v_pk_mul_f32 v[0:1], v[4:5], v[0:1]
	v_pk_mul_f32 v[2:3], v[6:7], v[2:3]
	global_store_dwordx4 v[24:25], v[0:3], off offset:3072 nt
	v_lshl_add_u64 v[24:25], v[24:25], 0, s[0:1]
	s_cbranch_scc1 .LBB0_1639
